# non-temporal (nt) loads and stores in the expert / dense weight conversion loops so that the streamed f32 weights do not displace GEMM operands in the caches
# speedup vs baseline: 1.0131x; 1.0062x over previous
.LBB0_839:
	s_add_i32 s17, s8, s9
	s_cmpk_gt_i32 s17, 0xaff
	s_cselect_b64 s[6:7], -1, 0
	s_and_b64 s[2:3], s[6:7], exec
	s_cselect_b32 s2, s14, 0xc0
	s_cselect_b32 s18, 0xfffff500, 0
	s_add_u32 s2, s74, s2
	s_addc_u32 s3, s75, 0
	s_add_i32 s17, s17, s18
	s_load_dwordx2 s[4:5], s[2:3], 0x0
	s_mul_hi_i32 s2, s17, 0x2e8ba2e9
	s_lshr_b32 s3, s2, 31
	s_ashr_i32 s2, s2, 5
	s_add_i32 s2, s2, s3
	s_mul_i32 s3, s2, 0xb0
	s_sub_i32 s17, s17, s3
	s_lshl_b32 s18, s17, 5
	v_or_b32_e32 v2, s18, v70
	s_lshl_b32 s2, s2, 7
	v_ashrrev_i32_e32 v3, 31, v2
	v_cmp_gt_i32_e32 vcc, s15, v2
	v_or_b32_e32 v77, s2, v71
	s_waitcnt lgkmcnt(0)
	v_lshl_add_u64 v[68:69], v[2:3], 2, s[4:5]
	v_mov_b32_e32 v2, 0
	v_mov_b32_e32 v3, 0
	v_mov_b32_e32 v4, 0
	v_mov_b32_e32 v5, 0
	s_and_saveexec_b64 s[4:5], vcc
	s_cbranch_execz .LBB0_841
	v_mad_i64_i32 v[2:3], s[20:21], v77, s16, v[68:69]
	global_load_dwordx4 v[2:5], v[2:3], off nt
.LBB0_841:
	s_or_b64 exec, exec, s[4:5]
	v_mov_b32_e32 v6, 0
	v_mov_b32_e32 v10, 0
	v_mov_b32_e32 v11, 0
	v_mov_b32_e32 v12, 0
	v_mov_b32_e32 v13, 0
	s_and_saveexec_b64 s[4:5], vcc
	s_cbranch_execz .LBB0_843
	v_or_b32_e32 v7, 8, v77
	v_mad_i64_i32 v[8:9], s[20:21], v7, s16, v[68:69]
	global_load_dwordx4 v[10:13], v[8:9], off nt
.LBB0_843:
	s_or_b64 exec, exec, s[4:5]
	v_mov_b32_e32 v7, 0
	v_mov_b32_e32 v8, 0
	v_mov_b32_e32 v9, 0
	s_and_saveexec_b64 s[4:5], vcc
	s_cbranch_execz .LBB0_845
	v_or_b32_e32 v6, 16, v77
	v_mad_i64_i32 v[6:7], s[20:21], v6, s16, v[68:69]
	global_load_dwordx4 v[6:9], v[6:7], off nt
.LBB0_845:
	s_or_b64 exec, exec, s[4:5]
	v_mov_b32_e32 v14, 0
	v_mov_b32_e32 v18, 0
	v_mov_b32_e32 v19, 0
	v_mov_b32_e32 v20, 0
	v_mov_b32_e32 v21, 0
	s_and_saveexec_b64 s[4:5], vcc
	s_cbranch_execz .LBB0_847
	v_or_b32_e32 v15, 24, v77
	v_mad_i64_i32 v[16:17], s[20:21], v15, s16, v[68:69]
	global_load_dwordx4 v[18:21], v[16:17], off nt
.LBB0_847:
	s_or_b64 exec, exec, s[4:5]
	v_mov_b32_e32 v15, 0
	v_mov_b32_e32 v16, 0
	v_mov_b32_e32 v17, 0
	s_and_saveexec_b64 s[4:5], vcc
	s_cbranch_execz .LBB0_849
	v_or_b32_e32 v14, 32, v77
	v_mad_i64_i32 v[14:15], s[20:21], v14, s16, v[68:69]
	global_load_dwordx4 v[14:17], v[14:15], off nt
.LBB0_849:
	s_or_b64 exec, exec, s[4:5]
	v_mov_b32_e32 v22, 0
	v_mov_b32_e32 v26, 0
	v_mov_b32_e32 v27, 0
	v_mov_b32_e32 v28, 0
	v_mov_b32_e32 v29, 0
	s_and_saveexec_b64 s[4:5], vcc
	s_cbranch_execz .LBB0_851
	v_or_b32_e32 v23, 40, v77
	v_mad_i64_i32 v[24:25], s[20:21], v23, s16, v[68:69]
	global_load_dwordx4 v[26:29], v[24:25], off nt
.LBB0_851:
	s_or_b64 exec, exec, s[4:5]
	v_mov_b32_e32 v23, 0
	v_mov_b32_e32 v24, 0
	v_mov_b32_e32 v25, 0
	s_and_saveexec_b64 s[4:5], vcc
	s_cbranch_execz .LBB0_853
	v_or_b32_e32 v22, 48, v77
	v_mad_i64_i32 v[22:23], s[20:21], v22, s16, v[68:69]
	global_load_dwordx4 v[22:25], v[22:23], off nt
.LBB0_853:
	s_or_b64 exec, exec, s[4:5]
	v_mov_b32_e32 v30, 0
	v_mov_b32_e32 v34, 0
	v_mov_b32_e32 v35, 0
	v_mov_b32_e32 v36, 0
	v_mov_b32_e32 v37, 0
	s_and_saveexec_b64 s[4:5], vcc
	s_cbranch_execz .LBB0_855
	v_or_b32_e32 v31, 56, v77
	v_mad_i64_i32 v[32:33], s[20:21], v31, s16, v[68:69]
	global_load_dwordx4 v[34:37], v[32:33], off nt
.LBB0_855:
	s_or_b64 exec, exec, s[4:5]
	v_mov_b32_e32 v31, 0
	v_mov_b32_e32 v32, 0
	v_mov_b32_e32 v33, 0
	s_and_saveexec_b64 s[4:5], vcc
	s_cbranch_execz .LBB0_857
	v_or_b32_e32 v30, 64, v77
	v_mad_i64_i32 v[30:31], s[20:21], v30, s16, v[68:69]
	global_load_dwordx4 v[30:33], v[30:31], off nt
.LBB0_857:
	s_or_b64 exec, exec, s[4:5]
	v_mov_b32_e32 v38, 0
	v_mov_b32_e32 v42, 0
	v_mov_b32_e32 v43, 0
	v_mov_b32_e32 v44, 0
	v_mov_b32_e32 v45, 0
	s_and_saveexec_b64 s[4:5], vcc
	s_cbranch_execz .LBB0_859
	v_or_b32_e32 v39, 0x48, v77
	v_mad_i64_i32 v[40:41], s[20:21], v39, s16, v[68:69]
	global_load_dwordx4 v[42:45], v[40:41], off nt
.LBB0_859:
	s_or_b64 exec, exec, s[4:5]
	v_mov_b32_e32 v39, 0
	v_mov_b32_e32 v40, 0
	v_mov_b32_e32 v41, 0
	s_and_saveexec_b64 s[4:5], vcc
	s_cbranch_execz .LBB0_861
	v_or_b32_e32 v38, 0x50, v77
	v_mad_i64_i32 v[38:39], s[20:21], v38, s16, v[68:69]
	global_load_dwordx4 v[38:41], v[38:39], off nt
.LBB0_861:
	s_or_b64 exec, exec, s[4:5]
	v_mov_b32_e32 v46, 0
	v_mov_b32_e32 v50, 0
	v_mov_b32_e32 v51, 0
	v_mov_b32_e32 v52, 0
	v_mov_b32_e32 v53, 0
	s_and_saveexec_b64 s[4:5], vcc
	s_cbranch_execz .LBB0_863
	v_or_b32_e32 v47, 0x58, v77
	v_mad_i64_i32 v[48:49], s[20:21], v47, s16, v[68:69]
	global_load_dwordx4 v[50:53], v[48:49], off nt
.LBB0_863:
	s_or_b64 exec, exec, s[4:5]
	v_mov_b32_e32 v47, 0
	v_mov_b32_e32 v48, 0
	v_mov_b32_e32 v49, 0
	s_and_saveexec_b64 s[4:5], vcc
	s_cbranch_execz .LBB0_865
	v_or_b32_e32 v46, 0x60, v77
	v_mad_i64_i32 v[46:47], s[20:21], v46, s16, v[68:69]
	global_load_dwordx4 v[46:49], v[46:47], off nt
.LBB0_865:
	s_or_b64 exec, exec, s[4:5]
	v_mov_b32_e32 v54, 0
	v_mov_b32_e32 v58, 0
	v_mov_b32_e32 v59, 0
	v_mov_b32_e32 v60, 0
	v_mov_b32_e32 v61, 0
	s_and_saveexec_b64 s[4:5], vcc
	s_cbranch_execz .LBB0_867
	v_or_b32_e32 v55, 0x68, v77
	v_mad_i64_i32 v[56:57], s[20:21], v55, s16, v[68:69]
	global_load_dwordx4 v[58:61], v[56:57], off nt
.LBB0_867:
	s_or_b64 exec, exec, s[4:5]
	v_mov_b32_e32 v55, 0
	v_mov_b32_e32 v56, 0
	v_mov_b32_e32 v57, 0
	s_and_saveexec_b64 s[4:5], vcc
	s_cbranch_execz .LBB0_869
	v_or_b32_e32 v54, 0x70, v77
	v_mad_i64_i32 v[54:55], s[20:21], v54, s16, v[68:69]
	global_load_dwordx4 v[54:57], v[54:55], off nt
.LBB0_869:
	s_or_b64 exec, exec, s[4:5]
	v_mov_b32_e32 v62, 0
	v_mov_b32_e32 v63, 0
	v_mov_b32_e32 v64, 0
	v_mov_b32_e32 v65, 0
	s_and_saveexec_b64 s[4:5], vcc
	s_cbranch_execz .LBB0_871
	v_or_b32_e32 v62, 0x78, v77
	v_mad_i64_i32 v[62:63], s[20:21], v62, s16, v[68:69]
	global_load_dwordx4 v[62:65], v[62:63], off nt
.LBB0_871:
	s_or_b64 exec, exec, s[4:5]
	s_waitcnt vmcnt(0)
	ds_write2_b32 v76, v2, v3 offset1:1
	ds_write2_b32 v76, v4, v5 offset0:2 offset1:3
	v_add_u32_e32 v2, 0x420, v76
	ds_write2_b32 v2, v10, v11 offset1:1
	v_add_u32_e32 v2, 0x428, v76
	ds_write2_b32 v2, v12, v13 offset1:1
	v_add_u32_e32 v2, 0x840, v76
	ds_write2_b32 v2, v6, v7 offset1:1
	v_add_u32_e32 v2, 0x848, v76
	ds_write2_b32 v2, v8, v9 offset1:1
	v_add_u32_e32 v2, 0xc60, v76
	ds_write2_b32 v2, v18, v19 offset1:1
	v_add_u32_e32 v2, 0xc68, v76
	ds_write2_b32 v2, v20, v21 offset1:1
	v_add_u32_e32 v2, 0x1080, v76
	ds_write2_b32 v2, v14, v15 offset1:1
	v_add_u32_e32 v2, 0x1088, v76
	ds_write2_b32 v2, v16, v17 offset1:1
	v_add_u32_e32 v2, 0x14a0, v76
	ds_write2_b32 v2, v26, v27 offset1:1
	v_add_u32_e32 v2, 0x14a8, v76
	ds_write2_b32 v2, v28, v29 offset1:1
	v_add_u32_e32 v2, 0x18c0, v76
	ds_write2_b32 v2, v22, v23 offset1:1
	v_add_u32_e32 v2, 0x18c8, v76
	ds_write2_b32 v2, v24, v25 offset1:1
	v_add_u32_e32 v2, 0x1ce0, v76
	ds_write2_b32 v2, v34, v35 offset1:1
	v_add_u32_e32 v2, 0x1ce8, v76
	ds_write2_b32 v2, v36, v37 offset1:1
	v_add_u32_e32 v2, 0x2100, v76
	ds_write2_b32 v2, v30, v31 offset1:1
	v_add_u32_e32 v2, 0x2108, v76
	ds_write2_b32 v2, v32, v33 offset1:1
	v_add_u32_e32 v2, 0x2520, v76
	ds_write2_b32 v2, v42, v43 offset1:1
	v_add_u32_e32 v2, 0x2528, v76
	ds_write2_b32 v2, v44, v45 offset1:1
	v_add_u32_e32 v2, 0x2940, v76
	ds_write2_b32 v2, v38, v39 offset1:1
	v_add_u32_e32 v2, 0x2948, v76
	ds_write2_b32 v2, v40, v41 offset1:1
	v_add_u32_e32 v2, 0x2d60, v76
	ds_write2_b32 v2, v50, v51 offset1:1
	v_add_u32_e32 v2, 0x2d68, v76
	ds_write2_b32 v2, v52, v53 offset1:1
	v_add_u32_e32 v2, 0x3180, v76
	ds_write2_b32 v2, v46, v47 offset1:1
	v_add_u32_e32 v2, 0x3188, v76
	ds_write2_b32 v2, v48, v49 offset1:1
	v_add_u32_e32 v2, 0x35a0, v76
	ds_write2_b32 v2, v58, v59 offset1:1
	v_add_u32_e32 v2, 0x35a8, v76
	ds_write2_b32 v2, v60, v61 offset1:1
	v_add_u32_e32 v2, 0x39c0, v76
	ds_write2_b32 v2, v54, v55 offset1:1
	v_add_u32_e32 v2, 0x39c8, v76
	ds_write2_b32 v2, v56, v57 offset1:1
	v_add_u32_e32 v2, 0x3de0, v76
	ds_write2_b32 v2, v62, v63 offset1:1
	v_add_u32_e32 v2, 0x3de8, v76
	ds_write2_b32 v2, v64, v65 offset1:1
	s_waitcnt lgkmcnt(0)
	s_ashr_i32 s3, s2, 31
	v_or_b32_e32 v5, s18, v71
	v_lshl_add_u64 v[2:3], v[66:67], 0, s[2:3]
	v_cmp_gt_i32_e32 vcc, s15, v5
	v_add_u32_e32 v4, 0x400, v75
	s_and_saveexec_b64 s[2:3], vcc
	s_cbranch_execz .LBB0_873
	s_lshl_b32 s4, s17, 6
	s_and_b32 s4, s4, 0xffffff00
	v_and_b32_e32 v5, 0x67, v5
	v_or_b32_e32 v5, s4, v5
	v_or_b32_e32 v6, 0x80, v5
	v_cndmask_b32_e64 v6, v5, v6, s[6:7]
	v_ashrrev_i32_e32 v7, 31, v6
	v_lshl_add_u64 v[8:9], v[6:7], 2, s[0:1]
	global_load_dword v5, v[8:9], off
	v_lshlrev_b64 v[24:25], 11, v[6:7]
	ds_read2_b32 v[8:9], v75 offset1:33
	ds_read2_b32 v[10:11], v75 offset0:66 offset1:99
	ds_read2_b32 v[12:13], v75 offset0:132 offset1:165
	ds_read2_b32 v[14:15], v75 offset0:198 offset1:231
	ds_read2_b32 v[16:17], v4 offset0:8 offset1:41
	ds_read2_b32 v[18:19], v4 offset0:74 offset1:107
	ds_read2_b32 v[20:21], v4 offset0:140 offset1:173
	ds_read2_b32 v[22:23], v4 offset0:206 offset1:239
	s_waitcnt vmcnt(0)
	v_div_scale_f32 v26, s[4:5], v5, v5, 1.0
	v_rcp_f32_e32 v27, v26
	v_div_scale_f32 v6, vcc, 1.0, v5, 1.0
	v_fma_f32 v7, -v26, v27, 1.0
	v_fmac_f32_e32 v27, v7, v27
	v_mul_f32_e32 v7, v6, v27
	v_fma_f32 v28, -v26, v7, v6
	v_fmac_f32_e32 v7, v28, v27
	v_fma_f32 v6, -v26, v7, v6
	v_div_fmas_f32 v6, v6, v27, v7
	v_div_fixup_f32 v5, v6, v5, 1.0
	s_waitcnt lgkmcnt(7)
	v_fmaak_f32 v6, v8, v5, 0x43000000
	s_waitcnt lgkmcnt(6)
	v_fmaak_f32 v8, v5, v10, 0x43000000
	s_waitcnt lgkmcnt(5)
	v_fmaak_f32 v10, v5, v12, 0x43000000
	s_waitcnt lgkmcnt(4)
	v_fmaak_f32 v12, v5, v14, 0x43000000
	s_waitcnt lgkmcnt(3)
	v_fmaak_f32 v14, v5, v16, 0x43000000
	s_waitcnt lgkmcnt(2)
	v_fmaak_f32 v16, v5, v18, 0x43000000
	s_waitcnt lgkmcnt(1)
	v_fmaak_f32 v18, v5, v20, 0x43000000
	v_fmaak_f32 v7, v5, v9, 0x43000000
	v_fmaak_f32 v9, v5, v11, 0x43000000
	v_fmaak_f32 v11, v5, v13, 0x43000000
	v_fmaak_f32 v13, v5, v15, 0x43000000
	v_fmaak_f32 v15, v5, v17, 0x43000000
	v_fmaak_f32 v17, v5, v19, 0x43000000
	v_fmaak_f32 v19, v5, v21, 0x43000000
	v_rndne_f32_e32 v6, v6
	v_rndne_f32_e32 v10, v10
	v_rndne_f32_e32 v14, v14
	v_rndne_f32_e32 v18, v18
	s_waitcnt lgkmcnt(0)
	v_fmaak_f32 v20, v5, v22, 0x43000000
	v_rndne_f32_e32 v7, v7
	v_rndne_f32_e32 v11, v11
	v_rndne_f32_e32 v15, v15
	v_rndne_f32_e32 v19, v19
	v_cvt_pk_u8_f32 v6, v6, 0, 0
	v_cvt_pk_u8_f32 v10, v10, 0, 0
	v_cvt_pk_u8_f32 v14, v14, 0, 0
	v_cvt_pk_u8_f32 v18, v18, 0, 0
	v_fmaak_f32 v5, v5, v23, 0x43000000
	v_rndne_f32_e32 v8, v8
	v_rndne_f32_e32 v12, v12
	v_rndne_f32_e32 v16, v16
	v_rndne_f32_e32 v20, v20
	v_cvt_pk_u8_f32 v6, v7, 1, v6
	v_cvt_pk_u8_f32 v7, v11, 1, v10
	v_cvt_pk_u8_f32 v10, v15, 1, v14
	v_cvt_pk_u8_f32 v11, v19, 1, v18
	v_rndne_f32_e32 v9, v9
	v_rndne_f32_e32 v13, v13
	v_rndne_f32_e32 v17, v17
	v_rndne_f32_e32 v5, v5
	v_cvt_pk_u8_f32 v6, v8, 2, v6
	v_cvt_pk_u8_f32 v7, v12, 2, v7
	v_cvt_pk_u8_f32 v8, v16, 2, v10
	v_cvt_pk_u8_f32 v10, v20, 2, v11
	v_cvt_pk_u8_f32 v6, v9, 3, v6
	v_cvt_pk_u8_f32 v7, v13, 3, v7
	v_cvt_pk_u8_f32 v8, v17, 3, v8
	v_cvt_pk_u8_f32 v5, v5, 3, v10
	v_xor_b32_e32 v6, 0x80808080, v6
	v_xor_b32_e32 v7, 0x80808080, v7
	v_xor_b32_e32 v8, 0x80808080, v8
	v_xor_b32_e32 v9, 0x80808080, v5
	v_lshl_add_u64 v[10:11], v[2:3], 0, v[24:25]
	global_store_dwordx4 v[10:11], v[6:9], off nt
.LBB0_873:
	s_or_b64 exec, exec, s[2:3]
	v_or_b32_e32 v5, s18, v72
	v_cmp_gt_i32_e32 vcc, s15, v5
	s_and_saveexec_b64 s[2:3], vcc
	s_cbranch_execz .LBB0_875
	s_lshl_b32 s4, s17, 6
	s_and_b32 s4, s4, 0xffffff00
	v_and_b32_e32 v5, 0x6f, v5
	v_or_b32_e32 v5, s4, v5
	v_or_b32_e32 v6, 0x80, v5
	v_cndmask_b32_e64 v6, v5, v6, s[6:7]
	v_ashrrev_i32_e32 v7, 31, v6
	v_lshl_add_u64 v[8:9], v[6:7], 2, s[0:1]
	global_load_dword v5, v[8:9], off
	v_lshlrev_b64 v[24:25], 11, v[6:7]
	ds_read2_b32 v[8:9], v75 offset0:8 offset1:41
	ds_read2_b32 v[10:11], v75 offset0:74 offset1:107
	ds_read2_b32 v[12:13], v75 offset0:140 offset1:173
	ds_read2_b32 v[14:15], v75 offset0:206 offset1:239
	ds_read2_b32 v[16:17], v4 offset0:16 offset1:49
	ds_read2_b32 v[18:19], v4 offset0:82 offset1:115
	ds_read2_b32 v[20:21], v4 offset0:148 offset1:181
	ds_read2_b32 v[22:23], v4 offset0:214 offset1:247
	s_waitcnt vmcnt(0)
	v_div_scale_f32 v26, s[4:5], v5, v5, 1.0
	v_rcp_f32_e32 v27, v26
	v_div_scale_f32 v6, vcc, 1.0, v5, 1.0
	v_fma_f32 v7, -v26, v27, 1.0
	v_fmac_f32_e32 v27, v7, v27
	v_mul_f32_e32 v7, v6, v27
	v_fma_f32 v28, -v26, v7, v6
	v_fmac_f32_e32 v7, v28, v27
	v_fma_f32 v6, -v26, v7, v6
	v_div_fmas_f32 v6, v6, v27, v7
	v_div_fixup_f32 v5, v6, v5, 1.0
	s_waitcnt lgkmcnt(7)
	v_fmaak_f32 v6, v8, v5, 0x43000000
	s_waitcnt lgkmcnt(6)
	v_fmaak_f32 v8, v5, v10, 0x43000000
	s_waitcnt lgkmcnt(5)
	v_fmaak_f32 v10, v5, v12, 0x43000000
	s_waitcnt lgkmcnt(4)
	v_fmaak_f32 v12, v5, v14, 0x43000000
	s_waitcnt lgkmcnt(3)
	v_fmaak_f32 v14, v5, v16, 0x43000000
	s_waitcnt lgkmcnt(2)
	v_fmaak_f32 v16, v5, v18, 0x43000000
	s_waitcnt lgkmcnt(1)
	v_fmaak_f32 v18, v5, v20, 0x43000000
	v_fmaak_f32 v7, v5, v9, 0x43000000
	v_fmaak_f32 v9, v5, v11, 0x43000000
	v_fmaak_f32 v11, v5, v13, 0x43000000
	v_fmaak_f32 v13, v5, v15, 0x43000000
	v_fmaak_f32 v15, v5, v17, 0x43000000
	v_fmaak_f32 v17, v5, v19, 0x43000000
	v_fmaak_f32 v19, v5, v21, 0x43000000
	v_rndne_f32_e32 v6, v6
	v_rndne_f32_e32 v10, v10
	v_rndne_f32_e32 v14, v14
	v_rndne_f32_e32 v18, v18
	s_waitcnt lgkmcnt(0)
	v_fmaak_f32 v20, v5, v22, 0x43000000
	v_rndne_f32_e32 v7, v7
	v_rndne_f32_e32 v11, v11
	v_rndne_f32_e32 v15, v15
	v_rndne_f32_e32 v19, v19
	v_cvt_pk_u8_f32 v6, v6, 0, 0
	v_cvt_pk_u8_f32 v10, v10, 0, 0
	v_cvt_pk_u8_f32 v14, v14, 0, 0
	v_cvt_pk_u8_f32 v18, v18, 0, 0
	v_fmaak_f32 v5, v5, v23, 0x43000000
	v_rndne_f32_e32 v8, v8
	v_rndne_f32_e32 v12, v12
	v_rndne_f32_e32 v16, v16
	v_rndne_f32_e32 v20, v20
	v_cvt_pk_u8_f32 v6, v7, 1, v6
	v_cvt_pk_u8_f32 v7, v11, 1, v10
	v_cvt_pk_u8_f32 v10, v15, 1, v14
	v_cvt_pk_u8_f32 v11, v19, 1, v18
	v_rndne_f32_e32 v9, v9
	v_rndne_f32_e32 v13, v13
	v_rndne_f32_e32 v17, v17
	v_rndne_f32_e32 v5, v5
	v_cvt_pk_u8_f32 v6, v8, 2, v6
	v_cvt_pk_u8_f32 v7, v12, 2, v7
	v_cvt_pk_u8_f32 v8, v16, 2, v10
	v_cvt_pk_u8_f32 v10, v20, 2, v11
	v_cvt_pk_u8_f32 v6, v9, 3, v6
	v_cvt_pk_u8_f32 v7, v13, 3, v7
	v_cvt_pk_u8_f32 v8, v17, 3, v8
	v_cvt_pk_u8_f32 v5, v5, 3, v10
	v_xor_b32_e32 v6, 0x80808080, v6
	v_xor_b32_e32 v7, 0x80808080, v7
	v_xor_b32_e32 v8, 0x80808080, v8
	v_xor_b32_e32 v9, 0x80808080, v5
	v_lshl_add_u64 v[10:11], v[2:3], 0, v[24:25]
	global_store_dwordx4 v[10:11], v[6:9], off nt
.LBB0_875:
	s_or_b64 exec, exec, s[2:3]
	v_or_b32_e32 v5, s18, v73
	v_cmp_gt_i32_e32 vcc, s15, v5
	s_and_saveexec_b64 s[2:3], vcc
	s_cbranch_execz .LBB0_877
	s_lshl_b32 s4, s17, 6
	s_and_b32 s4, s4, 0xffffff00
	v_and_b32_e32 v5, 0x77, v5
	v_or_b32_e32 v5, s4, v5
	v_or_b32_e32 v6, 0x80, v5
	v_cndmask_b32_e64 v6, v5, v6, s[6:7]
	v_ashrrev_i32_e32 v7, 31, v6
	v_lshl_add_u64 v[8:9], v[6:7], 2, s[0:1]
	global_load_dword v5, v[8:9], off
	v_lshlrev_b64 v[24:25], 11, v[6:7]
	ds_read2_b32 v[8:9], v75 offset0:16 offset1:49
	ds_read2_b32 v[10:11], v75 offset0:82 offset1:115
	ds_read2_b32 v[12:13], v75 offset0:148 offset1:181
	ds_read2_b32 v[14:15], v75 offset0:214 offset1:247
	ds_read2_b32 v[16:17], v4 offset0:24 offset1:57
	ds_read2_b32 v[18:19], v4 offset0:90 offset1:123
	ds_read2_b32 v[20:21], v4 offset0:156 offset1:189
	ds_read2_b32 v[22:23], v4 offset0:222 offset1:255
	s_waitcnt vmcnt(0)
	v_div_scale_f32 v26, s[4:5], v5, v5, 1.0
	v_rcp_f32_e32 v27, v26
	v_div_scale_f32 v6, vcc, 1.0, v5, 1.0
	v_fma_f32 v7, -v26, v27, 1.0
	v_fmac_f32_e32 v27, v7, v27
	v_mul_f32_e32 v7, v6, v27
	v_fma_f32 v28, -v26, v7, v6
	v_fmac_f32_e32 v7, v28, v27
	v_fma_f32 v6, -v26, v7, v6
	v_div_fmas_f32 v6, v6, v27, v7
	v_div_fixup_f32 v5, v6, v5, 1.0
	s_waitcnt lgkmcnt(7)
	v_fmaak_f32 v6, v8, v5, 0x43000000
	s_waitcnt lgkmcnt(6)
	v_fmaak_f32 v8, v5, v10, 0x43000000
	s_waitcnt lgkmcnt(5)
	v_fmaak_f32 v10, v5, v12, 0x43000000
	s_waitcnt lgkmcnt(4)
	v_fmaak_f32 v12, v5, v14, 0x43000000
	s_waitcnt lgkmcnt(3)
	v_fmaak_f32 v14, v5, v16, 0x43000000
	s_waitcnt lgkmcnt(2)
	v_fmaak_f32 v16, v5, v18, 0x43000000
	s_waitcnt lgkmcnt(1)
	v_fmaak_f32 v18, v5, v20, 0x43000000
	v_fmaak_f32 v7, v5, v9, 0x43000000
	v_fmaak_f32 v9, v5, v11, 0x43000000
	v_fmaak_f32 v11, v5, v13, 0x43000000
	v_fmaak_f32 v13, v5, v15, 0x43000000
	v_fmaak_f32 v15, v5, v17, 0x43000000
	v_fmaak_f32 v17, v5, v19, 0x43000000
	v_fmaak_f32 v19, v5, v21, 0x43000000
	v_rndne_f32_e32 v6, v6
	v_rndne_f32_e32 v10, v10
	v_rndne_f32_e32 v14, v14
	v_rndne_f32_e32 v18, v18
	s_waitcnt lgkmcnt(0)
	v_fmaak_f32 v20, v5, v22, 0x43000000
	v_rndne_f32_e32 v7, v7
	v_rndne_f32_e32 v11, v11
	v_rndne_f32_e32 v15, v15
	v_rndne_f32_e32 v19, v19
	v_cvt_pk_u8_f32 v6, v6, 0, 0
	v_cvt_pk_u8_f32 v10, v10, 0, 0
	v_cvt_pk_u8_f32 v14, v14, 0, 0
	v_cvt_pk_u8_f32 v18, v18, 0, 0
	v_fmaak_f32 v5, v5, v23, 0x43000000
	v_rndne_f32_e32 v8, v8
	v_rndne_f32_e32 v12, v12
	v_rndne_f32_e32 v16, v16
	v_rndne_f32_e32 v20, v20
	v_cvt_pk_u8_f32 v6, v7, 1, v6
	v_cvt_pk_u8_f32 v7, v11, 1, v10
	v_cvt_pk_u8_f32 v10, v15, 1, v14
	v_cvt_pk_u8_f32 v11, v19, 1, v18
	v_rndne_f32_e32 v9, v9
	v_rndne_f32_e32 v13, v13
	v_rndne_f32_e32 v17, v17
	v_rndne_f32_e32 v5, v5
	v_cvt_pk_u8_f32 v6, v8, 2, v6
	v_cvt_pk_u8_f32 v7, v12, 2, v7
	v_cvt_pk_u8_f32 v8, v16, 2, v10
	v_cvt_pk_u8_f32 v10, v20, 2, v11
	v_cvt_pk_u8_f32 v6, v9, 3, v6
	v_cvt_pk_u8_f32 v7, v13, 3, v7
	v_cvt_pk_u8_f32 v8, v17, 3, v8
	v_cvt_pk_u8_f32 v5, v5, 3, v10
	v_xor_b32_e32 v6, 0x80808080, v6
	v_xor_b32_e32 v7, 0x80808080, v7
	v_xor_b32_e32 v8, 0x80808080, v8
	v_xor_b32_e32 v9, 0x80808080, v5
	v_lshl_add_u64 v[10:11], v[2:3], 0, v[24:25]
	global_store_dwordx4 v[10:11], v[6:9], off nt
.LBB0_877:
	s_or_b64 exec, exec, s[2:3]
	v_or_b32_e32 v5, s18, v74
	v_cmp_gt_i32_e32 vcc, s15, v5
	s_and_saveexec_b64 s[2:3], vcc
	s_cbranch_execz .LBB0_838
	s_lshl_b32 s4, s17, 6
	s_and_b32 s4, s4, 0xffffff00
	v_and_b32_e32 v5, 0x7f, v5
	v_or_b32_e32 v5, s4, v5
	v_or_b32_e32 v6, 0x80, v5
	v_cndmask_b32_e64 v6, v5, v6, s[6:7]
	v_ashrrev_i32_e32 v7, 31, v6
	v_lshl_add_u64 v[8:9], v[6:7], 2, s[0:1]
	global_load_dword v24, v[8:9], off
	v_lshlrev_b64 v[22:23], 11, v[6:7]
	ds_read2_b32 v[8:9], v75 offset0:24 offset1:57
	ds_read2_b32 v[10:11], v75 offset0:90 offset1:123
	ds_read2_b32 v[12:13], v75 offset0:156 offset1:189
	ds_read2_b32 v[14:15], v75 offset0:222 offset1:255
	ds_read2_b32 v[16:17], v4 offset0:32 offset1:65
	ds_read2_b32 v[18:19], v4 offset0:98 offset1:131
	ds_read2_b32 v[4:5], v4 offset0:164 offset1:197
	v_add_u32_e32 v20, 0x600, v75
	ds_read2_b32 v[20:21], v20 offset0:102 offset1:135
	v_lshl_add_u64 v[2:3], v[2:3], 0, v[22:23]
	s_waitcnt vmcnt(0)
	v_div_scale_f32 v25, s[4:5], v24, v24, 1.0
	v_rcp_f32_e32 v26, v25
	v_div_scale_f32 v6, vcc, 1.0, v24, 1.0
	v_fma_f32 v7, -v25, v26, 1.0
	v_fmac_f32_e32 v26, v7, v26
	v_mul_f32_e32 v7, v6, v26
	v_fma_f32 v27, -v25, v7, v6
	v_fmac_f32_e32 v7, v27, v26
	v_fma_f32 v6, -v25, v7, v6
	v_div_fmas_f32 v6, v6, v26, v7
	v_div_fixup_f32 v6, v6, v24, 1.0
	s_waitcnt lgkmcnt(7)
	v_fmaak_f32 v7, v8, v6, 0x43000000
	v_fmaak_f32 v8, v6, v9, 0x43000000
	s_waitcnt lgkmcnt(6)
	v_fmaak_f32 v9, v6, v10, 0x43000000
	v_fmaak_f32 v10, v6, v11, 0x43000000
	s_waitcnt lgkmcnt(5)
	v_fmaak_f32 v11, v6, v12, 0x43000000
	v_fmaak_f32 v12, v6, v13, 0x43000000
	s_waitcnt lgkmcnt(4)
	v_fmaak_f32 v13, v6, v14, 0x43000000
	v_fmaak_f32 v14, v6, v15, 0x43000000
	s_waitcnt lgkmcnt(3)
	v_fmaak_f32 v15, v6, v16, 0x43000000
	s_waitcnt lgkmcnt(1)
	v_fmaak_f32 v4, v6, v4, 0x43000000
	v_fmaak_f32 v16, v6, v17, 0x43000000
	v_fmaak_f32 v5, v6, v5, 0x43000000
	v_rndne_f32_e32 v7, v7
	v_rndne_f32_e32 v11, v11
	v_rndne_f32_e32 v15, v15
	v_rndne_f32_e32 v4, v4
	v_fmaak_f32 v17, v6, v18, 0x43000000
	v_fmaak_f32 v18, v6, v19, 0x43000000
	s_waitcnt lgkmcnt(0)
	v_fmaak_f32 v19, v6, v20, 0x43000000
	v_rndne_f32_e32 v8, v8
	v_rndne_f32_e32 v12, v12
	v_rndne_f32_e32 v16, v16
	v_rndne_f32_e32 v5, v5
	v_cvt_pk_u8_f32 v7, v7, 0, 0
	v_cvt_pk_u8_f32 v11, v11, 0, 0
	v_cvt_pk_u8_f32 v15, v15, 0, 0
	v_cvt_pk_u8_f32 v4, v4, 0, 0
	v_fmaak_f32 v6, v6, v21, 0x43000000
	v_rndne_f32_e32 v9, v9
	v_rndne_f32_e32 v13, v13
	v_rndne_f32_e32 v17, v17
	v_rndne_f32_e32 v19, v19
	v_cvt_pk_u8_f32 v7, v8, 1, v7
	v_cvt_pk_u8_f32 v8, v12, 1, v11
	v_cvt_pk_u8_f32 v11, v16, 1, v15
	v_cvt_pk_u8_f32 v4, v5, 1, v4
	v_rndne_f32_e32 v10, v10
	v_rndne_f32_e32 v14, v14
	v_rndne_f32_e32 v18, v18
	v_rndne_f32_e32 v6, v6
	v_cvt_pk_u8_f32 v5, v9, 2, v7
	v_cvt_pk_u8_f32 v7, v13, 2, v8
	v_cvt_pk_u8_f32 v8, v17, 2, v11
	v_cvt_pk_u8_f32 v4, v19, 2, v4
	v_cvt_pk_u8_f32 v5, v10, 3, v5
	v_cvt_pk_u8_f32 v7, v14, 3, v7
	v_cvt_pk_u8_f32 v8, v18, 3, v8
	v_cvt_pk_u8_f32 v9, v6, 3, v4
	v_xor_b32_e32 v4, 0x80808080, v5
	v_xor_b32_e32 v5, 0x80808080, v7
	v_xor_b32_e32 v6, 0x80808080, v8
	v_xor_b32_e32 v7, 0x80808080, v9
	global_store_dwordx4 v[2:3], v[4:7], off nt
	s_branch .LBB0_838

.LBB0_882:
	s_mul_hi_i32 s4, s22, 0x473c1ab7
	s_lshr_b32 s5, s4, 31
	s_ashr_i32 s4, s4, 5
	s_add_i32 s5, s4, s5
	s_mul_i32 s8, s5, 0xfffff1a0
	s_add_i32 s8, s8, s14
	v_add_u32_e32 v2, s8, v71
	s_lshl_b32 s4, s5, 7
	v_ashrrev_i32_e32 v3, 31, v2
	v_cmp_gt_i32_e32 vcc, s16, v2
	v_or_b32_e32 v76, s4, v70
	v_lshl_add_u64 v[68:69], v[2:3], 2, s[0:1]
	v_mov_b32_e32 v2, 0
	v_mov_b32_e32 v3, 0
	v_mov_b32_e32 v4, 0
	v_mov_b32_e32 v5, 0
	s_and_saveexec_b64 s[6:7], vcc
	s_cbranch_execz .LBB0_884
	v_mad_i64_i32 v[2:3], s[24:25], v76, s17, v[68:69]
	global_load_dwordx4 v[2:5], v[2:3], off nt
.LBB0_884:
	s_or_b64 exec, exec, s[6:7]
	v_mov_b32_e32 v6, 0
	v_mov_b32_e32 v10, 0
	v_mov_b32_e32 v11, 0
	v_mov_b32_e32 v12, 0
	v_mov_b32_e32 v13, 0
	s_and_saveexec_b64 s[6:7], vcc
	s_cbranch_execz .LBB0_886
	v_or_b32_e32 v7, 8, v76
	v_mad_i64_i32 v[8:9], s[24:25], v7, s17, v[68:69]
	global_load_dwordx4 v[10:13], v[8:9], off nt
.LBB0_886:
	s_or_b64 exec, exec, s[6:7]
	v_mov_b32_e32 v7, 0
	v_mov_b32_e32 v8, 0
	v_mov_b32_e32 v9, 0
	s_and_saveexec_b64 s[6:7], vcc
	s_cbranch_execz .LBB0_888
	v_or_b32_e32 v6, 16, v76
	v_mad_i64_i32 v[6:7], s[24:25], v6, s17, v[68:69]
	global_load_dwordx4 v[6:9], v[6:7], off nt
.LBB0_888:
	s_or_b64 exec, exec, s[6:7]
	v_mov_b32_e32 v14, 0
	v_mov_b32_e32 v18, 0
	v_mov_b32_e32 v19, 0
	v_mov_b32_e32 v20, 0
	v_mov_b32_e32 v21, 0
	s_and_saveexec_b64 s[6:7], vcc
	s_cbranch_execz .LBB0_890
	v_or_b32_e32 v15, 24, v76
	v_mad_i64_i32 v[16:17], s[24:25], v15, s17, v[68:69]
	global_load_dwordx4 v[18:21], v[16:17], off nt
.LBB0_890:
	s_or_b64 exec, exec, s[6:7]
	v_mov_b32_e32 v15, 0
	v_mov_b32_e32 v16, 0
	v_mov_b32_e32 v17, 0
	s_and_saveexec_b64 s[6:7], vcc
	s_cbranch_execz .LBB0_892
	v_or_b32_e32 v14, 32, v76
	v_mad_i64_i32 v[14:15], s[24:25], v14, s17, v[68:69]
	global_load_dwordx4 v[14:17], v[14:15], off nt
.LBB0_892:
	s_or_b64 exec, exec, s[6:7]
	v_mov_b32_e32 v22, 0
	v_mov_b32_e32 v26, 0
	v_mov_b32_e32 v27, 0
	v_mov_b32_e32 v28, 0
	v_mov_b32_e32 v29, 0
	s_and_saveexec_b64 s[6:7], vcc
	s_cbranch_execz .LBB0_894
	v_or_b32_e32 v23, 40, v76
	v_mad_i64_i32 v[24:25], s[24:25], v23, s17, v[68:69]
	global_load_dwordx4 v[26:29], v[24:25], off nt
.LBB0_894:
	s_or_b64 exec, exec, s[6:7]
	v_mov_b32_e32 v23, 0
	v_mov_b32_e32 v24, 0
	v_mov_b32_e32 v25, 0
	s_and_saveexec_b64 s[6:7], vcc
	s_cbranch_execz .LBB0_896
	v_or_b32_e32 v22, 48, v76
	v_mad_i64_i32 v[22:23], s[24:25], v22, s17, v[68:69]
	global_load_dwordx4 v[22:25], v[22:23], off nt
.LBB0_896:
	s_or_b64 exec, exec, s[6:7]
	v_mov_b32_e32 v30, 0
	v_mov_b32_e32 v34, 0
	v_mov_b32_e32 v35, 0
	v_mov_b32_e32 v36, 0
	v_mov_b32_e32 v37, 0
	s_and_saveexec_b64 s[6:7], vcc
	s_cbranch_execz .LBB0_898
	v_or_b32_e32 v31, 56, v76
	v_mad_i64_i32 v[32:33], s[24:25], v31, s17, v[68:69]
	global_load_dwordx4 v[34:37], v[32:33], off nt
.LBB0_898:
	s_or_b64 exec, exec, s[6:7]
	v_mov_b32_e32 v31, 0
	v_mov_b32_e32 v32, 0
	v_mov_b32_e32 v33, 0
	s_and_saveexec_b64 s[6:7], vcc
	s_cbranch_execz .LBB0_900
	v_or_b32_e32 v30, 64, v76
	v_mad_i64_i32 v[30:31], s[24:25], v30, s17, v[68:69]
	global_load_dwordx4 v[30:33], v[30:31], off nt
.LBB0_900:
	s_or_b64 exec, exec, s[6:7]
	v_mov_b32_e32 v38, 0
	v_mov_b32_e32 v42, 0
	v_mov_b32_e32 v43, 0
	v_mov_b32_e32 v44, 0
	v_mov_b32_e32 v45, 0
	s_and_saveexec_b64 s[6:7], vcc
	s_cbranch_execz .LBB0_902
	v_or_b32_e32 v39, 0x48, v76
	v_mad_i64_i32 v[40:41], s[24:25], v39, s17, v[68:69]
	global_load_dwordx4 v[42:45], v[40:41], off nt
.LBB0_902:
	s_or_b64 exec, exec, s[6:7]
	v_mov_b32_e32 v39, 0
	v_mov_b32_e32 v40, 0
	v_mov_b32_e32 v41, 0
	s_and_saveexec_b64 s[6:7], vcc
	s_cbranch_execz .LBB0_904
	v_or_b32_e32 v38, 0x50, v76
	v_mad_i64_i32 v[38:39], s[24:25], v38, s17, v[68:69]
	global_load_dwordx4 v[38:41], v[38:39], off nt
.LBB0_904:
	s_or_b64 exec, exec, s[6:7]
	v_mov_b32_e32 v46, 0
	v_mov_b32_e32 v50, 0
	v_mov_b32_e32 v51, 0
	v_mov_b32_e32 v52, 0
	v_mov_b32_e32 v53, 0
	s_and_saveexec_b64 s[6:7], vcc
	s_cbranch_execz .LBB0_906
	v_or_b32_e32 v47, 0x58, v76
	v_mad_i64_i32 v[48:49], s[24:25], v47, s17, v[68:69]
	global_load_dwordx4 v[50:53], v[48:49], off nt
.LBB0_906:
	s_or_b64 exec, exec, s[6:7]
	v_mov_b32_e32 v47, 0
	v_mov_b32_e32 v48, 0
	v_mov_b32_e32 v49, 0
	s_and_saveexec_b64 s[6:7], vcc
	s_cbranch_execz .LBB0_908
	v_or_b32_e32 v46, 0x60, v76
	v_mad_i64_i32 v[46:47], s[24:25], v46, s17, v[68:69]
	global_load_dwordx4 v[46:49], v[46:47], off nt
.LBB0_908:
	s_or_b64 exec, exec, s[6:7]
	v_mov_b32_e32 v54, 0
	v_mov_b32_e32 v58, 0
	v_mov_b32_e32 v59, 0
	v_mov_b32_e32 v60, 0
	v_mov_b32_e32 v61, 0
	s_and_saveexec_b64 s[6:7], vcc
	s_cbranch_execz .LBB0_910
	v_or_b32_e32 v55, 0x68, v76
	v_mad_i64_i32 v[56:57], s[24:25], v55, s17, v[68:69]
	global_load_dwordx4 v[58:61], v[56:57], off nt
.LBB0_910:
	s_or_b64 exec, exec, s[6:7]
	v_mov_b32_e32 v55, 0
	v_mov_b32_e32 v56, 0
	v_mov_b32_e32 v57, 0
	s_and_saveexec_b64 s[6:7], vcc
	s_cbranch_execz .LBB0_912
	v_or_b32_e32 v54, 0x70, v76
	v_mad_i64_i32 v[54:55], s[24:25], v54, s17, v[68:69]
	global_load_dwordx4 v[54:57], v[54:55], off nt
.LBB0_912:
	s_or_b64 exec, exec, s[6:7]
	v_mov_b32_e32 v62, 0
	v_mov_b32_e32 v63, 0
	v_mov_b32_e32 v64, 0
	v_mov_b32_e32 v65, 0
	s_and_saveexec_b64 s[6:7], vcc
	s_cbranch_execz .LBB0_914
	v_or_b32_e32 v62, 0x78, v76
	v_mad_i64_i32 v[62:63], s[24:25], v62, s17, v[68:69]
	global_load_dwordx4 v[62:65], v[62:63], off nt

.LBB0_920:
	s_or_b64 exec, exec, s[6:7]
	v_ashrrev_i32_e32 v5, 31, v4
	v_lshl_add_u64 v[8:9], v[4:5], 2, s[2:3]
	global_load_dword v7, v[8:9], off
	v_add_u32_e32 v22, 0x400, v74
	ds_read2_b32 v[8:9], v74 offset1:33
	ds_read2_b32 v[10:11], v74 offset0:66 offset1:99
	ds_read2_b32 v[12:13], v74 offset0:132 offset1:165
	ds_read2_b32 v[14:15], v74 offset0:198 offset1:231
	ds_read2_b32 v[16:17], v22 offset0:8 offset1:41
	ds_read2_b32 v[18:19], v22 offset0:74 offset1:107
	ds_read2_b32 v[20:21], v22 offset0:140 offset1:173
	ds_read2_b32 v[22:23], v22 offset0:206 offset1:239
	v_lshlrev_b64 v[4:5], 11, v[4:5]
	v_lshl_add_u64 v[4:5], v[2:3], 0, v[4:5]
	s_waitcnt vmcnt(0)
	v_div_scale_f32 v24, s[6:7], v7, v7, 1.0
	v_rcp_f32_e32 v25, v24
	v_div_scale_f32 v26, vcc, 1.0, v7, 1.0
	v_fma_f32 v27, -v24, v25, 1.0
	v_fmac_f32_e32 v25, v27, v25
	v_mul_f32_e32 v27, v26, v25
	v_fma_f32 v28, -v24, v27, v26
	v_fmac_f32_e32 v27, v28, v25
	v_fma_f32 v24, -v24, v27, v26
	v_div_fmas_f32 v24, v24, v25, v27
	v_div_fixup_f32 v7, v24, v7, 1.0
	s_waitcnt lgkmcnt(7)
	v_fmaak_f32 v8, v8, v7, 0x43000000
	s_waitcnt lgkmcnt(5)
	v_fmaak_f32 v12, v7, v12, 0x43000000
	s_waitcnt lgkmcnt(3)
	v_fmaak_f32 v16, v7, v16, 0x43000000
	s_waitcnt lgkmcnt(1)
	v_fmaak_f32 v20, v7, v20, 0x43000000
	v_fmaak_f32 v9, v7, v9, 0x43000000
	v_fmaak_f32 v13, v7, v13, 0x43000000
	v_fmaak_f32 v17, v7, v17, 0x43000000
	v_fmaak_f32 v21, v7, v21, 0x43000000
	v_rndne_f32_e32 v8, v8
	v_rndne_f32_e32 v12, v12
	v_rndne_f32_e32 v16, v16
	v_rndne_f32_e32 v20, v20
	v_fmaak_f32 v10, v7, v10, 0x43000000
	v_fmaak_f32 v14, v7, v14, 0x43000000
	v_fmaak_f32 v18, v7, v18, 0x43000000
	s_waitcnt lgkmcnt(0)
	v_fmaak_f32 v22, v7, v22, 0x43000000
	v_rndne_f32_e32 v9, v9
	v_rndne_f32_e32 v13, v13
	v_rndne_f32_e32 v17, v17
	v_rndne_f32_e32 v21, v21
	v_cvt_pk_u8_f32 v8, v8, 0, 0
	v_cvt_pk_u8_f32 v12, v12, 0, 0
	v_cvt_pk_u8_f32 v16, v16, 0, 0
	v_cvt_pk_u8_f32 v20, v20, 0, 0
	v_fmaak_f32 v11, v7, v11, 0x43000000
	v_fmaak_f32 v15, v7, v15, 0x43000000
	v_fmaak_f32 v19, v7, v19, 0x43000000
	v_fmaak_f32 v7, v7, v23, 0x43000000
	v_rndne_f32_e32 v10, v10
	v_rndne_f32_e32 v14, v14
	v_rndne_f32_e32 v18, v18
	v_rndne_f32_e32 v22, v22
	v_cvt_pk_u8_f32 v8, v9, 1, v8
	v_cvt_pk_u8_f32 v9, v13, 1, v12
	v_cvt_pk_u8_f32 v12, v17, 1, v16
	v_cvt_pk_u8_f32 v13, v21, 1, v20
	v_rndne_f32_e32 v11, v11
	v_rndne_f32_e32 v15, v15
	v_rndne_f32_e32 v19, v19
	v_rndne_f32_e32 v7, v7
	v_cvt_pk_u8_f32 v8, v10, 2, v8
	v_cvt_pk_u8_f32 v9, v14, 2, v9
	v_cvt_pk_u8_f32 v10, v18, 2, v12
	v_cvt_pk_u8_f32 v12, v22, 2, v13
	v_cvt_pk_u8_f32 v8, v11, 3, v8
	v_cvt_pk_u8_f32 v9, v15, 3, v9
	v_cvt_pk_u8_f32 v10, v19, 3, v10
	v_cvt_pk_u8_f32 v7, v7, 3, v12
	v_xor_b32_e32 v8, 0x80808080, v8
	v_xor_b32_e32 v9, 0x80808080, v9
	v_xor_b32_e32 v10, 0x80808080, v10
	v_xor_b32_e32 v11, 0x80808080, v7
	global_store_dwordx4 v[4:5], v[8:11], off nt

.LBB0_928:
	s_or_b64 exec, exec, s[6:7]
	v_ashrrev_i32_e32 v5, 31, v4
	v_lshl_add_u64 v[8:9], v[4:5], 2, s[2:3]
	global_load_dword v7, v[8:9], off
	v_add_u32_e32 v22, 0x400, v74
	ds_read2_b32 v[8:9], v74 offset0:8 offset1:41
	ds_read2_b32 v[10:11], v74 offset0:74 offset1:107
	ds_read2_b32 v[12:13], v74 offset0:140 offset1:173
	ds_read2_b32 v[14:15], v74 offset0:206 offset1:239
	ds_read2_b32 v[16:17], v22 offset0:16 offset1:49
	ds_read2_b32 v[18:19], v22 offset0:82 offset1:115
	ds_read2_b32 v[20:21], v22 offset0:148 offset1:181
	ds_read2_b32 v[22:23], v22 offset0:214 offset1:247
	v_lshlrev_b64 v[4:5], 11, v[4:5]
	v_lshl_add_u64 v[4:5], v[2:3], 0, v[4:5]
	s_waitcnt vmcnt(0)
	v_div_scale_f32 v24, s[6:7], v7, v7, 1.0
	v_rcp_f32_e32 v25, v24
	v_div_scale_f32 v26, vcc, 1.0, v7, 1.0
	v_fma_f32 v27, -v24, v25, 1.0
	v_fmac_f32_e32 v25, v27, v25
	v_mul_f32_e32 v27, v26, v25
	v_fma_f32 v28, -v24, v27, v26
	v_fmac_f32_e32 v27, v28, v25
	v_fma_f32 v24, -v24, v27, v26
	v_div_fmas_f32 v24, v24, v25, v27
	v_div_fixup_f32 v7, v24, v7, 1.0
	s_waitcnt lgkmcnt(7)
	v_fmaak_f32 v8, v8, v7, 0x43000000
	s_waitcnt lgkmcnt(5)
	v_fmaak_f32 v12, v7, v12, 0x43000000
	s_waitcnt lgkmcnt(3)
	v_fmaak_f32 v16, v7, v16, 0x43000000
	s_waitcnt lgkmcnt(1)
	v_fmaak_f32 v20, v7, v20, 0x43000000
	v_fmaak_f32 v9, v7, v9, 0x43000000
	v_fmaak_f32 v13, v7, v13, 0x43000000
	v_fmaak_f32 v17, v7, v17, 0x43000000
	v_fmaak_f32 v21, v7, v21, 0x43000000
	v_rndne_f32_e32 v8, v8
	v_rndne_f32_e32 v12, v12
	v_rndne_f32_e32 v16, v16
	v_rndne_f32_e32 v20, v20
	v_fmaak_f32 v10, v7, v10, 0x43000000
	v_fmaak_f32 v14, v7, v14, 0x43000000
	v_fmaak_f32 v18, v7, v18, 0x43000000
	s_waitcnt lgkmcnt(0)
	v_fmaak_f32 v22, v7, v22, 0x43000000
	v_rndne_f32_e32 v9, v9
	v_rndne_f32_e32 v13, v13
	v_rndne_f32_e32 v17, v17
	v_rndne_f32_e32 v21, v21
	v_cvt_pk_u8_f32 v8, v8, 0, 0
	v_cvt_pk_u8_f32 v12, v12, 0, 0
	v_cvt_pk_u8_f32 v16, v16, 0, 0
	v_cvt_pk_u8_f32 v20, v20, 0, 0
	v_fmaak_f32 v11, v7, v11, 0x43000000
	v_fmaak_f32 v15, v7, v15, 0x43000000
	v_fmaak_f32 v19, v7, v19, 0x43000000
	v_fmaak_f32 v7, v7, v23, 0x43000000
	v_rndne_f32_e32 v10, v10
	v_rndne_f32_e32 v14, v14
	v_rndne_f32_e32 v18, v18
	v_rndne_f32_e32 v22, v22
	v_cvt_pk_u8_f32 v8, v9, 1, v8
	v_cvt_pk_u8_f32 v9, v13, 1, v12
	v_cvt_pk_u8_f32 v12, v17, 1, v16
	v_cvt_pk_u8_f32 v13, v21, 1, v20
	v_rndne_f32_e32 v11, v11
	v_rndne_f32_e32 v15, v15
	v_rndne_f32_e32 v19, v19
	v_rndne_f32_e32 v7, v7
	v_cvt_pk_u8_f32 v8, v10, 2, v8
	v_cvt_pk_u8_f32 v9, v14, 2, v9
	v_cvt_pk_u8_f32 v10, v18, 2, v12
	v_cvt_pk_u8_f32 v12, v22, 2, v13
	v_cvt_pk_u8_f32 v8, v11, 3, v8
	v_cvt_pk_u8_f32 v9, v15, 3, v9
	v_cvt_pk_u8_f32 v10, v19, 3, v10
	v_cvt_pk_u8_f32 v7, v7, 3, v12
	v_xor_b32_e32 v8, 0x80808080, v8
	v_xor_b32_e32 v9, 0x80808080, v9
	v_xor_b32_e32 v10, 0x80808080, v10
	v_xor_b32_e32 v11, 0x80808080, v7
	global_store_dwordx4 v[4:5], v[8:11], off nt

.LBB0_936:
	s_or_b64 exec, exec, s[6:7]
	v_ashrrev_i32_e32 v5, 31, v4
	v_lshl_add_u64 v[8:9], v[4:5], 2, s[2:3]
	global_load_dword v7, v[8:9], off
	v_add_u32_e32 v22, 0x400, v74
	ds_read2_b32 v[8:9], v74 offset0:16 offset1:49
	ds_read2_b32 v[10:11], v74 offset0:82 offset1:115
	ds_read2_b32 v[12:13], v74 offset0:148 offset1:181
	ds_read2_b32 v[14:15], v74 offset0:214 offset1:247
	ds_read2_b32 v[16:17], v22 offset0:24 offset1:57
	ds_read2_b32 v[18:19], v22 offset0:90 offset1:123
	ds_read2_b32 v[20:21], v22 offset0:156 offset1:189
	ds_read2_b32 v[22:23], v22 offset0:222 offset1:255
	v_lshlrev_b64 v[4:5], 11, v[4:5]
	v_lshl_add_u64 v[4:5], v[2:3], 0, v[4:5]
	s_waitcnt vmcnt(0)
	v_div_scale_f32 v24, s[6:7], v7, v7, 1.0
	v_rcp_f32_e32 v25, v24
	v_div_scale_f32 v26, vcc, 1.0, v7, 1.0
	v_fma_f32 v27, -v24, v25, 1.0
	v_fmac_f32_e32 v25, v27, v25
	v_mul_f32_e32 v27, v26, v25
	v_fma_f32 v28, -v24, v27, v26
	v_fmac_f32_e32 v27, v28, v25
	v_fma_f32 v24, -v24, v27, v26
	v_div_fmas_f32 v24, v24, v25, v27
	v_div_fixup_f32 v7, v24, v7, 1.0
	s_waitcnt lgkmcnt(7)
	v_fmaak_f32 v8, v8, v7, 0x43000000
	s_waitcnt lgkmcnt(5)
	v_fmaak_f32 v12, v7, v12, 0x43000000
	s_waitcnt lgkmcnt(3)
	v_fmaak_f32 v16, v7, v16, 0x43000000
	s_waitcnt lgkmcnt(1)
	v_fmaak_f32 v20, v7, v20, 0x43000000
	v_fmaak_f32 v9, v7, v9, 0x43000000
	v_fmaak_f32 v13, v7, v13, 0x43000000
	v_fmaak_f32 v17, v7, v17, 0x43000000
	v_fmaak_f32 v21, v7, v21, 0x43000000
	v_rndne_f32_e32 v8, v8
	v_rndne_f32_e32 v12, v12
	v_rndne_f32_e32 v16, v16
	v_rndne_f32_e32 v20, v20
	v_fmaak_f32 v10, v7, v10, 0x43000000
	v_fmaak_f32 v14, v7, v14, 0x43000000
	v_fmaak_f32 v18, v7, v18, 0x43000000
	s_waitcnt lgkmcnt(0)
	v_fmaak_f32 v22, v7, v22, 0x43000000
	v_rndne_f32_e32 v9, v9
	v_rndne_f32_e32 v13, v13
	v_rndne_f32_e32 v17, v17
	v_rndne_f32_e32 v21, v21
	v_cvt_pk_u8_f32 v8, v8, 0, 0
	v_cvt_pk_u8_f32 v12, v12, 0, 0
	v_cvt_pk_u8_f32 v16, v16, 0, 0
	v_cvt_pk_u8_f32 v20, v20, 0, 0
	v_fmaak_f32 v11, v7, v11, 0x43000000
	v_fmaak_f32 v15, v7, v15, 0x43000000
	v_fmaak_f32 v19, v7, v19, 0x43000000
	v_fmaak_f32 v7, v7, v23, 0x43000000
	v_rndne_f32_e32 v10, v10
	v_rndne_f32_e32 v14, v14
	v_rndne_f32_e32 v18, v18
	v_rndne_f32_e32 v22, v22
	v_cvt_pk_u8_f32 v8, v9, 1, v8
	v_cvt_pk_u8_f32 v9, v13, 1, v12
	v_cvt_pk_u8_f32 v12, v17, 1, v16
	v_cvt_pk_u8_f32 v13, v21, 1, v20
	v_rndne_f32_e32 v11, v11
	v_rndne_f32_e32 v15, v15
	v_rndne_f32_e32 v19, v19
	v_rndne_f32_e32 v7, v7
	v_cvt_pk_u8_f32 v8, v10, 2, v8
	v_cvt_pk_u8_f32 v9, v14, 2, v9
	v_cvt_pk_u8_f32 v10, v18, 2, v12
	v_cvt_pk_u8_f32 v12, v22, 2, v13
	v_cvt_pk_u8_f32 v8, v11, 3, v8
	v_cvt_pk_u8_f32 v9, v15, 3, v9
	v_cvt_pk_u8_f32 v10, v19, 3, v10
	v_cvt_pk_u8_f32 v7, v7, 3, v12
	v_xor_b32_e32 v8, 0x80808080, v8
	v_xor_b32_e32 v9, 0x80808080, v9
	v_xor_b32_e32 v10, 0x80808080, v10
	v_xor_b32_e32 v11, 0x80808080, v7
	global_store_dwordx4 v[4:5], v[8:11], off nt
.LBB0_937:
	s_or_b64 exec, exec, s[4:5]
	v_add_u32_e32 v4, 24, v6
	v_cmp_gt_i32_e32 vcc, s16, v4
	s_and_saveexec_b64 s[4:5], vcc
	s_cbranch_execz .LBB0_881
	v_add_u32_e32 v5, 0x658, v6
	v_cmp_gt_u32_e32 vcc, s21, v4
	v_add_u32_e32 v18, 0x400, v74
	v_add_u32_e32 v20, 0x600, v74
	v_cndmask_b32_e32 v5, v6, v5, vcc
	v_cmp_gt_i32_e32 vcc, s20, v4
	s_nop 1
	v_cndmask_b32_e32 v4, v5, v4, vcc
	v_ashrrev_i32_e32 v5, 31, v4
	v_lshl_add_u64 v[6:7], v[4:5], 2, s[2:3]
	global_load_dword v24, v[6:7], off
	v_lshlrev_b64 v[22:23], 11, v[4:5]
	ds_read2_b32 v[6:7], v74 offset0:24 offset1:57
	ds_read2_b32 v[8:9], v74 offset0:90 offset1:123
	ds_read2_b32 v[10:11], v74 offset0:156 offset1:189
	ds_read2_b32 v[12:13], v74 offset0:222 offset1:255
	ds_read2_b32 v[14:15], v18 offset0:32 offset1:65
	ds_read2_b32 v[16:17], v18 offset0:98 offset1:131
	ds_read2_b32 v[18:19], v18 offset0:164 offset1:197
	ds_read2_b32 v[20:21], v20 offset0:102 offset1:135
	v_lshl_add_u64 v[2:3], v[2:3], 0, v[22:23]
	s_waitcnt vmcnt(0)
	v_div_scale_f32 v25, s[6:7], v24, v24, 1.0
	v_rcp_f32_e32 v26, v25
	v_div_scale_f32 v4, vcc, 1.0, v24, 1.0
	v_fma_f32 v5, -v25, v26, 1.0
	v_fmac_f32_e32 v26, v5, v26
	v_mul_f32_e32 v5, v4, v26
	v_fma_f32 v27, -v25, v5, v4
	v_fmac_f32_e32 v5, v27, v26
	v_fma_f32 v4, -v25, v5, v4
	v_div_fmas_f32 v4, v4, v26, v5
	v_div_fixup_f32 v4, v4, v24, 1.0
	s_waitcnt lgkmcnt(7)
	v_fmaak_f32 v5, v6, v4, 0x43000000
	v_fmaak_f32 v6, v4, v7, 0x43000000
	s_waitcnt lgkmcnt(6)
	v_fmaak_f32 v7, v4, v8, 0x43000000
	v_fmaak_f32 v8, v4, v9, 0x43000000
	s_waitcnt lgkmcnt(5)
	v_fmaak_f32 v9, v4, v10, 0x43000000
	v_fmaak_f32 v10, v4, v11, 0x43000000
	s_waitcnt lgkmcnt(4)
	v_fmaak_f32 v11, v4, v12, 0x43000000
	v_fmaak_f32 v12, v4, v13, 0x43000000
	s_waitcnt lgkmcnt(3)
	v_fmaak_f32 v13, v4, v14, 0x43000000
	v_fmaak_f32 v14, v4, v15, 0x43000000
	s_waitcnt lgkmcnt(2)
	v_fmaak_f32 v15, v4, v16, 0x43000000
	v_fmaak_f32 v16, v4, v17, 0x43000000
	s_waitcnt lgkmcnt(1)
	v_fmaak_f32 v17, v4, v18, 0x43000000
	v_fmaak_f32 v18, v4, v19, 0x43000000
	v_rndne_f32_e32 v5, v5
	v_rndne_f32_e32 v9, v9
	v_rndne_f32_e32 v13, v13
	v_rndne_f32_e32 v17, v17
	s_waitcnt lgkmcnt(0)
	v_fmaak_f32 v19, v4, v20, 0x43000000
	v_rndne_f32_e32 v6, v6
	v_rndne_f32_e32 v10, v10
	v_rndne_f32_e32 v14, v14
	v_rndne_f32_e32 v18, v18
	v_cvt_pk_u8_f32 v5, v5, 0, 0
	v_cvt_pk_u8_f32 v9, v9, 0, 0
	v_cvt_pk_u8_f32 v13, v13, 0, 0
	v_cvt_pk_u8_f32 v17, v17, 0, 0
	v_fmaak_f32 v4, v4, v21, 0x43000000
	v_rndne_f32_e32 v7, v7
	v_rndne_f32_e32 v11, v11
	v_rndne_f32_e32 v15, v15
	v_rndne_f32_e32 v19, v19
	v_cvt_pk_u8_f32 v5, v6, 1, v5
	v_cvt_pk_u8_f32 v6, v10, 1, v9
	v_cvt_pk_u8_f32 v9, v14, 1, v13
	v_cvt_pk_u8_f32 v10, v18, 1, v17
	v_rndne_f32_e32 v8, v8
	v_rndne_f32_e32 v12, v12
	v_rndne_f32_e32 v16, v16
	v_rndne_f32_e32 v4, v4
	v_cvt_pk_u8_f32 v5, v7, 2, v5
	v_cvt_pk_u8_f32 v6, v11, 2, v6
	v_cvt_pk_u8_f32 v7, v15, 2, v9
	v_cvt_pk_u8_f32 v9, v19, 2, v10
	v_cvt_pk_u8_f32 v5, v8, 3, v5
	v_cvt_pk_u8_f32 v6, v12, 3, v6
	v_cvt_pk_u8_f32 v7, v16, 3, v7
	v_cvt_pk_u8_f32 v8, v4, 3, v9
	v_xor_b32_e32 v4, 0x80808080, v5
	v_xor_b32_e32 v5, 0x80808080, v6
	v_xor_b32_e32 v6, 0x80808080, v7
	v_xor_b32_e32 v7, 0x80808080, v8
	global_store_dwordx4 v[2:3], v[4:7], off nt
	s_branch .LBB0_881

.LBB0_943:
	s_add_i32 s9, s17, s18
	s_mul_hi_i32 s4, s9, 0x3e0f83e1
	s_lshr_b32 s5, s4, 31
	s_ashr_i32 s4, s4, 11
	s_add_i32 s8, s4, s5
	s_mul_i32 s4, s8, 0xffffdf00
	s_add_i32 s26, s9, s4
	s_mul_hi_i32 s5, s8, 0xb00000
	s_mul_i32 s4, s8, 0xb00000
	s_cmpk_gt_i32 s26, 0x15ff
	s_mov_b64 s[6:7], -1
	s_cbranch_scc0 .LBB0_945
	s_add_u32 s7, s3, s4
	s_addc_u32 s27, s13, s5
	s_mul_i32 s28, s8, 0x2c00000
	s_mul_hi_i32 s6, s8, 0x2c00000
	s_waitcnt lgkmcnt(0)
	s_add_u32 s30, s0, s28
	s_addc_u32 s31, s1, s6
	s_mul_i32 s6, s8, 0xffffbe00
	s_add_i32 s6, s11, s6
	s_and_b32 s28, s6, 0xffffff80
	s_addk_i32 s28, 0xd400
	s_and_b32 s6, s19, 0x7e0
	v_or_b32_e32 v62, s28, v73
	v_or_b32_e32 v2, s6, v72
	v_or_b32_e32 v4, 8, v62
	v_lshlrev_b32_e32 v68, 2, v2
	v_ashrrev_i32_e32 v63, 31, v62
	v_ashrrev_i32_e32 v5, 31, v4
	v_lshl_add_u64 v[64:65], s[30:31], 0, v[68:69]
	v_lshlrev_b64 v[2:3], 13, v[62:63]
	v_lshlrev_b64 v[4:5], 13, v[4:5]
	v_lshl_add_u64 v[2:3], v[64:65], 0, v[2:3]
	v_lshl_add_u64 v[6:7], v[64:65], 0, v[4:5]
	global_load_dwordx4 v[2:5], v[2:3], off nt
	s_nop 0
	global_load_dwordx4 v[6:9], v[6:7], off nt
	v_or_b32_e32 v10, 16, v62
	v_or_b32_e32 v12, 24, v62
	v_ashrrev_i32_e32 v11, 31, v10
	v_ashrrev_i32_e32 v13, 31, v12
	v_lshlrev_b64 v[10:11], 13, v[10:11]
	v_lshlrev_b64 v[12:13], 13, v[12:13]
	v_lshl_add_u64 v[10:11], v[64:65], 0, v[10:11]
	v_lshl_add_u64 v[14:15], v[64:65], 0, v[12:13]
	global_load_dwordx4 v[10:13], v[10:11], off nt
	s_nop 0
	global_load_dwordx4 v[14:17], v[14:15], off nt
	v_or_b32_e32 v18, 32, v62
	v_or_b32_e32 v20, 40, v62
	v_ashrrev_i32_e32 v19, 31, v18
	v_ashrrev_i32_e32 v21, 31, v20
	v_lshlrev_b64 v[18:19], 13, v[18:19]
	v_lshlrev_b64 v[20:21], 13, v[20:21]
	v_lshl_add_u64 v[18:19], v[64:65], 0, v[18:19]
	v_lshl_add_u64 v[22:23], v[64:65], 0, v[20:21]
	global_load_dwordx4 v[18:21], v[18:19], off nt
	s_nop 0
	global_load_dwordx4 v[22:25], v[22:23], off nt
	v_or_b32_e32 v26, 48, v62
	v_or_b32_e32 v28, 56, v62
	v_ashrrev_i32_e32 v27, 31, v26
	v_ashrrev_i32_e32 v29, 31, v28
	v_lshlrev_b64 v[26:27], 13, v[26:27]
	v_lshlrev_b64 v[28:29], 13, v[28:29]
	v_lshl_add_u64 v[26:27], v[64:65], 0, v[26:27]
	v_lshl_add_u64 v[30:31], v[64:65], 0, v[28:29]
	global_load_dwordx4 v[26:29], v[26:27], off nt
	s_nop 0
	global_load_dwordx4 v[30:33], v[30:31], off nt
	v_or_b32_e32 v34, 64, v62
	v_or_b32_e32 v36, 0x48, v62
	v_ashrrev_i32_e32 v35, 31, v34
	v_ashrrev_i32_e32 v37, 31, v36
	v_lshlrev_b64 v[34:35], 13, v[34:35]
	v_lshlrev_b64 v[36:37], 13, v[36:37]
	v_lshl_add_u64 v[34:35], v[64:65], 0, v[34:35]
	v_lshl_add_u64 v[38:39], v[64:65], 0, v[36:37]
	global_load_dwordx4 v[34:37], v[34:35], off nt
	s_nop 0
	global_load_dwordx4 v[38:41], v[38:39], off nt
	v_or_b32_e32 v42, 0x50, v62
	v_or_b32_e32 v44, 0x58, v62
	v_ashrrev_i32_e32 v43, 31, v42
	v_ashrrev_i32_e32 v45, 31, v44
	v_lshlrev_b64 v[42:43], 13, v[42:43]
	v_lshlrev_b64 v[44:45], 13, v[44:45]
	v_lshl_add_u64 v[42:43], v[64:65], 0, v[42:43]
	v_lshl_add_u64 v[46:47], v[64:65], 0, v[44:45]
	v_or_b32_e32 v50, 0x60, v62
	global_load_dwordx4 v[42:45], v[42:43], off nt
	s_nop 0
	global_load_dwordx4 v[46:49], v[46:47], off nt
	v_ashrrev_i32_e32 v51, 31, v50
	v_lshlrev_b64 v[50:51], 13, v[50:51]
	v_or_b32_e32 v54, 0x68, v62
	v_lshl_add_u64 v[50:51], v[64:65], 0, v[50:51]
	v_ashrrev_i32_e32 v55, 31, v54
	global_load_dwordx4 v[50:53], v[50:51], off nt
	v_lshlrev_b64 v[54:55], 13, v[54:55]
	v_or_b32_e32 v58, 0x70, v62
	v_lshl_add_u64 v[54:55], v[64:65], 0, v[54:55]
	v_ashrrev_i32_e32 v59, 31, v58
	global_load_dwordx4 v[54:57], v[54:55], off nt
	v_lshlrev_b64 v[58:59], 13, v[58:59]
	v_or_b32_e32 v62, 0x78, v62
	v_lshl_add_u64 v[58:59], v[64:65], 0, v[58:59]
	v_ashrrev_i32_e32 v63, 31, v62
	global_load_dwordx4 v[58:61], v[58:59], off nt
	v_lshlrev_b64 v[62:63], 13, v[62:63]
	v_lshl_add_u64 v[62:63], v[64:65], 0, v[62:63]
	global_load_dwordx4 v[62:65], v[62:63], off nt
	s_add_u32 s28, s7, s28
	s_addc_u32 s29, s27, 0
	s_waitcnt vmcnt(15)
	v_pk_mul_f32 v[2:3], v[2:3], s[2:3] op_sel_hi:[1,0]
	ds_write2_b32 v78, v2, v3 offset1:1
	v_pk_mul_f32 v[2:3], v[4:5], s[2:3] op_sel_hi:[1,0]
	ds_write2_b32 v78, v2, v3 offset0:2 offset1:3
	s_waitcnt vmcnt(14)
	v_pk_mul_f32 v[2:3], v[6:7], s[2:3] op_sel_hi:[1,0]
	ds_write2_b32 v79, v2, v3 offset1:1
	v_pk_mul_f32 v[2:3], v[8:9], s[2:3] op_sel_hi:[1,0]
	ds_write2_b32 v80, v2, v3 offset1:1
	v_mov_b32_e32 v5, v69
	s_waitcnt vmcnt(13)
	v_pk_mul_f32 v[2:3], v[10:11], s[2:3] op_sel_hi:[1,0]
	ds_write2_b32 v81, v2, v3 offset1:1
	v_pk_mul_f32 v[2:3], v[12:13], s[2:3] op_sel_hi:[1,0]
	ds_write2_b32 v82, v2, v3 offset1:1
	s_waitcnt vmcnt(12)
	v_pk_mul_f32 v[2:3], v[14:15], s[2:3] op_sel_hi:[1,0]
	ds_write2_b32 v83, v2, v3 offset1:1
	v_pk_mul_f32 v[2:3], v[16:17], s[2:3] op_sel_hi:[1,0]
	ds_write2_b32 v84, v2, v3 offset1:1
	v_lshl_add_u64 v[14:15], s[28:29], 0, v[66:67]
	s_waitcnt vmcnt(11)
	v_pk_mul_f32 v[2:3], v[18:19], s[2:3] op_sel_hi:[1,0]
	ds_write2_b32 v85, v2, v3 offset1:1
	v_pk_mul_f32 v[2:3], v[20:21], s[2:3] op_sel_hi:[1,0]
	ds_write2_b32 v86, v2, v3 offset1:1
	s_waitcnt vmcnt(10)
	v_pk_mul_f32 v[2:3], v[22:23], s[2:3] op_sel_hi:[1,0]
	ds_write2_b32 v87, v2, v3 offset1:1
	v_pk_mul_f32 v[2:3], v[24:25], s[2:3] op_sel_hi:[1,0]
	ds_write2_b32 v88, v2, v3 offset1:1
	s_waitcnt vmcnt(9)
	v_pk_mul_f32 v[2:3], v[26:27], s[2:3] op_sel_hi:[1,0]
	ds_write2_b32 v89, v2, v3 offset1:1
	v_pk_mul_f32 v[2:3], v[28:29], s[2:3] op_sel_hi:[1,0]
	ds_write2_b32 v90, v2, v3 offset1:1
	s_waitcnt vmcnt(8)
	v_pk_mul_f32 v[2:3], v[30:31], s[2:3] op_sel_hi:[1,0]
	ds_write2_b32 v91, v2, v3 offset1:1
	v_pk_mul_f32 v[2:3], v[32:33], s[2:3] op_sel_hi:[1,0]
	ds_write2_b32 v92, v2, v3 offset1:1
	s_waitcnt vmcnt(7)
	v_pk_mul_f32 v[2:3], v[34:35], s[2:3] op_sel_hi:[1,0]
	ds_write2_b32 v93, v2, v3 offset1:1
	v_pk_mul_f32 v[2:3], v[36:37], s[2:3] op_sel_hi:[1,0]
	ds_write2_b32 v94, v2, v3 offset1:1
	s_waitcnt vmcnt(6)
	v_pk_mul_f32 v[2:3], v[38:39], s[2:3] op_sel_hi:[1,0]
	ds_write2_b32 v95, v2, v3 offset1:1
	v_pk_mul_f32 v[2:3], v[40:41], s[2:3] op_sel_hi:[1,0]
	ds_write2_b32 v96, v2, v3 offset1:1
	s_waitcnt vmcnt(5)
	v_pk_mul_f32 v[2:3], v[42:43], s[2:3] op_sel_hi:[1,0]
	ds_write2_b32 v97, v2, v3 offset1:1
	v_pk_mul_f32 v[2:3], v[44:45], s[2:3] op_sel_hi:[1,0]
	ds_write2_b32 v98, v2, v3 offset1:1
	s_waitcnt vmcnt(4)
	v_pk_mul_f32 v[2:3], v[46:47], s[2:3] op_sel_hi:[1,0]
	ds_write2_b32 v99, v2, v3 offset1:1
	v_pk_mul_f32 v[2:3], v[48:49], s[2:3] op_sel_hi:[1,0]
	ds_write2_b32 v100, v2, v3 offset1:1
	s_waitcnt vmcnt(3)
	v_pk_mul_f32 v[2:3], v[50:51], s[2:3] op_sel_hi:[1,0]
	ds_write2_b32 v101, v2, v3 offset1:1
	v_pk_mul_f32 v[2:3], v[52:53], s[2:3] op_sel_hi:[1,0]
	ds_write2_b32 v102, v2, v3 offset1:1
	s_waitcnt vmcnt(2)
	v_pk_mul_f32 v[2:3], v[54:55], s[2:3] op_sel_hi:[1,0]
	ds_write2_b32 v103, v2, v3 offset1:1
	v_pk_mul_f32 v[2:3], v[56:57], s[2:3] op_sel_hi:[1,0]
	ds_write2_b32 v104, v2, v3 offset1:1
	s_waitcnt vmcnt(1)
	v_pk_mul_f32 v[2:3], v[58:59], s[2:3] op_sel_hi:[1,0]
	ds_write2_b32 v105, v2, v3 offset1:1
	v_pk_mul_f32 v[2:3], v[60:61], s[2:3] op_sel_hi:[1,0]
	ds_write2_b32 v106, v2, v3 offset1:1
	s_waitcnt vmcnt(0)
	v_pk_mul_f32 v[2:3], v[62:63], s[2:3] op_sel_hi:[1,0]
	ds_write2_b32 v107, v2, v3 offset1:1
	v_pk_mul_f32 v[2:3], v[64:65], s[2:3] op_sel_hi:[1,0]
	ds_write2_b32 v108, v2, v3 offset1:1
	s_waitcnt lgkmcnt(0)
	ds_read2_b32 v[6:7], v109 offset0:206 offset1:214
	ds_read2_b32 v[8:9], v109 offset0:239 offset1:247
	ds_read2_b32 v[10:11], v109 offset0:140 offset1:148
	ds_read2_b32 v[12:13], v109 offset0:173 offset1:181
	ds_read2_b32 v[16:17], v109 offset0:74 offset1:82
	ds_read2_b32 v[18:19], v109 offset0:107 offset1:115
	ds_read2_b32 v[20:21], v109 offset0:8 offset1:16
	ds_read2_b32 v[22:23], v109 offset0:41 offset1:49
	s_waitcnt lgkmcnt(7)
	v_med3_f32 v2, v6, s22, v110
	s_waitcnt lgkmcnt(6)
	v_med3_f32 v3, v8, s22, v110
	s_waitcnt lgkmcnt(5)
	v_med3_f32 v4, v10, s22, v110
	s_waitcnt lgkmcnt(4)
	v_med3_f32 v6, v12, s22, v110
	v_cvt_pk_fp8_f32 v5, v4, v6
	s_waitcnt lgkmcnt(1)
	v_med3_f32 v6, v20, s22, v110
	s_waitcnt lgkmcnt(0)
	v_med3_f32 v8, v22, s22, v110
	v_mov_b32_e32 v4, v69
	ds_read2_b32 v[24:25], v77 offset0:198 offset1:206
	ds_read2_b32 v[26:27], v77 offset0:231 offset1:239
	ds_read2_b32 v[28:29], v77 offset0:132 offset1:140
	ds_read2_b32 v[30:31], v77 offset0:165 offset1:173
	v_cvt_pk_fp8_f32 v4, v6, v8
	ds_read2_b32 v[32:33], v77 offset1:8
	ds_read2_b32 v[34:35], v77 offset0:33 offset1:41
	v_cvt_pk_fp8_f32 v5, v2, v3 op_sel:[0,0,1]
	v_med3_f32 v2, v16, s22, v110
	v_med3_f32 v3, v18, s22, v110
	v_cvt_pk_fp8_f32 v4, v2, v3 op_sel:[0,0,1]
	s_waitcnt lgkmcnt(3)
	v_med3_f32 v2, v28, s22, v110
	s_waitcnt lgkmcnt(2)
	v_med3_f32 v10, v30, s22, v110
	v_mov_b32_e32 v3, v69
	ds_read2_b32 v[36:37], v77 offset0:66 offset1:74
	ds_read2_b32 v[38:39], v77 offset0:99 offset1:107
	v_cvt_pk_fp8_f32 v3, v2, v10
	s_waitcnt lgkmcnt(3)
	v_med3_f32 v10, v32, s22, v110
	s_waitcnt lgkmcnt(2)
	v_med3_f32 v12, v34, s22, v110
	v_mov_b32_e32 v2, v69
	v_cvt_pk_fp8_f32 v2, v10, v12
	v_med3_f32 v6, v24, s22, v110
	v_med3_f32 v8, v26, s22, v110
	v_cvt_pk_fp8_f32 v3, v6, v8 op_sel:[0,0,1]
	s_waitcnt lgkmcnt(1)
	v_med3_f32 v6, v36, s22, v110
	s_waitcnt lgkmcnt(0)
	v_med3_f32 v8, v38, s22, v110
	v_cvt_pk_fp8_f32 v2, v6, v8 op_sel:[0,0,1]
	v_or_b32_e32 v6, s6, v73
	v_mul_u32_u24_e32 v68, 0x1600, v6
	v_lshl_add_u64 v[40:41], v[14:15], 0, v[68:69]
	global_store_dwordx4 v[40:41], v[2:5], off nt
	v_med3_f32 v8, v23, s22, v110
	v_med3_f32 v10, v35, s22, v110
	v_med3_f32 v2, v7, s22, v110
	v_med3_f32 v4, v11, s22, v110
	v_med3_f32 v7, v13, s22, v110
	v_mov_b32_e32 v5, v69
	v_cvt_pk_fp8_f32 v5, v4, v7
	v_med3_f32 v7, v21, s22, v110
	v_mov_b32_e32 v4, v69
	v_cvt_pk_fp8_f32 v4, v7, v8
	v_med3_f32 v3, v9, s22, v110
	v_cvt_pk_fp8_f32 v5, v2, v3 op_sel:[0,0,1]
	v_med3_f32 v2, v17, s22, v110
	v_med3_f32 v3, v19, s22, v110
	v_cvt_pk_fp8_f32 v4, v2, v3 op_sel:[0,0,1]
	v_med3_f32 v2, v29, s22, v110
	v_med3_f32 v9, v31, s22, v110
	v_mov_b32_e32 v3, v69
	v_cvt_pk_fp8_f32 v3, v2, v9
	v_med3_f32 v9, v33, s22, v110
	v_mov_b32_e32 v2, v69
	v_cvt_pk_fp8_f32 v2, v9, v10
	v_med3_f32 v7, v25, s22, v110
	v_med3_f32 v8, v27, s22, v110
	v_cvt_pk_fp8_f32 v3, v7, v8 op_sel:[0,0,1]
	v_med3_f32 v7, v37, s22, v110
	v_med3_f32 v8, v39, s22, v110
	v_cvt_pk_fp8_f32 v2, v7, v8 op_sel:[0,0,1]
	ds_read2_b32 v[8:9], v109 offset0:222 offset1:230
	ds_read2_b32 v[10:11], v111 offset0:127 offset1:135
	ds_read2_b32 v[12:13], v109 offset0:156 offset1:164
	ds_read2_b32 v[16:17], v109 offset0:189 offset1:197
	v_or_b32_e32 v6, s6, v74
	v_mul_u32_u24_e32 v68, 0x1600, v6
	v_lshl_add_u64 v[6:7], v[14:15], 0, v[68:69]
	global_store_dwordx4 v[6:7], v[2:5], off nt
	s_waitcnt lgkmcnt(0)
	v_med3_f32 v6, v16, s22, v110
	v_med3_f32 v4, v12, s22, v110
	v_mov_b32_e32 v5, v69
	v_cvt_pk_fp8_f32 v5, v4, v6
	ds_read2_b32 v[6:7], v109 offset0:90 offset1:98
	ds_read2_b32 v[18:19], v109 offset0:123 offset1:131
	ds_read2_b32 v[20:21], v109 offset0:24 offset1:32
	ds_read2_b32 v[22:23], v109 offset0:57 offset1:65
	v_med3_f32 v2, v8, s22, v110
	v_med3_f32 v3, v10, s22, v110
	v_cvt_pk_fp8_f32 v5, v2, v3 op_sel:[0,0,1]
	s_waitcnt lgkmcnt(3)
	v_med3_f32 v2, v6, s22, v110
	s_waitcnt lgkmcnt(1)
	v_med3_f32 v6, v20, s22, v110
	s_waitcnt lgkmcnt(0)
	v_med3_f32 v8, v22, s22, v110
	v_mov_b32_e32 v4, v69
	ds_read2_b32 v[24:25], v77 offset0:214 offset1:222
	ds_read2_b32 v[26:27], v77 offset0:247 offset1:255
	ds_read2_b32 v[28:29], v77 offset0:148 offset1:156
	ds_read2_b32 v[30:31], v77 offset0:181 offset1:189
	v_cvt_pk_fp8_f32 v4, v6, v8
	ds_read2_b32 v[32:33], v77 offset0:16 offset1:24
	ds_read2_b32 v[34:35], v77 offset0:49 offset1:57
	v_med3_f32 v3, v18, s22, v110
	ds_read2_b32 v[36:37], v77 offset0:82 offset1:90
	ds_read2_b32 v[38:39], v77 offset0:115 offset1:123
	v_cvt_pk_fp8_f32 v4, v2, v3 op_sel:[0,0,1]
	s_waitcnt lgkmcnt(5)
	v_med3_f32 v2, v28, s22, v110
	s_waitcnt lgkmcnt(4)
	v_med3_f32 v10, v30, s22, v110
	v_mov_b32_e32 v3, v69
	v_cvt_pk_fp8_f32 v3, v2, v10
	s_waitcnt lgkmcnt(3)
	v_med3_f32 v10, v32, s22, v110
	s_waitcnt lgkmcnt(2)
	v_med3_f32 v12, v34, s22, v110
	v_mov_b32_e32 v2, v69
	v_cvt_pk_fp8_f32 v2, v10, v12
	v_med3_f32 v6, v24, s22, v110
	v_med3_f32 v8, v26, s22, v110
	v_cvt_pk_fp8_f32 v3, v6, v8 op_sel:[0,0,1]
	s_waitcnt lgkmcnt(1)
	v_med3_f32 v6, v36, s22, v110
	s_waitcnt lgkmcnt(0)
	v_med3_f32 v8, v38, s22, v110
	v_cvt_pk_fp8_f32 v2, v6, v8 op_sel:[0,0,1]
	v_or_b32_e32 v6, s6, v75
	v_mul_u32_u24_e32 v68, 0x1600, v6
	v_lshl_add_u64 v[40:41], v[14:15], 0, v[68:69]
	global_store_dwordx4 v[40:41], v[2:5], off nt
	v_med3_f32 v6, v17, s22, v110
	v_med3_f32 v8, v23, s22, v110
	v_med3_f32 v4, v13, s22, v110
	v_mov_b32_e32 v5, v69
	v_cvt_pk_fp8_f32 v5, v4, v6
	v_med3_f32 v6, v21, s22, v110
	v_mov_b32_e32 v4, v69
	v_cvt_pk_fp8_f32 v4, v6, v8
	v_med3_f32 v2, v9, s22, v110
	v_med3_f32 v3, v11, s22, v110
	v_cvt_pk_fp8_f32 v5, v2, v3 op_sel:[0,0,1]
	v_med3_f32 v2, v7, s22, v110
	v_med3_f32 v3, v19, s22, v110
	v_cvt_pk_fp8_f32 v4, v2, v3 op_sel:[0,0,1]
	v_med3_f32 v2, v29, s22, v110
	v_med3_f32 v8, v31, s22, v110
	v_mov_b32_e32 v3, v69
	v_cvt_pk_fp8_f32 v3, v2, v8
	v_med3_f32 v8, v33, s22, v110
	v_med3_f32 v9, v35, s22, v110
	v_mov_b32_e32 v2, v69
	v_cvt_pk_fp8_f32 v2, v8, v9
	v_med3_f32 v6, v25, s22, v110
	v_med3_f32 v7, v27, s22, v110
	v_cvt_pk_fp8_f32 v3, v6, v7 op_sel:[0,0,1]
	v_med3_f32 v6, v37, s22, v110
	v_med3_f32 v7, v39, s22, v110
	v_cvt_pk_fp8_f32 v2, v6, v7 op_sel:[0,0,1]
	v_or_b32_e32 v6, s6, v76
	v_mul_u32_u24_e32 v68, 0x1600, v6
	v_lshl_add_u64 v[6:7], v[14:15], 0, v[68:69]
	global_store_dwordx4 v[6:7], v[2:5], off nt
	s_waitcnt lgkmcnt(0)
	s_mov_b64 s[6:7], 0
.LBB0_945:
	s_andn2_b64 vcc, exec, s[6:7]
	s_cbranch_vccnz .LBB0_942
	s_cmpk_gt_i32 s26, 0xaff
	s_cselect_b64 s[6:7], -1, 0
	s_and_b64 s[26:27], s[6:7], exec
	s_cselect_b32 s26, 0xfffff500, 0
	s_mul_i32 s27, s8, 0x2100
	s_cselect_b32 s28, s24, 0xe0
	s_sub_i32 s26, s26, s27
	s_add_i32 s9, s9, s26
	s_add_u32 s26, s74, s28
	s_addc_u32 s27, s75, 0
	s_load_dwordx2 s[26:27], s[26:27], 0x0
	s_lshl_b64 s[4:5], s[4:5], 2
	s_mul_hi_i32 s28, s9, 0x2e8ba2e9
	v_mov_b32_e32 v6, 0
	v_mov_b32_e32 v7, 0
	s_waitcnt lgkmcnt(0)
	s_add_u32 s4, s26, s4
	s_addc_u32 s5, s27, s5
	s_lshr_b32 s26, s28, 31
	s_ashr_i32 s27, s28, 5
	s_add_i32 s27, s27, s26
	s_mul_i32 s26, s27, 0xb0
	s_sub_i32 s26, s9, s26
	s_lshl_b32 s9, s27, 7
	s_lshl_b32 s27, s26, 5
	v_or_b32_e32 v2, s27, v72
	v_ashrrev_i32_e32 v3, 31, v2
	v_cmp_gt_i32_e32 vcc, s23, v2
	v_or_b32_e32 v68, s9, v73
	v_lshl_add_u64 v[70:71], v[2:3], 2, s[4:5]
	v_mov_b32_e32 v2, 0
	v_mov_b32_e32 v8, 0
	v_mov_b32_e32 v9, 0
	s_and_saveexec_b64 s[4:5], vcc
	s_cbranch_execz .LBB0_948
	v_mad_i64_i32 v[4:5], s[28:29], v68, s25, v[70:71]
	global_load_dwordx4 v[6:9], v[4:5], off nt
.LBB0_948:
	s_or_b64 exec, exec, s[4:5]
	v_mov_b32_e32 v3, 0
	v_mov_b32_e32 v4, 0
	v_mov_b32_e32 v5, 0
	s_and_saveexec_b64 s[4:5], vcc
	s_cbranch_execz .LBB0_950
	v_or_b32_e32 v2, 8, v68
	v_mad_i64_i32 v[2:3], s[28:29], v2, s25, v[70:71]
	global_load_dwordx4 v[2:5], v[2:3], off nt
.LBB0_950:
	s_or_b64 exec, exec, s[4:5]
	v_mov_b32_e32 v10, 0
	v_mov_b32_e32 v14, 0
	v_mov_b32_e32 v15, 0
	v_mov_b32_e32 v16, 0
	v_mov_b32_e32 v17, 0
	s_and_saveexec_b64 s[4:5], vcc
	s_cbranch_execz .LBB0_952
	v_or_b32_e32 v11, 16, v68
	v_mad_i64_i32 v[12:13], s[28:29], v11, s25, v[70:71]
	global_load_dwordx4 v[14:17], v[12:13], off nt
.LBB0_952:
	s_or_b64 exec, exec, s[4:5]
	v_mov_b32_e32 v11, 0
	v_mov_b32_e32 v12, 0
	v_mov_b32_e32 v13, 0
	s_and_saveexec_b64 s[4:5], vcc
	s_cbranch_execz .LBB0_954
	v_or_b32_e32 v10, 24, v68
	v_mad_i64_i32 v[10:11], s[28:29], v10, s25, v[70:71]
	global_load_dwordx4 v[10:13], v[10:11], off nt
.LBB0_954:
	s_or_b64 exec, exec, s[4:5]
	v_mov_b32_e32 v18, 0
	v_mov_b32_e32 v22, 0
	v_mov_b32_e32 v23, 0
	v_mov_b32_e32 v24, 0
	v_mov_b32_e32 v25, 0
	s_and_saveexec_b64 s[4:5], vcc
	s_cbranch_execz .LBB0_956
	v_or_b32_e32 v19, 32, v68
	v_mad_i64_i32 v[20:21], s[28:29], v19, s25, v[70:71]
	global_load_dwordx4 v[22:25], v[20:21], off nt
.LBB0_956:
	s_or_b64 exec, exec, s[4:5]
	v_mov_b32_e32 v19, 0
	v_mov_b32_e32 v20, 0
	v_mov_b32_e32 v21, 0
	s_and_saveexec_b64 s[4:5], vcc
	s_cbranch_execz .LBB0_958
	v_or_b32_e32 v18, 40, v68
	v_mad_i64_i32 v[18:19], s[28:29], v18, s25, v[70:71]
	global_load_dwordx4 v[18:21], v[18:19], off nt
.LBB0_958:
	s_or_b64 exec, exec, s[4:5]
	v_mov_b32_e32 v26, 0
	v_mov_b32_e32 v30, 0
	v_mov_b32_e32 v31, 0
	v_mov_b32_e32 v32, 0
	v_mov_b32_e32 v33, 0
	s_and_saveexec_b64 s[4:5], vcc
	s_cbranch_execz .LBB0_960
	v_or_b32_e32 v27, 48, v68
	v_mad_i64_i32 v[28:29], s[28:29], v27, s25, v[70:71]
	global_load_dwordx4 v[30:33], v[28:29], off nt
.LBB0_960:
	s_or_b64 exec, exec, s[4:5]
	v_mov_b32_e32 v27, 0
	v_mov_b32_e32 v28, 0
	v_mov_b32_e32 v29, 0
	s_and_saveexec_b64 s[4:5], vcc
	s_cbranch_execz .LBB0_962
	v_or_b32_e32 v26, 56, v68
	v_mad_i64_i32 v[26:27], s[28:29], v26, s25, v[70:71]
	global_load_dwordx4 v[26:29], v[26:27], off nt
.LBB0_962:
	s_or_b64 exec, exec, s[4:5]
	v_mov_b32_e32 v34, 0
	v_mov_b32_e32 v38, 0
	v_mov_b32_e32 v39, 0
	v_mov_b32_e32 v40, 0
	v_mov_b32_e32 v41, 0
	s_and_saveexec_b64 s[4:5], vcc
	s_cbranch_execz .LBB0_964
	v_or_b32_e32 v35, 64, v68
	v_mad_i64_i32 v[36:37], s[28:29], v35, s25, v[70:71]
	global_load_dwordx4 v[38:41], v[36:37], off nt
.LBB0_964:
	s_or_b64 exec, exec, s[4:5]
	v_mov_b32_e32 v35, 0
	v_mov_b32_e32 v36, 0
	v_mov_b32_e32 v37, 0
	s_and_saveexec_b64 s[4:5], vcc
	s_cbranch_execz .LBB0_966
	v_or_b32_e32 v34, 0x48, v68
	v_mad_i64_i32 v[34:35], s[28:29], v34, s25, v[70:71]
	global_load_dwordx4 v[34:37], v[34:35], off nt
.LBB0_966:
	s_or_b64 exec, exec, s[4:5]
	v_mov_b32_e32 v42, 0
	v_mov_b32_e32 v46, 0
	v_mov_b32_e32 v47, 0
	v_mov_b32_e32 v48, 0
	v_mov_b32_e32 v49, 0
	s_and_saveexec_b64 s[4:5], vcc
	s_cbranch_execz .LBB0_968
	v_or_b32_e32 v43, 0x50, v68
	v_mad_i64_i32 v[44:45], s[28:29], v43, s25, v[70:71]
	global_load_dwordx4 v[46:49], v[44:45], off nt
.LBB0_968:
	s_or_b64 exec, exec, s[4:5]
	v_mov_b32_e32 v43, 0
	v_mov_b32_e32 v44, 0
	v_mov_b32_e32 v45, 0
	s_and_saveexec_b64 s[4:5], vcc
	s_cbranch_execz .LBB0_970
	v_or_b32_e32 v42, 0x58, v68
	v_mad_i64_i32 v[42:43], s[28:29], v42, s25, v[70:71]
	global_load_dwordx4 v[42:45], v[42:43], off nt
.LBB0_970:
	s_or_b64 exec, exec, s[4:5]
	v_mov_b32_e32 v50, 0
	v_mov_b32_e32 v54, 0
	v_mov_b32_e32 v55, 0
	v_mov_b32_e32 v56, 0
	v_mov_b32_e32 v57, 0
	s_and_saveexec_b64 s[4:5], vcc
	s_cbranch_execz .LBB0_972
	v_or_b32_e32 v51, 0x60, v68
	v_mad_i64_i32 v[52:53], s[28:29], v51, s25, v[70:71]
	global_load_dwordx4 v[54:57], v[52:53], off nt
.LBB0_972:
	s_or_b64 exec, exec, s[4:5]
	v_mov_b32_e32 v51, 0
	v_mov_b32_e32 v52, 0
	v_mov_b32_e32 v53, 0
	s_and_saveexec_b64 s[4:5], vcc
	s_cbranch_execz .LBB0_974
	v_or_b32_e32 v50, 0x68, v68
	v_mad_i64_i32 v[50:51], s[28:29], v50, s25, v[70:71]
	global_load_dwordx4 v[50:53], v[50:51], off nt
.LBB0_974:
	s_or_b64 exec, exec, s[4:5]
	v_mov_b32_e32 v58, 0
	v_mov_b32_e32 v62, 0
	v_mov_b32_e32 v63, 0
	v_mov_b32_e32 v64, 0
	v_mov_b32_e32 v65, 0
	s_and_saveexec_b64 s[4:5], vcc
	s_cbranch_execz .LBB0_976
	v_or_b32_e32 v59, 0x70, v68
	v_mad_i64_i32 v[60:61], s[28:29], v59, s25, v[70:71]
	global_load_dwordx4 v[62:65], v[60:61], off nt
.LBB0_976:
	s_or_b64 exec, exec, s[4:5]
	v_mov_b32_e32 v59, 0
	v_mov_b32_e32 v60, 0
	v_mov_b32_e32 v61, 0
	s_and_saveexec_b64 s[4:5], vcc
	s_cbranch_execz .LBB0_978
	v_or_b32_e32 v58, 0x78, v68
	v_mad_i64_i32 v[58:59], s[28:29], v58, s25, v[70:71]
	global_load_dwordx4 v[58:61], v[58:59], off nt
.LBB0_978:
	s_or_b64 exec, exec, s[4:5]
	s_mul_i32 s5, s8, 0x1600000
	s_mul_hi_i32 s4, s8, 0x1600000
	s_add_u32 s28, s12, s5
	s_addc_u32 s29, s14, s4
	s_mul_i32 s4, s8, 0x2c00
	s_ashr_i32 s5, s4, 31
	s_lshl_b64 s[4:5], s[4:5], 2
	s_add_u32 s4, s15, s4
	s_waitcnt vmcnt(0)
	ds_write2_b32 v78, v6, v7 offset1:1
	ds_write2_b32 v78, v8, v9 offset0:2 offset1:3
	ds_write2_b32 v79, v2, v3 offset1:1
	ds_write2_b32 v80, v4, v5 offset1:1
	ds_write2_b32 v81, v14, v15 offset1:1
	ds_write2_b32 v82, v16, v17 offset1:1
	ds_write2_b32 v83, v10, v11 offset1:1
	ds_write2_b32 v84, v12, v13 offset1:1
	ds_write2_b32 v85, v22, v23 offset1:1
	ds_write2_b32 v86, v24, v25 offset1:1
	ds_write2_b32 v87, v18, v19 offset1:1
	ds_write2_b32 v88, v20, v21 offset1:1
	ds_write2_b32 v89, v30, v31 offset1:1
	ds_write2_b32 v90, v32, v33 offset1:1
	ds_write2_b32 v91, v26, v27 offset1:1
	ds_write2_b32 v92, v28, v29 offset1:1
	ds_write2_b32 v93, v38, v39 offset1:1
	ds_write2_b32 v94, v40, v41 offset1:1
	ds_write2_b32 v95, v34, v35 offset1:1
	ds_write2_b32 v96, v36, v37 offset1:1
	ds_write2_b32 v97, v46, v47 offset1:1
	ds_write2_b32 v98, v48, v49 offset1:1
	ds_write2_b32 v99, v42, v43 offset1:1
	ds_write2_b32 v100, v44, v45 offset1:1
	ds_write2_b32 v101, v54, v55 offset1:1
	ds_write2_b32 v102, v56, v57 offset1:1
	ds_write2_b32 v103, v50, v51 offset1:1
	ds_write2_b32 v104, v52, v53 offset1:1
	ds_write2_b32 v105, v62, v63 offset1:1
	ds_write2_b32 v106, v64, v65 offset1:1
	ds_write2_b32 v107, v58, v59 offset1:1
	ds_write2_b32 v108, v60, v61 offset1:1
	s_addc_u32 s5, s16, s5
	s_waitcnt lgkmcnt(0)
	s_ashr_i32 s30, s9, 31
	s_add_u32 s8, s28, s9
	s_addc_u32 s9, s29, s30
	v_or_b32_e32 v4, s27, v73
	v_lshl_add_u64 v[2:3], s[8:9], 0, v[66:67]
	v_cmp_gt_i32_e32 vcc, s23, v4
	s_and_saveexec_b64 s[8:9], vcc
	s_cbranch_execz .LBB0_980
	s_lshl_b32 s28, s26, 6
	s_and_b32 s28, s28, 0xffffff00
	v_and_b32_e32 v4, 0x67, v4
	v_or_b32_e32 v4, s28, v4
	v_or_b32_e32 v5, 0x80, v4
	v_cndmask_b32_e64 v4, v4, v5, s[6:7]
	v_ashrrev_i32_e32 v5, 31, v4
	v_lshl_add_u64 v[6:7], v[4:5], 2, s[4:5]
	global_load_dword v24, v[6:7], off
	v_lshlrev_b64 v[22:23], 11, v[4:5]
	ds_read2_b32 v[6:7], v77 offset1:33
	ds_read2_b32 v[8:9], v77 offset0:66 offset1:99
	ds_read2_b32 v[10:11], v77 offset0:132 offset1:165
	ds_read2_b32 v[12:13], v77 offset0:198 offset1:231
	ds_read2_b32 v[14:15], v109 offset0:8 offset1:41
	ds_read2_b32 v[16:17], v109 offset0:74 offset1:107
	ds_read2_b32 v[18:19], v109 offset0:140 offset1:173
	ds_read2_b32 v[20:21], v109 offset0:206 offset1:239
	s_waitcnt vmcnt(0)
	v_div_scale_f32 v25, s[28:29], v24, v24, 1.0
	v_rcp_f32_e32 v26, v25
	v_div_scale_f32 v4, vcc, 1.0, v24, 1.0
	v_fma_f32 v5, -v25, v26, 1.0
	v_fmac_f32_e32 v26, v5, v26
	v_mul_f32_e32 v5, v4, v26
	v_fma_f32 v27, -v25, v5, v4
	v_fmac_f32_e32 v5, v27, v26
	v_fma_f32 v4, -v25, v5, v4
	v_div_fmas_f32 v4, v4, v26, v5
	v_div_fixup_f32 v4, v4, v24, 1.0
	s_waitcnt lgkmcnt(7)
	v_fmaak_f32 v5, v6, v4, 0x43000000
	v_fmaak_f32 v6, v4, v7, 0x43000000
	s_waitcnt lgkmcnt(6)
	v_fmaak_f32 v7, v4, v8, 0x43000000
	v_fmaak_f32 v8, v4, v9, 0x43000000
	s_waitcnt lgkmcnt(5)
	v_fmaak_f32 v9, v4, v10, 0x43000000
	v_fmaak_f32 v10, v4, v11, 0x43000000
	s_waitcnt lgkmcnt(4)
	v_fmaak_f32 v11, v4, v12, 0x43000000
	v_fmaak_f32 v12, v4, v13, 0x43000000
	s_waitcnt lgkmcnt(3)
	v_fmaak_f32 v13, v4, v14, 0x43000000
	v_fmaak_f32 v14, v4, v15, 0x43000000
	s_waitcnt lgkmcnt(2)
	v_fmaak_f32 v15, v4, v16, 0x43000000
	v_fmaak_f32 v16, v4, v17, 0x43000000
	s_waitcnt lgkmcnt(1)
	v_fmaak_f32 v17, v4, v18, 0x43000000
	v_fmaak_f32 v18, v4, v19, 0x43000000
	v_rndne_f32_e32 v5, v5
	v_rndne_f32_e32 v9, v9
	v_rndne_f32_e32 v13, v13
	v_rndne_f32_e32 v17, v17
	s_waitcnt lgkmcnt(0)
	v_fmaak_f32 v19, v4, v20, 0x43000000
	v_rndne_f32_e32 v6, v6
	v_rndne_f32_e32 v10, v10
	v_rndne_f32_e32 v14, v14
	v_rndne_f32_e32 v18, v18
	v_cvt_pk_u8_f32 v5, v5, 0, 0
	v_cvt_pk_u8_f32 v9, v9, 0, 0
	v_cvt_pk_u8_f32 v13, v13, 0, 0
	v_cvt_pk_u8_f32 v17, v17, 0, 0
	v_fmaak_f32 v4, v4, v21, 0x43000000
	v_rndne_f32_e32 v7, v7
	v_rndne_f32_e32 v11, v11
	v_rndne_f32_e32 v15, v15
	v_rndne_f32_e32 v19, v19
	v_cvt_pk_u8_f32 v5, v6, 1, v5
	v_cvt_pk_u8_f32 v6, v10, 1, v9
	v_cvt_pk_u8_f32 v9, v14, 1, v13
	v_cvt_pk_u8_f32 v10, v18, 1, v17
	v_rndne_f32_e32 v8, v8
	v_rndne_f32_e32 v12, v12
	v_rndne_f32_e32 v16, v16
	v_rndne_f32_e32 v4, v4
	v_cvt_pk_u8_f32 v5, v7, 2, v5
	v_cvt_pk_u8_f32 v6, v11, 2, v6
	v_cvt_pk_u8_f32 v7, v15, 2, v9
	v_cvt_pk_u8_f32 v9, v19, 2, v10
	v_cvt_pk_u8_f32 v5, v8, 3, v5
	v_cvt_pk_u8_f32 v6, v12, 3, v6
	v_cvt_pk_u8_f32 v7, v16, 3, v7
	v_cvt_pk_u8_f32 v8, v4, 3, v9
	v_xor_b32_e32 v4, 0x80808080, v5
	v_xor_b32_e32 v5, 0x80808080, v6
	v_xor_b32_e32 v6, 0x80808080, v7
	v_xor_b32_e32 v7, 0x80808080, v8
	v_lshl_add_u64 v[8:9], v[2:3], 0, v[22:23]
	global_store_dwordx4 v[8:9], v[4:7], off nt
.LBB0_980:
	s_or_b64 exec, exec, s[8:9]
	s_nop 0
	v_or_b32_e32 v4, s27, v74
	v_cmp_gt_i32_e32 vcc, s23, v4
	s_and_saveexec_b64 s[8:9], vcc
	s_cbranch_execz .LBB0_982
	s_lshl_b32 s28, s26, 6
	s_and_b32 s28, s28, 0xffffff00
	v_and_b32_e32 v4, 0x6f, v4
	v_or_b32_e32 v4, s28, v4
	v_or_b32_e32 v5, 0x80, v4
	v_cndmask_b32_e64 v4, v4, v5, s[6:7]
	v_ashrrev_i32_e32 v5, 31, v4
	v_lshl_add_u64 v[6:7], v[4:5], 2, s[4:5]
	global_load_dword v24, v[6:7], off
	v_lshlrev_b64 v[22:23], 11, v[4:5]
	ds_read2_b32 v[6:7], v77 offset0:8 offset1:41
	ds_read2_b32 v[8:9], v77 offset0:74 offset1:107
	ds_read2_b32 v[10:11], v77 offset0:140 offset1:173
	ds_read2_b32 v[12:13], v77 offset0:206 offset1:239
	ds_read2_b32 v[14:15], v109 offset0:16 offset1:49
	ds_read2_b32 v[16:17], v109 offset0:82 offset1:115
	ds_read2_b32 v[18:19], v109 offset0:148 offset1:181
	ds_read2_b32 v[20:21], v109 offset0:214 offset1:247
	s_waitcnt vmcnt(0)
	v_div_scale_f32 v25, s[28:29], v24, v24, 1.0
	v_rcp_f32_e32 v26, v25
	v_div_scale_f32 v4, vcc, 1.0, v24, 1.0
	v_fma_f32 v5, -v25, v26, 1.0
	v_fmac_f32_e32 v26, v5, v26
	v_mul_f32_e32 v5, v4, v26
	v_fma_f32 v27, -v25, v5, v4
	v_fmac_f32_e32 v5, v27, v26
	v_fma_f32 v4, -v25, v5, v4
	v_div_fmas_f32 v4, v4, v26, v5
	v_div_fixup_f32 v4, v4, v24, 1.0
	s_waitcnt lgkmcnt(7)
	v_fmaak_f32 v5, v6, v4, 0x43000000
	v_fmaak_f32 v6, v4, v7, 0x43000000
	s_waitcnt lgkmcnt(6)
	v_fmaak_f32 v7, v4, v8, 0x43000000
	v_fmaak_f32 v8, v4, v9, 0x43000000
	s_waitcnt lgkmcnt(5)
	v_fmaak_f32 v9, v4, v10, 0x43000000
	v_fmaak_f32 v10, v4, v11, 0x43000000
	s_waitcnt lgkmcnt(4)
	v_fmaak_f32 v11, v4, v12, 0x43000000
	v_fmaak_f32 v12, v4, v13, 0x43000000
	s_waitcnt lgkmcnt(3)
	v_fmaak_f32 v13, v4, v14, 0x43000000
	v_fmaak_f32 v14, v4, v15, 0x43000000
	s_waitcnt lgkmcnt(2)
	v_fmaak_f32 v15, v4, v16, 0x43000000
	v_fmaak_f32 v16, v4, v17, 0x43000000
	s_waitcnt lgkmcnt(1)
	v_fmaak_f32 v17, v4, v18, 0x43000000
	v_fmaak_f32 v18, v4, v19, 0x43000000
	v_rndne_f32_e32 v5, v5
	v_rndne_f32_e32 v9, v9
	v_rndne_f32_e32 v13, v13
	v_rndne_f32_e32 v17, v17
	s_waitcnt lgkmcnt(0)
	v_fmaak_f32 v19, v4, v20, 0x43000000
	v_rndne_f32_e32 v6, v6
	v_rndne_f32_e32 v10, v10
	v_rndne_f32_e32 v14, v14
	v_rndne_f32_e32 v18, v18
	v_cvt_pk_u8_f32 v5, v5, 0, 0
	v_cvt_pk_u8_f32 v9, v9, 0, 0
	v_cvt_pk_u8_f32 v13, v13, 0, 0
	v_cvt_pk_u8_f32 v17, v17, 0, 0
	v_fmaak_f32 v4, v4, v21, 0x43000000
	v_rndne_f32_e32 v7, v7
	v_rndne_f32_e32 v11, v11
	v_rndne_f32_e32 v15, v15
	v_rndne_f32_e32 v19, v19
	v_cvt_pk_u8_f32 v5, v6, 1, v5
	v_cvt_pk_u8_f32 v6, v10, 1, v9
	v_cvt_pk_u8_f32 v9, v14, 1, v13
	v_cvt_pk_u8_f32 v10, v18, 1, v17
	v_rndne_f32_e32 v8, v8
	v_rndne_f32_e32 v12, v12
	v_rndne_f32_e32 v16, v16
	v_rndne_f32_e32 v4, v4
	v_cvt_pk_u8_f32 v5, v7, 2, v5
	v_cvt_pk_u8_f32 v6, v11, 2, v6
	v_cvt_pk_u8_f32 v7, v15, 2, v9
	v_cvt_pk_u8_f32 v9, v19, 2, v10
	v_cvt_pk_u8_f32 v5, v8, 3, v5
	v_cvt_pk_u8_f32 v6, v12, 3, v6
	v_cvt_pk_u8_f32 v7, v16, 3, v7
	v_cvt_pk_u8_f32 v8, v4, 3, v9
	v_xor_b32_e32 v4, 0x80808080, v5
	v_xor_b32_e32 v5, 0x80808080, v6
	v_xor_b32_e32 v6, 0x80808080, v7
	v_xor_b32_e32 v7, 0x80808080, v8
	v_lshl_add_u64 v[8:9], v[2:3], 0, v[22:23]
	global_store_dwordx4 v[8:9], v[4:7], off nt
.LBB0_982:
	s_or_b64 exec, exec, s[8:9]
	s_nop 0
	v_or_b32_e32 v4, s27, v75
	v_cmp_gt_i32_e32 vcc, s23, v4
	s_and_saveexec_b64 s[8:9], vcc
	s_cbranch_execz .LBB0_984
	s_lshl_b32 s28, s26, 6
	s_and_b32 s28, s28, 0xffffff00
	v_and_b32_e32 v4, 0x77, v4
	v_or_b32_e32 v4, s28, v4
	v_or_b32_e32 v5, 0x80, v4
	v_cndmask_b32_e64 v4, v4, v5, s[6:7]
	v_ashrrev_i32_e32 v5, 31, v4
	v_lshl_add_u64 v[6:7], v[4:5], 2, s[4:5]
	global_load_dword v24, v[6:7], off
	v_lshlrev_b64 v[22:23], 11, v[4:5]
	ds_read2_b32 v[6:7], v77 offset0:16 offset1:49
	ds_read2_b32 v[8:9], v77 offset0:82 offset1:115
	ds_read2_b32 v[10:11], v77 offset0:148 offset1:181
	ds_read2_b32 v[12:13], v77 offset0:214 offset1:247
	ds_read2_b32 v[14:15], v109 offset0:24 offset1:57
	ds_read2_b32 v[16:17], v109 offset0:90 offset1:123
	ds_read2_b32 v[18:19], v109 offset0:156 offset1:189
	ds_read2_b32 v[20:21], v109 offset0:222 offset1:255
	s_waitcnt vmcnt(0)
	v_div_scale_f32 v25, s[28:29], v24, v24, 1.0
	v_rcp_f32_e32 v26, v25
	v_div_scale_f32 v4, vcc, 1.0, v24, 1.0
	v_fma_f32 v5, -v25, v26, 1.0
	v_fmac_f32_e32 v26, v5, v26
	v_mul_f32_e32 v5, v4, v26
	v_fma_f32 v27, -v25, v5, v4
	v_fmac_f32_e32 v5, v27, v26
	v_fma_f32 v4, -v25, v5, v4
	v_div_fmas_f32 v4, v4, v26, v5
	v_div_fixup_f32 v4, v4, v24, 1.0
	s_waitcnt lgkmcnt(7)
	v_fmaak_f32 v5, v6, v4, 0x43000000
	v_fmaak_f32 v6, v4, v7, 0x43000000
	s_waitcnt lgkmcnt(6)
	v_fmaak_f32 v7, v4, v8, 0x43000000
	v_fmaak_f32 v8, v4, v9, 0x43000000
	s_waitcnt lgkmcnt(5)
	v_fmaak_f32 v9, v4, v10, 0x43000000
	v_fmaak_f32 v10, v4, v11, 0x43000000
	s_waitcnt lgkmcnt(4)
	v_fmaak_f32 v11, v4, v12, 0x43000000
	v_fmaak_f32 v12, v4, v13, 0x43000000
	s_waitcnt lgkmcnt(3)
	v_fmaak_f32 v13, v4, v14, 0x43000000
	v_fmaak_f32 v14, v4, v15, 0x43000000
	s_waitcnt lgkmcnt(2)
	v_fmaak_f32 v15, v4, v16, 0x43000000
	v_fmaak_f32 v16, v4, v17, 0x43000000
	s_waitcnt lgkmcnt(1)
	v_fmaak_f32 v17, v4, v18, 0x43000000
	v_fmaak_f32 v18, v4, v19, 0x43000000
	v_rndne_f32_e32 v5, v5
	v_rndne_f32_e32 v9, v9
	v_rndne_f32_e32 v13, v13
	v_rndne_f32_e32 v17, v17
	s_waitcnt lgkmcnt(0)
	v_fmaak_f32 v19, v4, v20, 0x43000000
	v_rndne_f32_e32 v6, v6
	v_rndne_f32_e32 v10, v10
	v_rndne_f32_e32 v14, v14
	v_rndne_f32_e32 v18, v18
	v_cvt_pk_u8_f32 v5, v5, 0, 0
	v_cvt_pk_u8_f32 v9, v9, 0, 0
	v_cvt_pk_u8_f32 v13, v13, 0, 0
	v_cvt_pk_u8_f32 v17, v17, 0, 0
	v_fmaak_f32 v4, v4, v21, 0x43000000
	v_rndne_f32_e32 v7, v7
	v_rndne_f32_e32 v11, v11
	v_rndne_f32_e32 v15, v15
	v_rndne_f32_e32 v19, v19
	v_cvt_pk_u8_f32 v5, v6, 1, v5
	v_cvt_pk_u8_f32 v6, v10, 1, v9
	v_cvt_pk_u8_f32 v9, v14, 1, v13
	v_cvt_pk_u8_f32 v10, v18, 1, v17
	v_rndne_f32_e32 v8, v8
	v_rndne_f32_e32 v12, v12
	v_rndne_f32_e32 v16, v16
	v_rndne_f32_e32 v4, v4
	v_cvt_pk_u8_f32 v5, v7, 2, v5
	v_cvt_pk_u8_f32 v6, v11, 2, v6
	v_cvt_pk_u8_f32 v7, v15, 2, v9
	v_cvt_pk_u8_f32 v9, v19, 2, v10
	v_cvt_pk_u8_f32 v5, v8, 3, v5
	v_cvt_pk_u8_f32 v6, v12, 3, v6
	v_cvt_pk_u8_f32 v7, v16, 3, v7
	v_cvt_pk_u8_f32 v8, v4, 3, v9
	v_xor_b32_e32 v4, 0x80808080, v5
	v_xor_b32_e32 v5, 0x80808080, v6
	v_xor_b32_e32 v6, 0x80808080, v7
	v_xor_b32_e32 v7, 0x80808080, v8
	v_lshl_add_u64 v[8:9], v[2:3], 0, v[22:23]
	global_store_dwordx4 v[8:9], v[4:7], off nt
.LBB0_984:
	s_or_b64 exec, exec, s[8:9]
	s_nop 0
	v_or_b32_e32 v4, s27, v76
	v_cmp_gt_i32_e32 vcc, s23, v4
	s_and_saveexec_b64 s[8:9], vcc
	s_cbranch_execz .LBB0_941
	s_lshl_b32 s26, s26, 6
	s_and_b32 s26, s26, 0xffffff00
	v_and_b32_e32 v4, 0x7f, v4
	v_or_b32_e32 v4, s26, v4
	v_or_b32_e32 v5, 0x80, v4
	v_cndmask_b32_e64 v4, v4, v5, s[6:7]
	v_ashrrev_i32_e32 v5, 31, v4
	v_lshl_add_u64 v[6:7], v[4:5], 2, s[4:5]
	global_load_dword v24, v[6:7], off
	v_lshlrev_b64 v[22:23], 11, v[4:5]
	ds_read2_b32 v[6:7], v77 offset0:24 offset1:57
	ds_read2_b32 v[8:9], v77 offset0:90 offset1:123
	ds_read2_b32 v[10:11], v77 offset0:156 offset1:189
	ds_read2_b32 v[12:13], v77 offset0:222 offset1:255
	ds_read2_b32 v[14:15], v109 offset0:32 offset1:65
	ds_read2_b32 v[16:17], v109 offset0:98 offset1:131
	ds_read2_b32 v[18:19], v109 offset0:164 offset1:197
	ds_read2_b32 v[20:21], v111 offset0:102 offset1:135
	v_lshl_add_u64 v[2:3], v[2:3], 0, v[22:23]
	s_waitcnt vmcnt(0)
	v_div_scale_f32 v25, s[4:5], v24, v24, 1.0
	v_rcp_f32_e32 v26, v25
	v_div_scale_f32 v4, vcc, 1.0, v24, 1.0
	v_fma_f32 v5, -v25, v26, 1.0
	v_fmac_f32_e32 v26, v5, v26
	v_mul_f32_e32 v5, v4, v26
	v_fma_f32 v27, -v25, v5, v4
	v_fmac_f32_e32 v5, v27, v26
	v_fma_f32 v4, -v25, v5, v4
	v_div_fmas_f32 v4, v4, v26, v5
	v_div_fixup_f32 v4, v4, v24, 1.0
	s_waitcnt lgkmcnt(7)
	v_fmaak_f32 v5, v6, v4, 0x43000000
	v_fmaak_f32 v6, v4, v7, 0x43000000
	s_waitcnt lgkmcnt(6)
	v_fmaak_f32 v7, v4, v8, 0x43000000
	v_fmaak_f32 v8, v4, v9, 0x43000000
	s_waitcnt lgkmcnt(5)
	v_fmaak_f32 v9, v4, v10, 0x43000000
	v_fmaak_f32 v10, v4, v11, 0x43000000
	s_waitcnt lgkmcnt(4)
	v_fmaak_f32 v11, v4, v12, 0x43000000
	v_fmaak_f32 v12, v4, v13, 0x43000000
	s_waitcnt lgkmcnt(3)
	v_fmaak_f32 v13, v4, v14, 0x43000000
	v_fmaak_f32 v14, v4, v15, 0x43000000
	s_waitcnt lgkmcnt(2)
	v_fmaak_f32 v15, v4, v16, 0x43000000
	v_fmaak_f32 v16, v4, v17, 0x43000000
	s_waitcnt lgkmcnt(1)
	v_fmaak_f32 v17, v4, v18, 0x43000000
	v_fmaak_f32 v18, v4, v19, 0x43000000
	v_rndne_f32_e32 v5, v5
	v_rndne_f32_e32 v9, v9
	v_rndne_f32_e32 v13, v13
	v_rndne_f32_e32 v17, v17
	s_waitcnt lgkmcnt(0)
	v_fmaak_f32 v19, v4, v20, 0x43000000
	v_rndne_f32_e32 v6, v6
	v_rndne_f32_e32 v10, v10
	v_rndne_f32_e32 v14, v14
	v_rndne_f32_e32 v18, v18
	v_cvt_pk_u8_f32 v5, v5, 0, 0
	v_cvt_pk_u8_f32 v9, v9, 0, 0
	v_cvt_pk_u8_f32 v13, v13, 0, 0
	v_cvt_pk_u8_f32 v17, v17, 0, 0
	v_fmaak_f32 v4, v4, v21, 0x43000000
	v_rndne_f32_e32 v7, v7
	v_rndne_f32_e32 v11, v11
	v_rndne_f32_e32 v15, v15
	v_rndne_f32_e32 v19, v19
	v_cvt_pk_u8_f32 v5, v6, 1, v5
	v_cvt_pk_u8_f32 v6, v10, 1, v9
	v_cvt_pk_u8_f32 v9, v14, 1, v13
	v_cvt_pk_u8_f32 v10, v18, 1, v17
	v_rndne_f32_e32 v8, v8
	v_rndne_f32_e32 v12, v12
	v_rndne_f32_e32 v16, v16
	v_rndne_f32_e32 v4, v4
	v_cvt_pk_u8_f32 v5, v7, 2, v5
	v_cvt_pk_u8_f32 v6, v11, 2, v6
	v_cvt_pk_u8_f32 v7, v15, 2, v9
	v_cvt_pk_u8_f32 v9, v19, 2, v10
	v_cvt_pk_u8_f32 v5, v8, 3, v5
	v_cvt_pk_u8_f32 v6, v12, 3, v6
	v_cvt_pk_u8_f32 v7, v16, 3, v7
	v_cvt_pk_u8_f32 v8, v4, 3, v9
	v_xor_b32_e32 v4, 0x80808080, v5
	v_xor_b32_e32 v5, 0x80808080, v6
	v_xor_b32_e32 v6, 0x80808080, v7
	v_xor_b32_e32 v7, 0x80808080, v8
	global_store_dwordx4 v[2:3], v[4:7], off nt
	s_branch .LBB0_941

.LBB0_1253:
	s_mul_hi_i32 s6, s12, 0x3e0f83e1
	s_lshr_b32 s7, s6, 31
	s_ashr_i32 s6, s6, 11
	s_add_i32 s10, s6, s7
	s_mul_i32 s6, s10, 0xffffdf00
	s_add_i32 s11, s12, s6
	s_mul_hi_i32 s9, s10, 0xb00000
	s_mul_i32 s8, s10, 0xb00000
	s_cmpk_gt_i32 s11, 0x15ff
	s_mov_b64 s[6:7], -1
	s_cbranch_scc0 .LBB0_1255
	s_add_u32 s7, s13, s8
	s_addc_u32 s27, s14, s9
	s_mul_i32 s28, s10, 0x2c00000
	s_mul_hi_i32 s6, s10, 0x2c00000
	s_waitcnt lgkmcnt(0)
	s_add_u32 s30, s2, s28
	s_addc_u32 s31, s3, s6
	s_mul_i32 s6, s10, 0xffffbe00
	s_add_i32 s6, s21, s6
	s_and_b32 s28, s6, 0xffffff80
	s_addk_i32 s28, 0xd400
	s_and_b32 s6, s19, 0x7e0
	v_or_b32_e32 v2, s6, v72
	v_or_b32_e32 v62, s28, v73
	v_lshlrev_b32_e32 v68, 2, v2
	v_ashrrev_i32_e32 v63, 31, v62
	v_lshl_add_u64 v[64:65], s[30:31], 0, v[68:69]
	v_lshlrev_b64 v[2:3], 13, v[62:63]
	v_lshl_add_u64 v[10:11], v[64:65], 0, v[2:3]
	v_or_b32_e32 v2, 8, v62
	v_ashrrev_i32_e32 v3, 31, v2
	v_lshlrev_b64 v[2:3], 13, v[2:3]
	v_lshl_add_u64 v[12:13], v[64:65], 0, v[2:3]
	global_load_dwordx4 v[2:5], v[10:11], off nt
	global_load_dwordx4 v[6:9], v[12:13], off nt
	v_or_b32_e32 v10, 16, v62
	v_ashrrev_i32_e32 v11, 31, v10
	v_lshlrev_b64 v[10:11], 13, v[10:11]
	v_lshl_add_u64 v[18:19], v[64:65], 0, v[10:11]
	v_or_b32_e32 v10, 24, v62
	v_ashrrev_i32_e32 v11, 31, v10
	v_lshlrev_b64 v[10:11], 13, v[10:11]
	v_lshl_add_u64 v[20:21], v[64:65], 0, v[10:11]
	global_load_dwordx4 v[10:13], v[18:19], off nt
	global_load_dwordx4 v[14:17], v[20:21], off nt
	v_or_b32_e32 v18, 32, v62
	v_ashrrev_i32_e32 v19, 31, v18
	v_lshlrev_b64 v[18:19], 13, v[18:19]
	v_lshl_add_u64 v[26:27], v[64:65], 0, v[18:19]
	v_or_b32_e32 v18, 40, v62
	v_ashrrev_i32_e32 v19, 31, v18
	v_lshlrev_b64 v[18:19], 13, v[18:19]
	v_lshl_add_u64 v[28:29], v[64:65], 0, v[18:19]
	global_load_dwordx4 v[18:21], v[26:27], off nt
	global_load_dwordx4 v[22:25], v[28:29], off nt
	v_or_b32_e32 v26, 48, v62
	v_ashrrev_i32_e32 v27, 31, v26
	v_lshlrev_b64 v[26:27], 13, v[26:27]
	v_lshl_add_u64 v[34:35], v[64:65], 0, v[26:27]
	v_or_b32_e32 v26, 56, v62
	v_ashrrev_i32_e32 v27, 31, v26
	v_lshlrev_b64 v[26:27], 13, v[26:27]
	v_lshl_add_u64 v[36:37], v[64:65], 0, v[26:27]
	global_load_dwordx4 v[26:29], v[34:35], off nt
	global_load_dwordx4 v[30:33], v[36:37], off nt
	v_or_b32_e32 v34, 64, v62
	v_ashrrev_i32_e32 v35, 31, v34
	v_lshlrev_b64 v[34:35], 13, v[34:35]
	v_lshl_add_u64 v[42:43], v[64:65], 0, v[34:35]
	v_or_b32_e32 v34, 0x48, v62
	v_ashrrev_i32_e32 v35, 31, v34
	v_lshlrev_b64 v[34:35], 13, v[34:35]
	v_lshl_add_u64 v[44:45], v[64:65], 0, v[34:35]
	global_load_dwordx4 v[34:37], v[42:43], off nt
	global_load_dwordx4 v[38:41], v[44:45], off nt
	v_or_b32_e32 v42, 0x50, v62
	v_ashrrev_i32_e32 v43, 31, v42
	v_lshlrev_b64 v[42:43], 13, v[42:43]
	v_lshl_add_u64 v[50:51], v[64:65], 0, v[42:43]
	v_or_b32_e32 v42, 0x58, v62
	v_ashrrev_i32_e32 v43, 31, v42
	v_lshlrev_b64 v[42:43], 13, v[42:43]
	v_lshl_add_u64 v[52:53], v[64:65], 0, v[42:43]
	global_load_dwordx4 v[42:45], v[50:51], off nt
	global_load_dwordx4 v[46:49], v[52:53], off nt
	v_or_b32_e32 v50, 0x60, v62
	v_ashrrev_i32_e32 v51, 31, v50
	v_lshlrev_b64 v[50:51], 13, v[50:51]
	v_or_b32_e32 v54, 0x68, v62
	v_lshl_add_u64 v[50:51], v[64:65], 0, v[50:51]
	v_ashrrev_i32_e32 v55, 31, v54
	global_load_dwordx4 v[50:53], v[50:51], off nt
	v_lshlrev_b64 v[54:55], 13, v[54:55]
	v_or_b32_e32 v58, 0x70, v62
	v_lshl_add_u64 v[54:55], v[64:65], 0, v[54:55]
	v_ashrrev_i32_e32 v59, 31, v58
	global_load_dwordx4 v[54:57], v[54:55], off nt
	v_lshlrev_b64 v[58:59], 13, v[58:59]
	v_or_b32_e32 v62, 0x78, v62
	v_lshl_add_u64 v[58:59], v[64:65], 0, v[58:59]
	v_ashrrev_i32_e32 v63, 31, v62
	global_load_dwordx4 v[58:61], v[58:59], off nt
	v_lshlrev_b64 v[62:63], 13, v[62:63]
	v_lshl_add_u64 v[62:63], v[64:65], 0, v[62:63]
	global_load_dwordx4 v[62:65], v[62:63], off nt
	s_add_u32 s28, s7, s28
	s_addc_u32 s29, s27, 0
	s_waitcnt vmcnt(15)
	v_pk_mul_f32 v[2:3], v[2:3], s[4:5] op_sel_hi:[1,0]
	ds_write2_b32 v78, v2, v3 offset1:1
	v_pk_mul_f32 v[2:3], v[4:5], s[4:5] op_sel_hi:[1,0]
	ds_write2_b32 v78, v2, v3 offset0:2 offset1:3
	s_waitcnt vmcnt(14)
	v_pk_mul_f32 v[2:3], v[6:7], s[4:5] op_sel_hi:[1,0]
	ds_write2_b32 v79, v2, v3 offset1:1
	v_pk_mul_f32 v[2:3], v[8:9], s[4:5] op_sel_hi:[1,0]
	ds_write2_b32 v80, v2, v3 offset1:1
	v_mov_b32_e32 v5, v69
	s_waitcnt vmcnt(13)
	v_pk_mul_f32 v[2:3], v[10:11], s[4:5] op_sel_hi:[1,0]
	ds_write2_b32 v81, v2, v3 offset1:1
	v_pk_mul_f32 v[2:3], v[12:13], s[4:5] op_sel_hi:[1,0]
	ds_write2_b32 v82, v2, v3 offset1:1
	s_waitcnt vmcnt(12)
	v_pk_mul_f32 v[2:3], v[14:15], s[4:5] op_sel_hi:[1,0]
	ds_write2_b32 v83, v2, v3 offset1:1
	v_pk_mul_f32 v[2:3], v[16:17], s[4:5] op_sel_hi:[1,0]
	ds_write2_b32 v84, v2, v3 offset1:1
	v_lshl_add_u64 v[14:15], s[28:29], 0, v[66:67]
	s_waitcnt vmcnt(11)
	v_pk_mul_f32 v[2:3], v[18:19], s[4:5] op_sel_hi:[1,0]
	ds_write2_b32 v85, v2, v3 offset1:1
	v_pk_mul_f32 v[2:3], v[20:21], s[4:5] op_sel_hi:[1,0]
	ds_write2_b32 v86, v2, v3 offset1:1
	s_waitcnt vmcnt(10)
	v_pk_mul_f32 v[2:3], v[22:23], s[4:5] op_sel_hi:[1,0]
	ds_write2_b32 v87, v2, v3 offset1:1
	v_pk_mul_f32 v[2:3], v[24:25], s[4:5] op_sel_hi:[1,0]
	ds_write2_b32 v88, v2, v3 offset1:1
	s_waitcnt vmcnt(9)
	v_pk_mul_f32 v[2:3], v[26:27], s[4:5] op_sel_hi:[1,0]
	ds_write2_b32 v89, v2, v3 offset1:1
	v_pk_mul_f32 v[2:3], v[28:29], s[4:5] op_sel_hi:[1,0]
	ds_write2_b32 v90, v2, v3 offset1:1
	s_waitcnt vmcnt(8)
	v_pk_mul_f32 v[2:3], v[30:31], s[4:5] op_sel_hi:[1,0]
	ds_write2_b32 v91, v2, v3 offset1:1
	v_pk_mul_f32 v[2:3], v[32:33], s[4:5] op_sel_hi:[1,0]
	ds_write2_b32 v92, v2, v3 offset1:1
	s_waitcnt vmcnt(7)
	v_pk_mul_f32 v[2:3], v[34:35], s[4:5] op_sel_hi:[1,0]
	ds_write2_b32 v93, v2, v3 offset1:1
	v_pk_mul_f32 v[2:3], v[36:37], s[4:5] op_sel_hi:[1,0]
	ds_write2_b32 v94, v2, v3 offset1:1
	s_waitcnt vmcnt(6)
	v_pk_mul_f32 v[2:3], v[38:39], s[4:5] op_sel_hi:[1,0]
	ds_write2_b32 v95, v2, v3 offset1:1
	v_pk_mul_f32 v[2:3], v[40:41], s[4:5] op_sel_hi:[1,0]
	ds_write2_b32 v96, v2, v3 offset1:1
	s_waitcnt vmcnt(5)
	v_pk_mul_f32 v[2:3], v[42:43], s[4:5] op_sel_hi:[1,0]
	ds_write2_b32 v97, v2, v3 offset1:1
	v_pk_mul_f32 v[2:3], v[44:45], s[4:5] op_sel_hi:[1,0]
	ds_write2_b32 v98, v2, v3 offset1:1
	s_waitcnt vmcnt(4)
	v_pk_mul_f32 v[2:3], v[46:47], s[4:5] op_sel_hi:[1,0]
	ds_write2_b32 v99, v2, v3 offset1:1
	v_pk_mul_f32 v[2:3], v[48:49], s[4:5] op_sel_hi:[1,0]
	ds_write2_b32 v100, v2, v3 offset1:1
	s_waitcnt vmcnt(3)
	v_pk_mul_f32 v[2:3], v[50:51], s[4:5] op_sel_hi:[1,0]
	ds_write2_b32 v101, v2, v3 offset1:1
	v_pk_mul_f32 v[2:3], v[52:53], s[4:5] op_sel_hi:[1,0]
	ds_write2_b32 v102, v2, v3 offset1:1
	s_waitcnt vmcnt(2)
	v_pk_mul_f32 v[2:3], v[54:55], s[4:5] op_sel_hi:[1,0]
	ds_write2_b32 v103, v2, v3 offset1:1
	v_pk_mul_f32 v[2:3], v[56:57], s[4:5] op_sel_hi:[1,0]
	ds_write2_b32 v104, v2, v3 offset1:1
	s_waitcnt vmcnt(1)
	v_pk_mul_f32 v[2:3], v[58:59], s[4:5] op_sel_hi:[1,0]
	ds_write2_b32 v105, v2, v3 offset1:1
	v_pk_mul_f32 v[2:3], v[60:61], s[4:5] op_sel_hi:[1,0]
	ds_write2_b32 v106, v2, v3 offset1:1
	s_waitcnt vmcnt(0)
	v_pk_mul_f32 v[2:3], v[62:63], s[4:5] op_sel_hi:[1,0]
	ds_write2_b32 v107, v2, v3 offset1:1
	v_pk_mul_f32 v[2:3], v[64:65], s[4:5] op_sel_hi:[1,0]
	ds_write2_b32 v108, v2, v3 offset1:1
	s_waitcnt lgkmcnt(0)
	ds_read2_b32 v[6:7], v109 offset0:206 offset1:214
	ds_read2_b32 v[8:9], v109 offset0:239 offset1:247
	ds_read2_b32 v[10:11], v109 offset0:140 offset1:148
	ds_read2_b32 v[12:13], v109 offset0:173 offset1:181
	ds_read2_b32 v[16:17], v109 offset0:74 offset1:82
	ds_read2_b32 v[18:19], v109 offset0:107 offset1:115
	ds_read2_b32 v[20:21], v109 offset0:8 offset1:16
	ds_read2_b32 v[22:23], v109 offset0:41 offset1:49
	s_waitcnt lgkmcnt(7)
	v_med3_f32 v2, v6, s23, v110
	s_waitcnt lgkmcnt(6)
	v_med3_f32 v3, v8, s23, v110
	s_waitcnt lgkmcnt(5)
	v_med3_f32 v4, v10, s23, v110
	s_waitcnt lgkmcnt(4)
	v_med3_f32 v6, v12, s23, v110
	v_cvt_pk_fp8_f32 v5, v4, v6
	s_waitcnt lgkmcnt(1)
	v_med3_f32 v6, v20, s23, v110
	s_waitcnt lgkmcnt(0)
	v_med3_f32 v8, v22, s23, v110
	v_mov_b32_e32 v4, v69
	ds_read2_b32 v[24:25], v77 offset0:198 offset1:206
	ds_read2_b32 v[26:27], v77 offset0:231 offset1:239
	ds_read2_b32 v[28:29], v77 offset0:132 offset1:140
	ds_read2_b32 v[30:31], v77 offset0:165 offset1:173
	v_cvt_pk_fp8_f32 v4, v6, v8
	ds_read2_b32 v[32:33], v77 offset1:8
	ds_read2_b32 v[34:35], v77 offset0:33 offset1:41
	v_cvt_pk_fp8_f32 v5, v2, v3 op_sel:[0,0,1]
	v_med3_f32 v2, v16, s23, v110
	v_med3_f32 v3, v18, s23, v110
	v_cvt_pk_fp8_f32 v4, v2, v3 op_sel:[0,0,1]
	s_waitcnt lgkmcnt(3)
	v_med3_f32 v2, v28, s23, v110
	s_waitcnt lgkmcnt(2)
	v_med3_f32 v10, v30, s23, v110
	v_mov_b32_e32 v3, v69
	ds_read2_b32 v[36:37], v77 offset0:66 offset1:74
	ds_read2_b32 v[38:39], v77 offset0:99 offset1:107
	v_cvt_pk_fp8_f32 v3, v2, v10
	s_waitcnt lgkmcnt(3)
	v_med3_f32 v10, v32, s23, v110
	s_waitcnt lgkmcnt(2)
	v_med3_f32 v12, v34, s23, v110
	v_mov_b32_e32 v2, v69
	v_cvt_pk_fp8_f32 v2, v10, v12
	v_med3_f32 v6, v24, s23, v110
	v_med3_f32 v8, v26, s23, v110
	v_cvt_pk_fp8_f32 v3, v6, v8 op_sel:[0,0,1]
	s_waitcnt lgkmcnt(1)
	v_med3_f32 v6, v36, s23, v110
	s_waitcnt lgkmcnt(0)
	v_med3_f32 v8, v38, s23, v110
	v_cvt_pk_fp8_f32 v2, v6, v8 op_sel:[0,0,1]
	v_or_b32_e32 v6, s6, v73
	v_mul_u32_u24_e32 v68, 0x1600, v6
	v_lshl_add_u64 v[40:41], v[14:15], 0, v[68:69]
	global_store_dwordx4 v[40:41], v[2:5], off nt
	v_med3_f32 v8, v23, s23, v110
	v_med3_f32 v10, v35, s23, v110
	v_med3_f32 v2, v7, s23, v110
	v_med3_f32 v4, v11, s23, v110
	v_med3_f32 v7, v13, s23, v110
	v_mov_b32_e32 v5, v69
	v_cvt_pk_fp8_f32 v5, v4, v7
	v_med3_f32 v7, v21, s23, v110
	v_mov_b32_e32 v4, v69
	v_cvt_pk_fp8_f32 v4, v7, v8
	v_med3_f32 v3, v9, s23, v110
	v_cvt_pk_fp8_f32 v5, v2, v3 op_sel:[0,0,1]
	v_med3_f32 v2, v17, s23, v110
	v_med3_f32 v3, v19, s23, v110
	v_cvt_pk_fp8_f32 v4, v2, v3 op_sel:[0,0,1]
	v_med3_f32 v2, v29, s23, v110
	v_med3_f32 v9, v31, s23, v110
	v_mov_b32_e32 v3, v69
	v_cvt_pk_fp8_f32 v3, v2, v9
	v_med3_f32 v9, v33, s23, v110
	v_mov_b32_e32 v2, v69
	v_cvt_pk_fp8_f32 v2, v9, v10
	v_med3_f32 v7, v25, s23, v110
	v_med3_f32 v8, v27, s23, v110
	v_cvt_pk_fp8_f32 v3, v7, v8 op_sel:[0,0,1]
	v_med3_f32 v7, v37, s23, v110
	v_med3_f32 v8, v39, s23, v110
	v_cvt_pk_fp8_f32 v2, v7, v8 op_sel:[0,0,1]
	ds_read2_b32 v[8:9], v109 offset0:222 offset1:230
	ds_read2_b32 v[10:11], v111 offset0:127 offset1:135
	ds_read2_b32 v[12:13], v109 offset0:156 offset1:164
	ds_read2_b32 v[16:17], v109 offset0:189 offset1:197
	v_or_b32_e32 v6, s6, v74
	v_mul_u32_u24_e32 v68, 0x1600, v6
	v_lshl_add_u64 v[6:7], v[14:15], 0, v[68:69]
	global_store_dwordx4 v[6:7], v[2:5], off nt
	s_waitcnt lgkmcnt(0)
	v_med3_f32 v6, v16, s23, v110
	v_med3_f32 v4, v12, s23, v110
	v_mov_b32_e32 v5, v69
	v_cvt_pk_fp8_f32 v5, v4, v6
	ds_read2_b32 v[6:7], v109 offset0:90 offset1:98
	ds_read2_b32 v[18:19], v109 offset0:123 offset1:131
	ds_read2_b32 v[20:21], v109 offset0:24 offset1:32
	ds_read2_b32 v[22:23], v109 offset0:57 offset1:65
	v_med3_f32 v2, v8, s23, v110
	v_med3_f32 v3, v10, s23, v110
	v_cvt_pk_fp8_f32 v5, v2, v3 op_sel:[0,0,1]
	s_waitcnt lgkmcnt(3)
	v_med3_f32 v2, v6, s23, v110
	s_waitcnt lgkmcnt(1)
	v_med3_f32 v6, v20, s23, v110
	s_waitcnt lgkmcnt(0)
	v_med3_f32 v8, v22, s23, v110
	v_mov_b32_e32 v4, v69
	ds_read2_b32 v[24:25], v77 offset0:214 offset1:222
	ds_read2_b32 v[26:27], v77 offset0:247 offset1:255
	ds_read2_b32 v[28:29], v77 offset0:148 offset1:156
	ds_read2_b32 v[30:31], v77 offset0:181 offset1:189
	v_cvt_pk_fp8_f32 v4, v6, v8
	ds_read2_b32 v[32:33], v77 offset0:16 offset1:24
	ds_read2_b32 v[34:35], v77 offset0:49 offset1:57
	v_med3_f32 v3, v18, s23, v110
	ds_read2_b32 v[36:37], v77 offset0:82 offset1:90
	ds_read2_b32 v[38:39], v77 offset0:115 offset1:123
	v_cvt_pk_fp8_f32 v4, v2, v3 op_sel:[0,0,1]
	s_waitcnt lgkmcnt(5)
	v_med3_f32 v2, v28, s23, v110
	s_waitcnt lgkmcnt(4)
	v_med3_f32 v10, v30, s23, v110
	v_mov_b32_e32 v3, v69
	v_cvt_pk_fp8_f32 v3, v2, v10
	s_waitcnt lgkmcnt(3)
	v_med3_f32 v10, v32, s23, v110
	s_waitcnt lgkmcnt(2)
	v_med3_f32 v12, v34, s23, v110
	v_mov_b32_e32 v2, v69
	v_cvt_pk_fp8_f32 v2, v10, v12
	v_med3_f32 v6, v24, s23, v110
	v_med3_f32 v8, v26, s23, v110
	v_cvt_pk_fp8_f32 v3, v6, v8 op_sel:[0,0,1]
	s_waitcnt lgkmcnt(1)
	v_med3_f32 v6, v36, s23, v110
	s_waitcnt lgkmcnt(0)
	v_med3_f32 v8, v38, s23, v110
	v_cvt_pk_fp8_f32 v2, v6, v8 op_sel:[0,0,1]
	v_or_b32_e32 v6, s6, v75
	v_mul_u32_u24_e32 v68, 0x1600, v6
	v_lshl_add_u64 v[40:41], v[14:15], 0, v[68:69]
	global_store_dwordx4 v[40:41], v[2:5], off nt
	v_med3_f32 v6, v17, s23, v110
	v_med3_f32 v8, v23, s23, v110
	v_med3_f32 v4, v13, s23, v110
	v_mov_b32_e32 v5, v69
	v_cvt_pk_fp8_f32 v5, v4, v6
	v_med3_f32 v6, v21, s23, v110
	v_mov_b32_e32 v4, v69
	v_cvt_pk_fp8_f32 v4, v6, v8
	v_med3_f32 v2, v9, s23, v110
	v_med3_f32 v3, v11, s23, v110
	v_cvt_pk_fp8_f32 v5, v2, v3 op_sel:[0,0,1]
	v_med3_f32 v2, v7, s23, v110
	v_med3_f32 v3, v19, s23, v110
	v_cvt_pk_fp8_f32 v4, v2, v3 op_sel:[0,0,1]
	v_med3_f32 v2, v29, s23, v110
	v_med3_f32 v8, v31, s23, v110
	v_mov_b32_e32 v3, v69
	v_cvt_pk_fp8_f32 v3, v2, v8
	v_med3_f32 v8, v33, s23, v110
	v_med3_f32 v9, v35, s23, v110
	v_mov_b32_e32 v2, v69
	v_cvt_pk_fp8_f32 v2, v8, v9
	v_med3_f32 v6, v25, s23, v110
	v_med3_f32 v7, v27, s23, v110
	v_cvt_pk_fp8_f32 v3, v6, v7 op_sel:[0,0,1]
	v_med3_f32 v6, v37, s23, v110
	v_med3_f32 v7, v39, s23, v110
	v_cvt_pk_fp8_f32 v2, v6, v7 op_sel:[0,0,1]
	v_or_b32_e32 v6, s6, v76
	v_mul_u32_u24_e32 v68, 0x1600, v6
	v_lshl_add_u64 v[6:7], v[14:15], 0, v[68:69]
	global_store_dwordx4 v[6:7], v[2:5], off nt
	s_waitcnt lgkmcnt(0)
	s_mov_b64 s[6:7], 0
.LBB0_1255:
	s_andn2_b64 vcc, exec, s[6:7]
	s_cbranch_vccnz .LBB0_1252
	s_cmpk_gt_i32 s11, 0xaff
	s_cselect_b64 s[6:7], -1, 0
	s_and_b64 s[28:29], s[6:7], exec
	s_cselect_b32 s11, 0xfffff500, 0
	s_mul_i32 s27, s10, 0x2100
	s_cselect_b32 s28, s25, 0xe0
	s_sub_i32 s11, s11, s27
	s_add_i32 s11, s12, s11
	s_add_u32 s28, s74, s28
	s_addc_u32 s29, s75, 0
	s_load_dwordx2 s[28:29], s[28:29], 0x0
	s_lshl_b64 s[8:9], s[8:9], 2
	s_mul_hi_i32 s27, s11, 0x2e8ba2e9
	v_mov_b32_e32 v6, 0
	v_mov_b32_e32 v7, 0
	s_waitcnt lgkmcnt(0)
	s_add_u32 s8, s28, s8
	s_addc_u32 s9, s29, s9
	s_lshr_b32 s28, s27, 31
	s_ashr_i32 s27, s27, 5
	s_add_i32 s28, s27, s28
	s_mul_i32 s27, s28, 0xb0
	s_sub_i32 s27, s11, s27
	s_lshl_b32 s11, s28, 7
	s_lshl_b32 s28, s27, 5
	v_or_b32_e32 v2, s28, v72
	v_ashrrev_i32_e32 v3, 31, v2
	v_cmp_gt_i32_e32 vcc, s24, v2
	v_or_b32_e32 v68, s11, v73
	v_lshl_add_u64 v[70:71], v[2:3], 2, s[8:9]
	v_mov_b32_e32 v2, 0
	v_mov_b32_e32 v8, 0
	v_mov_b32_e32 v9, 0
	s_and_saveexec_b64 s[8:9], vcc
	s_cbranch_execz .LBB0_1258
	v_mad_i64_i32 v[4:5], s[30:31], v68, s26, v[70:71]
	global_load_dwordx4 v[6:9], v[4:5], off nt
.LBB0_1258:
	s_or_b64 exec, exec, s[8:9]
	v_mov_b32_e32 v3, 0
	v_mov_b32_e32 v4, 0
	v_mov_b32_e32 v5, 0
	s_and_saveexec_b64 s[8:9], vcc
	s_cbranch_execz .LBB0_1260
	v_or_b32_e32 v2, 8, v68
	v_mad_i64_i32 v[2:3], s[30:31], v2, s26, v[70:71]
	global_load_dwordx4 v[2:5], v[2:3], off nt
.LBB0_1260:
	s_or_b64 exec, exec, s[8:9]
	v_mov_b32_e32 v10, 0
	v_mov_b32_e32 v14, 0
	v_mov_b32_e32 v15, 0
	v_mov_b32_e32 v16, 0
	v_mov_b32_e32 v17, 0
	s_and_saveexec_b64 s[8:9], vcc
	s_cbranch_execz .LBB0_1262
	v_or_b32_e32 v11, 16, v68
	v_mad_i64_i32 v[12:13], s[30:31], v11, s26, v[70:71]
	global_load_dwordx4 v[14:17], v[12:13], off nt
.LBB0_1262:
	s_or_b64 exec, exec, s[8:9]
	v_mov_b32_e32 v11, 0
	v_mov_b32_e32 v12, 0
	v_mov_b32_e32 v13, 0
	s_and_saveexec_b64 s[8:9], vcc
	s_cbranch_execz .LBB0_1264
	v_or_b32_e32 v10, 24, v68
	v_mad_i64_i32 v[10:11], s[30:31], v10, s26, v[70:71]
	global_load_dwordx4 v[10:13], v[10:11], off nt
.LBB0_1264:
	s_or_b64 exec, exec, s[8:9]
	v_mov_b32_e32 v18, 0
	v_mov_b32_e32 v22, 0
	v_mov_b32_e32 v23, 0
	v_mov_b32_e32 v24, 0
	v_mov_b32_e32 v25, 0
	s_and_saveexec_b64 s[8:9], vcc
	s_cbranch_execz .LBB0_1266
	v_or_b32_e32 v19, 32, v68
	v_mad_i64_i32 v[20:21], s[30:31], v19, s26, v[70:71]
	global_load_dwordx4 v[22:25], v[20:21], off nt
.LBB0_1266:
	s_or_b64 exec, exec, s[8:9]
	v_mov_b32_e32 v19, 0
	v_mov_b32_e32 v20, 0
	v_mov_b32_e32 v21, 0
	s_and_saveexec_b64 s[8:9], vcc
	s_cbranch_execz .LBB0_1268
	v_or_b32_e32 v18, 40, v68
	v_mad_i64_i32 v[18:19], s[30:31], v18, s26, v[70:71]
	global_load_dwordx4 v[18:21], v[18:19], off nt
.LBB0_1268:
	s_or_b64 exec, exec, s[8:9]
	v_mov_b32_e32 v26, 0
	v_mov_b32_e32 v30, 0
	v_mov_b32_e32 v31, 0
	v_mov_b32_e32 v32, 0
	v_mov_b32_e32 v33, 0
	s_and_saveexec_b64 s[8:9], vcc
	s_cbranch_execz .LBB0_1270
	v_or_b32_e32 v27, 48, v68
	v_mad_i64_i32 v[28:29], s[30:31], v27, s26, v[70:71]
	global_load_dwordx4 v[30:33], v[28:29], off nt
.LBB0_1270:
	s_or_b64 exec, exec, s[8:9]
	v_mov_b32_e32 v27, 0
	v_mov_b32_e32 v28, 0
	v_mov_b32_e32 v29, 0
	s_and_saveexec_b64 s[8:9], vcc
	s_cbranch_execz .LBB0_1272
	v_or_b32_e32 v26, 56, v68
	v_mad_i64_i32 v[26:27], s[30:31], v26, s26, v[70:71]
	global_load_dwordx4 v[26:29], v[26:27], off nt
.LBB0_1272:
	s_or_b64 exec, exec, s[8:9]
	v_mov_b32_e32 v34, 0
	v_mov_b32_e32 v38, 0
	v_mov_b32_e32 v39, 0
	v_mov_b32_e32 v40, 0
	v_mov_b32_e32 v41, 0
	s_and_saveexec_b64 s[8:9], vcc
	s_cbranch_execz .LBB0_1274
	v_or_b32_e32 v35, 64, v68
	v_mad_i64_i32 v[36:37], s[30:31], v35, s26, v[70:71]
	global_load_dwordx4 v[38:41], v[36:37], off nt
.LBB0_1274:
	s_or_b64 exec, exec, s[8:9]
	v_mov_b32_e32 v35, 0
	v_mov_b32_e32 v36, 0
	v_mov_b32_e32 v37, 0
	s_and_saveexec_b64 s[8:9], vcc
	s_cbranch_execz .LBB0_1276
	v_or_b32_e32 v34, 0x48, v68
	v_mad_i64_i32 v[34:35], s[30:31], v34, s26, v[70:71]
	global_load_dwordx4 v[34:37], v[34:35], off nt
.LBB0_1276:
	s_or_b64 exec, exec, s[8:9]
	v_mov_b32_e32 v42, 0
	v_mov_b32_e32 v46, 0
	v_mov_b32_e32 v47, 0
	v_mov_b32_e32 v48, 0
	v_mov_b32_e32 v49, 0
	s_and_saveexec_b64 s[8:9], vcc
	s_cbranch_execz .LBB0_1278
	v_or_b32_e32 v43, 0x50, v68
	v_mad_i64_i32 v[44:45], s[30:31], v43, s26, v[70:71]
	global_load_dwordx4 v[46:49], v[44:45], off nt
.LBB0_1278:
	s_or_b64 exec, exec, s[8:9]
	v_mov_b32_e32 v43, 0
	v_mov_b32_e32 v44, 0
	v_mov_b32_e32 v45, 0
	s_and_saveexec_b64 s[8:9], vcc
	s_cbranch_execz .LBB0_1280
	v_or_b32_e32 v42, 0x58, v68
	v_mad_i64_i32 v[42:43], s[30:31], v42, s26, v[70:71]
	global_load_dwordx4 v[42:45], v[42:43], off nt
.LBB0_1280:
	s_or_b64 exec, exec, s[8:9]
	v_mov_b32_e32 v50, 0
	v_mov_b32_e32 v54, 0
	v_mov_b32_e32 v55, 0
	v_mov_b32_e32 v56, 0
	v_mov_b32_e32 v57, 0
	s_and_saveexec_b64 s[8:9], vcc
	s_cbranch_execz .LBB0_1282
	v_or_b32_e32 v51, 0x60, v68
	v_mad_i64_i32 v[52:53], s[30:31], v51, s26, v[70:71]
	global_load_dwordx4 v[54:57], v[52:53], off nt
.LBB0_1282:
	s_or_b64 exec, exec, s[8:9]
	v_mov_b32_e32 v51, 0
	v_mov_b32_e32 v52, 0
	v_mov_b32_e32 v53, 0
	s_and_saveexec_b64 s[8:9], vcc
	s_cbranch_execz .LBB0_1284
	v_or_b32_e32 v50, 0x68, v68
	v_mad_i64_i32 v[50:51], s[30:31], v50, s26, v[70:71]
	global_load_dwordx4 v[50:53], v[50:51], off nt
.LBB0_1284:
	s_or_b64 exec, exec, s[8:9]
	v_mov_b32_e32 v58, 0
	v_mov_b32_e32 v62, 0
	v_mov_b32_e32 v63, 0
	v_mov_b32_e32 v64, 0
	v_mov_b32_e32 v65, 0
	s_and_saveexec_b64 s[8:9], vcc
	s_cbranch_execz .LBB0_1286
	v_or_b32_e32 v59, 0x70, v68
	v_mad_i64_i32 v[60:61], s[30:31], v59, s26, v[70:71]
	global_load_dwordx4 v[62:65], v[60:61], off nt
.LBB0_1286:
	s_or_b64 exec, exec, s[8:9]
	v_mov_b32_e32 v59, 0
	v_mov_b32_e32 v60, 0
	v_mov_b32_e32 v61, 0
	s_and_saveexec_b64 s[8:9], vcc
	s_cbranch_execz .LBB0_1288
	v_or_b32_e32 v58, 0x78, v68
	v_mad_i64_i32 v[58:59], s[30:31], v58, s26, v[70:71]
	global_load_dwordx4 v[58:61], v[58:59], off nt
.LBB0_1288:
	s_or_b64 exec, exec, s[8:9]
	s_mul_i32 s9, s10, 0x1600000
	s_mul_hi_i32 s8, s10, 0x1600000
	s_add_u32 s29, s15, s9
	s_addc_u32 s30, s16, s8
	s_mul_i32 s8, s10, 0x2c00
	s_ashr_i32 s9, s8, 31
	s_lshl_b64 s[8:9], s[8:9], 2
	s_add_u32 s8, s17, s8
	s_waitcnt vmcnt(0)
	ds_write2_b32 v78, v6, v7 offset1:1
	ds_write2_b32 v78, v8, v9 offset0:2 offset1:3
	ds_write2_b32 v79, v2, v3 offset1:1
	ds_write2_b32 v80, v4, v5 offset1:1
	ds_write2_b32 v81, v14, v15 offset1:1
	ds_write2_b32 v82, v16, v17 offset1:1
	ds_write2_b32 v83, v10, v11 offset1:1
	ds_write2_b32 v84, v12, v13 offset1:1
	ds_write2_b32 v85, v22, v23 offset1:1
	ds_write2_b32 v86, v24, v25 offset1:1
	ds_write2_b32 v87, v18, v19 offset1:1
	ds_write2_b32 v88, v20, v21 offset1:1
	ds_write2_b32 v89, v30, v31 offset1:1
	ds_write2_b32 v90, v32, v33 offset1:1
	ds_write2_b32 v91, v26, v27 offset1:1
	ds_write2_b32 v92, v28, v29 offset1:1
	ds_write2_b32 v93, v38, v39 offset1:1
	ds_write2_b32 v94, v40, v41 offset1:1
	ds_write2_b32 v95, v34, v35 offset1:1
	ds_write2_b32 v96, v36, v37 offset1:1
	ds_write2_b32 v97, v46, v47 offset1:1
	ds_write2_b32 v98, v48, v49 offset1:1
	ds_write2_b32 v99, v42, v43 offset1:1
	ds_write2_b32 v100, v44, v45 offset1:1
	ds_write2_b32 v101, v54, v55 offset1:1
	ds_write2_b32 v102, v56, v57 offset1:1
	ds_write2_b32 v103, v50, v51 offset1:1
	ds_write2_b32 v104, v52, v53 offset1:1
	ds_write2_b32 v105, v62, v63 offset1:1
	ds_write2_b32 v106, v64, v65 offset1:1
	ds_write2_b32 v107, v58, v59 offset1:1
	ds_write2_b32 v108, v60, v61 offset1:1
	s_addc_u32 s9, s18, s9
	s_waitcnt lgkmcnt(0)
	s_ashr_i32 s31, s11, 31
	s_add_u32 s10, s29, s11
	s_addc_u32 s11, s30, s31
	v_or_b32_e32 v4, s28, v73
	v_lshl_add_u64 v[2:3], s[10:11], 0, v[66:67]
	v_cmp_gt_i32_e32 vcc, s24, v4
	s_and_saveexec_b64 s[10:11], vcc
	s_cbranch_execz .LBB0_1290
	s_lshl_b32 s29, s27, 6
	s_and_b32 s29, s29, 0xffffff00
	v_and_b32_e32 v4, 0x67, v4
	v_or_b32_e32 v4, s29, v4
	v_or_b32_e32 v5, 0x80, v4
	v_cndmask_b32_e64 v4, v4, v5, s[6:7]
	v_ashrrev_i32_e32 v5, 31, v4
	v_lshl_add_u64 v[6:7], v[4:5], 2, s[8:9]
	global_load_dword v24, v[6:7], off
	v_lshlrev_b64 v[22:23], 11, v[4:5]
	ds_read2_b32 v[6:7], v77 offset1:33
	ds_read2_b32 v[8:9], v77 offset0:66 offset1:99
	ds_read2_b32 v[10:11], v77 offset0:132 offset1:165
	ds_read2_b32 v[12:13], v77 offset0:198 offset1:231
	ds_read2_b32 v[14:15], v109 offset0:8 offset1:41
	ds_read2_b32 v[16:17], v109 offset0:74 offset1:107
	ds_read2_b32 v[18:19], v109 offset0:140 offset1:173
	ds_read2_b32 v[20:21], v109 offset0:206 offset1:239
	s_waitcnt vmcnt(0)
	v_div_scale_f32 v25, s[30:31], v24, v24, 1.0
	v_rcp_f32_e32 v26, v25
	v_div_scale_f32 v4, vcc, 1.0, v24, 1.0
	v_fma_f32 v5, -v25, v26, 1.0
	v_fmac_f32_e32 v26, v5, v26
	v_mul_f32_e32 v5, v4, v26
	v_fma_f32 v27, -v25, v5, v4
	v_fmac_f32_e32 v5, v27, v26
	v_fma_f32 v4, -v25, v5, v4
	v_div_fmas_f32 v4, v4, v26, v5
	v_div_fixup_f32 v4, v4, v24, 1.0
	s_waitcnt lgkmcnt(7)
	v_fmaak_f32 v5, v6, v4, 0x43000000
	v_fmaak_f32 v6, v4, v7, 0x43000000
	s_waitcnt lgkmcnt(6)
	v_fmaak_f32 v7, v4, v8, 0x43000000
	v_fmaak_f32 v8, v4, v9, 0x43000000
	s_waitcnt lgkmcnt(5)
	v_fmaak_f32 v9, v4, v10, 0x43000000
	v_fmaak_f32 v10, v4, v11, 0x43000000
	s_waitcnt lgkmcnt(4)
	v_fmaak_f32 v11, v4, v12, 0x43000000
	v_fmaak_f32 v12, v4, v13, 0x43000000
	s_waitcnt lgkmcnt(3)
	v_fmaak_f32 v13, v4, v14, 0x43000000
	v_fmaak_f32 v14, v4, v15, 0x43000000
	s_waitcnt lgkmcnt(2)
	v_fmaak_f32 v15, v4, v16, 0x43000000
	v_fmaak_f32 v16, v4, v17, 0x43000000
	s_waitcnt lgkmcnt(1)
	v_fmaak_f32 v17, v4, v18, 0x43000000
	v_fmaak_f32 v18, v4, v19, 0x43000000
	v_rndne_f32_e32 v5, v5
	v_rndne_f32_e32 v9, v9
	v_rndne_f32_e32 v13, v13
	v_rndne_f32_e32 v17, v17
	s_waitcnt lgkmcnt(0)
	v_fmaak_f32 v19, v4, v20, 0x43000000
	v_rndne_f32_e32 v6, v6
	v_rndne_f32_e32 v10, v10
	v_rndne_f32_e32 v14, v14
	v_rndne_f32_e32 v18, v18
	v_cvt_pk_u8_f32 v5, v5, 0, 0
	v_cvt_pk_u8_f32 v9, v9, 0, 0
	v_cvt_pk_u8_f32 v13, v13, 0, 0
	v_cvt_pk_u8_f32 v17, v17, 0, 0
	v_fmaak_f32 v4, v4, v21, 0x43000000
	v_rndne_f32_e32 v7, v7
	v_rndne_f32_e32 v11, v11
	v_rndne_f32_e32 v15, v15
	v_rndne_f32_e32 v19, v19
	v_cvt_pk_u8_f32 v5, v6, 1, v5
	v_cvt_pk_u8_f32 v6, v10, 1, v9
	v_cvt_pk_u8_f32 v9, v14, 1, v13
	v_cvt_pk_u8_f32 v10, v18, 1, v17
	v_rndne_f32_e32 v8, v8
	v_rndne_f32_e32 v12, v12
	v_rndne_f32_e32 v16, v16
	v_rndne_f32_e32 v4, v4
	v_cvt_pk_u8_f32 v5, v7, 2, v5
	v_cvt_pk_u8_f32 v6, v11, 2, v6
	v_cvt_pk_u8_f32 v7, v15, 2, v9
	v_cvt_pk_u8_f32 v9, v19, 2, v10
	v_cvt_pk_u8_f32 v5, v8, 3, v5
	v_cvt_pk_u8_f32 v6, v12, 3, v6
	v_cvt_pk_u8_f32 v7, v16, 3, v7
	v_cvt_pk_u8_f32 v8, v4, 3, v9
	v_xor_b32_e32 v4, 0x80808080, v5
	v_xor_b32_e32 v5, 0x80808080, v6
	v_xor_b32_e32 v6, 0x80808080, v7
	v_xor_b32_e32 v7, 0x80808080, v8
	v_lshl_add_u64 v[8:9], v[2:3], 0, v[22:23]
	global_store_dwordx4 v[8:9], v[4:7], off nt
.LBB0_1290:
	s_or_b64 exec, exec, s[10:11]
	s_nop 0
	v_or_b32_e32 v4, s28, v74
	v_cmp_gt_i32_e32 vcc, s24, v4
	s_and_saveexec_b64 s[10:11], vcc
	s_cbranch_execz .LBB0_1292
	s_lshl_b32 s29, s27, 6
	s_and_b32 s29, s29, 0xffffff00
	v_and_b32_e32 v4, 0x6f, v4
	v_or_b32_e32 v4, s29, v4
	v_or_b32_e32 v5, 0x80, v4
	v_cndmask_b32_e64 v4, v4, v5, s[6:7]
	v_ashrrev_i32_e32 v5, 31, v4
	v_lshl_add_u64 v[6:7], v[4:5], 2, s[8:9]
	global_load_dword v24, v[6:7], off
	v_lshlrev_b64 v[22:23], 11, v[4:5]
	ds_read2_b32 v[6:7], v77 offset0:8 offset1:41
	ds_read2_b32 v[8:9], v77 offset0:74 offset1:107
	ds_read2_b32 v[10:11], v77 offset0:140 offset1:173
	ds_read2_b32 v[12:13], v77 offset0:206 offset1:239
	ds_read2_b32 v[14:15], v109 offset0:16 offset1:49
	ds_read2_b32 v[16:17], v109 offset0:82 offset1:115
	ds_read2_b32 v[18:19], v109 offset0:148 offset1:181
	ds_read2_b32 v[20:21], v109 offset0:214 offset1:247
	s_waitcnt vmcnt(0)
	v_div_scale_f32 v25, s[30:31], v24, v24, 1.0
	v_rcp_f32_e32 v26, v25
	v_div_scale_f32 v4, vcc, 1.0, v24, 1.0
	v_fma_f32 v5, -v25, v26, 1.0
	v_fmac_f32_e32 v26, v5, v26
	v_mul_f32_e32 v5, v4, v26
	v_fma_f32 v27, -v25, v5, v4
	v_fmac_f32_e32 v5, v27, v26
	v_fma_f32 v4, -v25, v5, v4
	v_div_fmas_f32 v4, v4, v26, v5
	v_div_fixup_f32 v4, v4, v24, 1.0
	s_waitcnt lgkmcnt(7)
	v_fmaak_f32 v5, v6, v4, 0x43000000
	v_fmaak_f32 v6, v4, v7, 0x43000000
	s_waitcnt lgkmcnt(6)
	v_fmaak_f32 v7, v4, v8, 0x43000000
	v_fmaak_f32 v8, v4, v9, 0x43000000
	s_waitcnt lgkmcnt(5)
	v_fmaak_f32 v9, v4, v10, 0x43000000
	v_fmaak_f32 v10, v4, v11, 0x43000000
	s_waitcnt lgkmcnt(4)
	v_fmaak_f32 v11, v4, v12, 0x43000000
	v_fmaak_f32 v12, v4, v13, 0x43000000
	s_waitcnt lgkmcnt(3)
	v_fmaak_f32 v13, v4, v14, 0x43000000
	v_fmaak_f32 v14, v4, v15, 0x43000000
	s_waitcnt lgkmcnt(2)
	v_fmaak_f32 v15, v4, v16, 0x43000000
	v_fmaak_f32 v16, v4, v17, 0x43000000
	s_waitcnt lgkmcnt(1)
	v_fmaak_f32 v17, v4, v18, 0x43000000
	v_fmaak_f32 v18, v4, v19, 0x43000000
	v_rndne_f32_e32 v5, v5
	v_rndne_f32_e32 v9, v9
	v_rndne_f32_e32 v13, v13
	v_rndne_f32_e32 v17, v17
	s_waitcnt lgkmcnt(0)
	v_fmaak_f32 v19, v4, v20, 0x43000000
	v_rndne_f32_e32 v6, v6
	v_rndne_f32_e32 v10, v10
	v_rndne_f32_e32 v14, v14
	v_rndne_f32_e32 v18, v18
	v_cvt_pk_u8_f32 v5, v5, 0, 0
	v_cvt_pk_u8_f32 v9, v9, 0, 0
	v_cvt_pk_u8_f32 v13, v13, 0, 0
	v_cvt_pk_u8_f32 v17, v17, 0, 0
	v_fmaak_f32 v4, v4, v21, 0x43000000
	v_rndne_f32_e32 v7, v7
	v_rndne_f32_e32 v11, v11
	v_rndne_f32_e32 v15, v15
	v_rndne_f32_e32 v19, v19
	v_cvt_pk_u8_f32 v5, v6, 1, v5
	v_cvt_pk_u8_f32 v6, v10, 1, v9
	v_cvt_pk_u8_f32 v9, v14, 1, v13
	v_cvt_pk_u8_f32 v10, v18, 1, v17
	v_rndne_f32_e32 v8, v8
	v_rndne_f32_e32 v12, v12
	v_rndne_f32_e32 v16, v16
	v_rndne_f32_e32 v4, v4
	v_cvt_pk_u8_f32 v5, v7, 2, v5
	v_cvt_pk_u8_f32 v6, v11, 2, v6
	v_cvt_pk_u8_f32 v7, v15, 2, v9
	v_cvt_pk_u8_f32 v9, v19, 2, v10
	v_cvt_pk_u8_f32 v5, v8, 3, v5
	v_cvt_pk_u8_f32 v6, v12, 3, v6
	v_cvt_pk_u8_f32 v7, v16, 3, v7
	v_cvt_pk_u8_f32 v8, v4, 3, v9
	v_xor_b32_e32 v4, 0x80808080, v5
	v_xor_b32_e32 v5, 0x80808080, v6
	v_xor_b32_e32 v6, 0x80808080, v7
	v_xor_b32_e32 v7, 0x80808080, v8
	v_lshl_add_u64 v[8:9], v[2:3], 0, v[22:23]
	global_store_dwordx4 v[8:9], v[4:7], off nt
.LBB0_1292:
	s_or_b64 exec, exec, s[10:11]
	s_nop 0
	v_or_b32_e32 v4, s28, v75
	v_cmp_gt_i32_e32 vcc, s24, v4
	s_and_saveexec_b64 s[10:11], vcc
	s_cbranch_execz .LBB0_1294
	s_lshl_b32 s29, s27, 6
	s_and_b32 s29, s29, 0xffffff00
	v_and_b32_e32 v4, 0x77, v4
	v_or_b32_e32 v4, s29, v4
	v_or_b32_e32 v5, 0x80, v4
	v_cndmask_b32_e64 v4, v4, v5, s[6:7]
	v_ashrrev_i32_e32 v5, 31, v4
	v_lshl_add_u64 v[6:7], v[4:5], 2, s[8:9]
	global_load_dword v24, v[6:7], off
	v_lshlrev_b64 v[22:23], 11, v[4:5]
	ds_read2_b32 v[6:7], v77 offset0:16 offset1:49
	ds_read2_b32 v[8:9], v77 offset0:82 offset1:115
	ds_read2_b32 v[10:11], v77 offset0:148 offset1:181
	ds_read2_b32 v[12:13], v77 offset0:214 offset1:247
	ds_read2_b32 v[14:15], v109 offset0:24 offset1:57
	ds_read2_b32 v[16:17], v109 offset0:90 offset1:123
	ds_read2_b32 v[18:19], v109 offset0:156 offset1:189
	ds_read2_b32 v[20:21], v109 offset0:222 offset1:255
	s_waitcnt vmcnt(0)
	v_div_scale_f32 v25, s[30:31], v24, v24, 1.0
	v_rcp_f32_e32 v26, v25
	v_div_scale_f32 v4, vcc, 1.0, v24, 1.0
	v_fma_f32 v5, -v25, v26, 1.0
	v_fmac_f32_e32 v26, v5, v26
	v_mul_f32_e32 v5, v4, v26
	v_fma_f32 v27, -v25, v5, v4
	v_fmac_f32_e32 v5, v27, v26
	v_fma_f32 v4, -v25, v5, v4
	v_div_fmas_f32 v4, v4, v26, v5
	v_div_fixup_f32 v4, v4, v24, 1.0
	s_waitcnt lgkmcnt(7)
	v_fmaak_f32 v5, v6, v4, 0x43000000
	v_fmaak_f32 v6, v4, v7, 0x43000000
	s_waitcnt lgkmcnt(6)
	v_fmaak_f32 v7, v4, v8, 0x43000000
	v_fmaak_f32 v8, v4, v9, 0x43000000
	s_waitcnt lgkmcnt(5)
	v_fmaak_f32 v9, v4, v10, 0x43000000
	v_fmaak_f32 v10, v4, v11, 0x43000000
	s_waitcnt lgkmcnt(4)
	v_fmaak_f32 v11, v4, v12, 0x43000000
	v_fmaak_f32 v12, v4, v13, 0x43000000
	s_waitcnt lgkmcnt(3)
	v_fmaak_f32 v13, v4, v14, 0x43000000
	v_fmaak_f32 v14, v4, v15, 0x43000000
	s_waitcnt lgkmcnt(2)
	v_fmaak_f32 v15, v4, v16, 0x43000000
	v_fmaak_f32 v16, v4, v17, 0x43000000
	s_waitcnt lgkmcnt(1)
	v_fmaak_f32 v17, v4, v18, 0x43000000
	v_fmaak_f32 v18, v4, v19, 0x43000000
	v_rndne_f32_e32 v5, v5
	v_rndne_f32_e32 v9, v9
	v_rndne_f32_e32 v13, v13
	v_rndne_f32_e32 v17, v17
	s_waitcnt lgkmcnt(0)
	v_fmaak_f32 v19, v4, v20, 0x43000000
	v_rndne_f32_e32 v6, v6
	v_rndne_f32_e32 v10, v10
	v_rndne_f32_e32 v14, v14
	v_rndne_f32_e32 v18, v18
	v_cvt_pk_u8_f32 v5, v5, 0, 0
	v_cvt_pk_u8_f32 v9, v9, 0, 0
	v_cvt_pk_u8_f32 v13, v13, 0, 0
	v_cvt_pk_u8_f32 v17, v17, 0, 0
	v_fmaak_f32 v4, v4, v21, 0x43000000
	v_rndne_f32_e32 v7, v7
	v_rndne_f32_e32 v11, v11
	v_rndne_f32_e32 v15, v15
	v_rndne_f32_e32 v19, v19
	v_cvt_pk_u8_f32 v5, v6, 1, v5
	v_cvt_pk_u8_f32 v6, v10, 1, v9
	v_cvt_pk_u8_f32 v9, v14, 1, v13
	v_cvt_pk_u8_f32 v10, v18, 1, v17
	v_rndne_f32_e32 v8, v8
	v_rndne_f32_e32 v12, v12
	v_rndne_f32_e32 v16, v16
	v_rndne_f32_e32 v4, v4
	v_cvt_pk_u8_f32 v5, v7, 2, v5
	v_cvt_pk_u8_f32 v6, v11, 2, v6
	v_cvt_pk_u8_f32 v7, v15, 2, v9
	v_cvt_pk_u8_f32 v9, v19, 2, v10
	v_cvt_pk_u8_f32 v5, v8, 3, v5
	v_cvt_pk_u8_f32 v6, v12, 3, v6
	v_cvt_pk_u8_f32 v7, v16, 3, v7
	v_cvt_pk_u8_f32 v8, v4, 3, v9
	v_xor_b32_e32 v4, 0x80808080, v5
	v_xor_b32_e32 v5, 0x80808080, v6
	v_xor_b32_e32 v6, 0x80808080, v7
	v_xor_b32_e32 v7, 0x80808080, v8
	v_lshl_add_u64 v[8:9], v[2:3], 0, v[22:23]
	global_store_dwordx4 v[8:9], v[4:7], off nt
.LBB0_1294:
	s_or_b64 exec, exec, s[10:11]
	s_nop 0
	v_or_b32_e32 v4, s28, v76
	v_cmp_gt_i32_e32 vcc, s24, v4
	s_and_saveexec_b64 s[10:11], vcc
	s_cbranch_execz .LBB0_1251
	s_lshl_b32 s27, s27, 6
	s_and_b32 s27, s27, 0xffffff00
	v_and_b32_e32 v4, 0x7f, v4
	v_or_b32_e32 v4, s27, v4
	v_or_b32_e32 v5, 0x80, v4
	v_cndmask_b32_e64 v4, v4, v5, s[6:7]
	v_ashrrev_i32_e32 v5, 31, v4
	v_lshl_add_u64 v[6:7], v[4:5], 2, s[8:9]
	global_load_dword v24, v[6:7], off
	v_lshlrev_b64 v[22:23], 11, v[4:5]
	ds_read2_b32 v[6:7], v77 offset0:24 offset1:57
	ds_read2_b32 v[8:9], v77 offset0:90 offset1:123
	ds_read2_b32 v[10:11], v77 offset0:156 offset1:189
	ds_read2_b32 v[12:13], v77 offset0:222 offset1:255
	ds_read2_b32 v[14:15], v109 offset0:32 offset1:65
	ds_read2_b32 v[16:17], v109 offset0:98 offset1:131
	ds_read2_b32 v[18:19], v109 offset0:164 offset1:197
	ds_read2_b32 v[20:21], v111 offset0:102 offset1:135
	v_lshl_add_u64 v[2:3], v[2:3], 0, v[22:23]
	s_waitcnt vmcnt(0)
	v_div_scale_f32 v25, s[6:7], v24, v24, 1.0
	v_rcp_f32_e32 v26, v25
	v_div_scale_f32 v4, vcc, 1.0, v24, 1.0
	v_fma_f32 v5, -v25, v26, 1.0
	v_fmac_f32_e32 v26, v5, v26
	v_mul_f32_e32 v5, v4, v26
	v_fma_f32 v27, -v25, v5, v4
	v_fmac_f32_e32 v5, v27, v26
	v_fma_f32 v4, -v25, v5, v4
	v_div_fmas_f32 v4, v4, v26, v5
	v_div_fixup_f32 v4, v4, v24, 1.0
	s_waitcnt lgkmcnt(7)
	v_fmaak_f32 v5, v6, v4, 0x43000000
	v_fmaak_f32 v6, v4, v7, 0x43000000
	s_waitcnt lgkmcnt(6)
	v_fmaak_f32 v7, v4, v8, 0x43000000
	v_fmaak_f32 v8, v4, v9, 0x43000000
	s_waitcnt lgkmcnt(5)
	v_fmaak_f32 v9, v4, v10, 0x43000000
	v_fmaak_f32 v10, v4, v11, 0x43000000
	s_waitcnt lgkmcnt(4)
	v_fmaak_f32 v11, v4, v12, 0x43000000
	v_fmaak_f32 v12, v4, v13, 0x43000000
	s_waitcnt lgkmcnt(3)
	v_fmaak_f32 v13, v4, v14, 0x43000000
	v_fmaak_f32 v14, v4, v15, 0x43000000
	s_waitcnt lgkmcnt(2)
	v_fmaak_f32 v15, v4, v16, 0x43000000
	v_fmaak_f32 v16, v4, v17, 0x43000000
	s_waitcnt lgkmcnt(1)
	v_fmaak_f32 v17, v4, v18, 0x43000000
	v_fmaak_f32 v18, v4, v19, 0x43000000
	v_rndne_f32_e32 v5, v5
	v_rndne_f32_e32 v9, v9
	v_rndne_f32_e32 v13, v13
	v_rndne_f32_e32 v17, v17
	s_waitcnt lgkmcnt(0)
	v_fmaak_f32 v19, v4, v20, 0x43000000
	v_rndne_f32_e32 v6, v6
	v_rndne_f32_e32 v10, v10
	v_rndne_f32_e32 v14, v14
	v_rndne_f32_e32 v18, v18
	v_cvt_pk_u8_f32 v5, v5, 0, 0
	v_cvt_pk_u8_f32 v9, v9, 0, 0
	v_cvt_pk_u8_f32 v13, v13, 0, 0
	v_cvt_pk_u8_f32 v17, v17, 0, 0
	v_fmaak_f32 v4, v4, v21, 0x43000000
	v_rndne_f32_e32 v7, v7
	v_rndne_f32_e32 v11, v11
	v_rndne_f32_e32 v15, v15
	v_rndne_f32_e32 v19, v19
	v_cvt_pk_u8_f32 v5, v6, 1, v5
	v_cvt_pk_u8_f32 v6, v10, 1, v9
	v_cvt_pk_u8_f32 v9, v14, 1, v13
	v_cvt_pk_u8_f32 v10, v18, 1, v17
	v_rndne_f32_e32 v8, v8
	v_rndne_f32_e32 v12, v12
	v_rndne_f32_e32 v16, v16
	v_rndne_f32_e32 v4, v4
	v_cvt_pk_u8_f32 v5, v7, 2, v5
	v_cvt_pk_u8_f32 v6, v11, 2, v6
	v_cvt_pk_u8_f32 v7, v15, 2, v9
	v_cvt_pk_u8_f32 v9, v19, 2, v10
	v_cvt_pk_u8_f32 v5, v8, 3, v5
	v_cvt_pk_u8_f32 v6, v12, 3, v6
	v_cvt_pk_u8_f32 v7, v16, 3, v7
	v_cvt_pk_u8_f32 v8, v4, 3, v9
	v_xor_b32_e32 v4, 0x80808080, v5
	v_xor_b32_e32 v5, 0x80808080, v6
	v_xor_b32_e32 v6, 0x80808080, v7
	v_xor_b32_e32 v7, 0x80808080, v8
	global_store_dwordx4 v[2:3], v[4:7], off nt
	s_branch .LBB0_1251

.LBB0_2048:
	s_add_i32 s9, s16, s17
	s_mul_hi_i32 s4, s9, 0x3e0f83e1
	s_lshr_b32 s5, s4, 31
	s_ashr_i32 s4, s4, 11
	s_add_i32 s8, s4, s5
	s_mul_i32 s4, s8, 0xffffdf00
	s_add_i32 s26, s9, s4
	s_mul_hi_i32 s5, s8, 0xb00000
	s_mul_i32 s4, s8, 0xb00000
	s_cmpk_gt_i32 s26, 0x15ff
	s_mov_b64 s[6:7], -1
	s_cbranch_scc0 .LBB0_2050
	s_add_u32 s7, s10, s4
	s_addc_u32 s27, s11, s5
	s_mul_i32 s28, s8, 0x2c00000
	s_mul_hi_i32 s6, s8, 0x2c00000
	s_waitcnt lgkmcnt(0)
	s_add_u32 s30, s0, s28
	s_addc_u32 s31, s1, s6
	s_mul_i32 s6, s8, 0xffffbe00
	s_add_i32 s6, s20, s6
	s_and_b32 s28, s6, 0xffffff80
	s_addk_i32 s28, 0xd400
	s_and_b32 s6, s18, 0x7e0
	v_or_b32_e32 v62, s28, v73
	v_or_b32_e32 v2, s6, v72
	v_or_b32_e32 v4, 8, v62
	v_lshlrev_b32_e32 v68, 2, v2
	v_ashrrev_i32_e32 v63, 31, v62
	v_ashrrev_i32_e32 v5, 31, v4
	v_lshl_add_u64 v[64:65], s[30:31], 0, v[68:69]
	v_lshlrev_b64 v[2:3], 13, v[62:63]
	v_lshlrev_b64 v[4:5], 13, v[4:5]
	v_lshl_add_u64 v[2:3], v[64:65], 0, v[2:3]
	v_lshl_add_u64 v[6:7], v[64:65], 0, v[4:5]
	global_load_dwordx4 v[2:5], v[2:3], off nt
	s_nop 0
	global_load_dwordx4 v[6:9], v[6:7], off nt
	v_or_b32_e32 v10, 16, v62
	v_or_b32_e32 v12, 24, v62
	v_ashrrev_i32_e32 v11, 31, v10
	v_ashrrev_i32_e32 v13, 31, v12
	v_lshlrev_b64 v[10:11], 13, v[10:11]
	v_lshlrev_b64 v[12:13], 13, v[12:13]
	v_lshl_add_u64 v[10:11], v[64:65], 0, v[10:11]
	v_lshl_add_u64 v[14:15], v[64:65], 0, v[12:13]
	global_load_dwordx4 v[10:13], v[10:11], off nt
	s_nop 0
	global_load_dwordx4 v[14:17], v[14:15], off nt
	v_or_b32_e32 v18, 32, v62
	v_or_b32_e32 v20, 40, v62
	v_ashrrev_i32_e32 v19, 31, v18
	v_ashrrev_i32_e32 v21, 31, v20
	v_lshlrev_b64 v[18:19], 13, v[18:19]
	v_lshlrev_b64 v[20:21], 13, v[20:21]
	v_lshl_add_u64 v[18:19], v[64:65], 0, v[18:19]
	v_lshl_add_u64 v[22:23], v[64:65], 0, v[20:21]
	global_load_dwordx4 v[18:21], v[18:19], off nt
	s_nop 0
	global_load_dwordx4 v[22:25], v[22:23], off nt
	v_or_b32_e32 v26, 48, v62
	v_or_b32_e32 v28, 56, v62
	v_ashrrev_i32_e32 v27, 31, v26
	v_ashrrev_i32_e32 v29, 31, v28
	v_lshlrev_b64 v[26:27], 13, v[26:27]
	v_lshlrev_b64 v[28:29], 13, v[28:29]
	v_lshl_add_u64 v[26:27], v[64:65], 0, v[26:27]
	v_lshl_add_u64 v[30:31], v[64:65], 0, v[28:29]
	global_load_dwordx4 v[26:29], v[26:27], off nt
	s_nop 0
	global_load_dwordx4 v[30:33], v[30:31], off nt
	v_or_b32_e32 v34, 64, v62
	v_or_b32_e32 v36, 0x48, v62
	v_ashrrev_i32_e32 v35, 31, v34
	v_ashrrev_i32_e32 v37, 31, v36
	v_lshlrev_b64 v[34:35], 13, v[34:35]
	v_lshlrev_b64 v[36:37], 13, v[36:37]
	v_lshl_add_u64 v[34:35], v[64:65], 0, v[34:35]
	v_lshl_add_u64 v[38:39], v[64:65], 0, v[36:37]
	global_load_dwordx4 v[34:37], v[34:35], off nt
	s_nop 0
	global_load_dwordx4 v[38:41], v[38:39], off nt
	v_or_b32_e32 v42, 0x50, v62
	v_or_b32_e32 v44, 0x58, v62
	v_ashrrev_i32_e32 v43, 31, v42
	v_ashrrev_i32_e32 v45, 31, v44
	v_lshlrev_b64 v[42:43], 13, v[42:43]
	v_lshlrev_b64 v[44:45], 13, v[44:45]
	v_lshl_add_u64 v[42:43], v[64:65], 0, v[42:43]
	v_lshl_add_u64 v[46:47], v[64:65], 0, v[44:45]
	v_or_b32_e32 v50, 0x60, v62
	global_load_dwordx4 v[42:45], v[42:43], off nt
	s_nop 0
	global_load_dwordx4 v[46:49], v[46:47], off nt
	v_ashrrev_i32_e32 v51, 31, v50
	v_lshlrev_b64 v[50:51], 13, v[50:51]
	v_or_b32_e32 v54, 0x68, v62
	v_lshl_add_u64 v[50:51], v[64:65], 0, v[50:51]
	v_ashrrev_i32_e32 v55, 31, v54
	global_load_dwordx4 v[50:53], v[50:51], off nt
	v_lshlrev_b64 v[54:55], 13, v[54:55]
	v_or_b32_e32 v58, 0x70, v62
	v_lshl_add_u64 v[54:55], v[64:65], 0, v[54:55]
	v_ashrrev_i32_e32 v59, 31, v58
	global_load_dwordx4 v[54:57], v[54:55], off nt
	v_lshlrev_b64 v[58:59], 13, v[58:59]
	v_or_b32_e32 v62, 0x78, v62
	v_lshl_add_u64 v[58:59], v[64:65], 0, v[58:59]
	v_ashrrev_i32_e32 v63, 31, v62
	global_load_dwordx4 v[58:61], v[58:59], off nt
	v_lshlrev_b64 v[62:63], 13, v[62:63]
	v_lshl_add_u64 v[62:63], v[64:65], 0, v[62:63]
	global_load_dwordx4 v[62:65], v[62:63], off nt
	s_add_u32 s28, s7, s28
	s_addc_u32 s29, s27, 0
	s_waitcnt vmcnt(15)
	v_pk_mul_f32 v[2:3], v[2:3], s[2:3] op_sel_hi:[1,0]
	ds_write2_b32 v78, v2, v3 offset1:1
	v_pk_mul_f32 v[2:3], v[4:5], s[2:3] op_sel_hi:[1,0]
	ds_write2_b32 v78, v2, v3 offset0:2 offset1:3
	s_waitcnt vmcnt(14)
	v_pk_mul_f32 v[2:3], v[6:7], s[2:3] op_sel_hi:[1,0]
	ds_write2_b32 v79, v2, v3 offset1:1
	v_pk_mul_f32 v[2:3], v[8:9], s[2:3] op_sel_hi:[1,0]
	ds_write2_b32 v80, v2, v3 offset1:1
	v_mov_b32_e32 v5, v69
	s_waitcnt vmcnt(13)
	v_pk_mul_f32 v[2:3], v[10:11], s[2:3] op_sel_hi:[1,0]
	ds_write2_b32 v81, v2, v3 offset1:1
	v_pk_mul_f32 v[2:3], v[12:13], s[2:3] op_sel_hi:[1,0]
	ds_write2_b32 v82, v2, v3 offset1:1
	s_waitcnt vmcnt(12)
	v_pk_mul_f32 v[2:3], v[14:15], s[2:3] op_sel_hi:[1,0]
	ds_write2_b32 v83, v2, v3 offset1:1
	v_pk_mul_f32 v[2:3], v[16:17], s[2:3] op_sel_hi:[1,0]
	ds_write2_b32 v84, v2, v3 offset1:1
	v_lshl_add_u64 v[14:15], s[28:29], 0, v[66:67]
	s_waitcnt vmcnt(11)
	v_pk_mul_f32 v[2:3], v[18:19], s[2:3] op_sel_hi:[1,0]
	ds_write2_b32 v85, v2, v3 offset1:1
	v_pk_mul_f32 v[2:3], v[20:21], s[2:3] op_sel_hi:[1,0]
	ds_write2_b32 v86, v2, v3 offset1:1
	s_waitcnt vmcnt(10)
	v_pk_mul_f32 v[2:3], v[22:23], s[2:3] op_sel_hi:[1,0]
	ds_write2_b32 v87, v2, v3 offset1:1
	v_pk_mul_f32 v[2:3], v[24:25], s[2:3] op_sel_hi:[1,0]
	ds_write2_b32 v88, v2, v3 offset1:1
	s_waitcnt vmcnt(9)
	v_pk_mul_f32 v[2:3], v[26:27], s[2:3] op_sel_hi:[1,0]
	ds_write2_b32 v89, v2, v3 offset1:1
	v_pk_mul_f32 v[2:3], v[28:29], s[2:3] op_sel_hi:[1,0]
	ds_write2_b32 v90, v2, v3 offset1:1
	s_waitcnt vmcnt(8)
	v_pk_mul_f32 v[2:3], v[30:31], s[2:3] op_sel_hi:[1,0]
	ds_write2_b32 v91, v2, v3 offset1:1
	v_pk_mul_f32 v[2:3], v[32:33], s[2:3] op_sel_hi:[1,0]
	ds_write2_b32 v92, v2, v3 offset1:1
	s_waitcnt vmcnt(7)
	v_pk_mul_f32 v[2:3], v[34:35], s[2:3] op_sel_hi:[1,0]
	ds_write2_b32 v93, v2, v3 offset1:1
	v_pk_mul_f32 v[2:3], v[36:37], s[2:3] op_sel_hi:[1,0]
	ds_write2_b32 v94, v2, v3 offset1:1
	s_waitcnt vmcnt(6)
	v_pk_mul_f32 v[2:3], v[38:39], s[2:3] op_sel_hi:[1,0]
	ds_write2_b32 v95, v2, v3 offset1:1
	v_pk_mul_f32 v[2:3], v[40:41], s[2:3] op_sel_hi:[1,0]
	ds_write2_b32 v96, v2, v3 offset1:1
	s_waitcnt vmcnt(5)
	v_pk_mul_f32 v[2:3], v[42:43], s[2:3] op_sel_hi:[1,0]
	ds_write2_b32 v97, v2, v3 offset1:1
	v_pk_mul_f32 v[2:3], v[44:45], s[2:3] op_sel_hi:[1,0]
	ds_write2_b32 v98, v2, v3 offset1:1
	s_waitcnt vmcnt(4)
	v_pk_mul_f32 v[2:3], v[46:47], s[2:3] op_sel_hi:[1,0]
	ds_write2_b32 v99, v2, v3 offset1:1
	v_pk_mul_f32 v[2:3], v[48:49], s[2:3] op_sel_hi:[1,0]
	ds_write2_b32 v100, v2, v3 offset1:1
	s_waitcnt vmcnt(3)
	v_pk_mul_f32 v[2:3], v[50:51], s[2:3] op_sel_hi:[1,0]
	ds_write2_b32 v101, v2, v3 offset1:1
	v_pk_mul_f32 v[2:3], v[52:53], s[2:3] op_sel_hi:[1,0]
	ds_write2_b32 v102, v2, v3 offset1:1
	s_waitcnt vmcnt(2)
	v_pk_mul_f32 v[2:3], v[54:55], s[2:3] op_sel_hi:[1,0]
	ds_write2_b32 v103, v2, v3 offset1:1
	v_pk_mul_f32 v[2:3], v[56:57], s[2:3] op_sel_hi:[1,0]
	ds_write2_b32 v104, v2, v3 offset1:1
	s_waitcnt vmcnt(1)
	v_pk_mul_f32 v[2:3], v[58:59], s[2:3] op_sel_hi:[1,0]
	ds_write2_b32 v105, v2, v3 offset1:1
	v_pk_mul_f32 v[2:3], v[60:61], s[2:3] op_sel_hi:[1,0]
	ds_write2_b32 v106, v2, v3 offset1:1
	s_waitcnt vmcnt(0)
	v_pk_mul_f32 v[2:3], v[62:63], s[2:3] op_sel_hi:[1,0]
	ds_write2_b32 v107, v2, v3 offset1:1
	v_pk_mul_f32 v[2:3], v[64:65], s[2:3] op_sel_hi:[1,0]
	ds_write2_b32 v108, v2, v3 offset1:1
	s_waitcnt lgkmcnt(0)
	ds_read2_b32 v[6:7], v109 offset0:206 offset1:214
	ds_read2_b32 v[8:9], v109 offset0:239 offset1:247
	ds_read2_b32 v[10:11], v109 offset0:140 offset1:148
	ds_read2_b32 v[12:13], v109 offset0:173 offset1:181
	ds_read2_b32 v[16:17], v109 offset0:74 offset1:82
	ds_read2_b32 v[18:19], v109 offset0:107 offset1:115
	ds_read2_b32 v[20:21], v109 offset0:8 offset1:16
	ds_read2_b32 v[22:23], v109 offset0:41 offset1:49
	s_waitcnt lgkmcnt(7)
	v_med3_f32 v2, v6, s22, v110
	s_waitcnt lgkmcnt(6)
	v_med3_f32 v3, v8, s22, v110
	s_waitcnt lgkmcnt(5)
	v_med3_f32 v4, v10, s22, v110
	s_waitcnt lgkmcnt(4)
	v_med3_f32 v6, v12, s22, v110
	v_cvt_pk_fp8_f32 v5, v4, v6
	s_waitcnt lgkmcnt(1)
	v_med3_f32 v6, v20, s22, v110
	s_waitcnt lgkmcnt(0)
	v_med3_f32 v8, v22, s22, v110
	v_mov_b32_e32 v4, v69
	ds_read2_b32 v[24:25], v77 offset0:198 offset1:206
	ds_read2_b32 v[26:27], v77 offset0:231 offset1:239
	ds_read2_b32 v[28:29], v77 offset0:132 offset1:140
	ds_read2_b32 v[30:31], v77 offset0:165 offset1:173
	v_cvt_pk_fp8_f32 v4, v6, v8
	ds_read2_b32 v[32:33], v77 offset1:8
	ds_read2_b32 v[34:35], v77 offset0:33 offset1:41
	v_cvt_pk_fp8_f32 v5, v2, v3 op_sel:[0,0,1]
	v_med3_f32 v2, v16, s22, v110
	v_med3_f32 v3, v18, s22, v110
	v_cvt_pk_fp8_f32 v4, v2, v3 op_sel:[0,0,1]
	s_waitcnt lgkmcnt(3)
	v_med3_f32 v2, v28, s22, v110
	s_waitcnt lgkmcnt(2)
	v_med3_f32 v10, v30, s22, v110
	v_mov_b32_e32 v3, v69
	ds_read2_b32 v[36:37], v77 offset0:66 offset1:74
	ds_read2_b32 v[38:39], v77 offset0:99 offset1:107
	v_cvt_pk_fp8_f32 v3, v2, v10
	s_waitcnt lgkmcnt(3)
	v_med3_f32 v10, v32, s22, v110
	s_waitcnt lgkmcnt(2)
	v_med3_f32 v12, v34, s22, v110
	v_mov_b32_e32 v2, v69
	v_cvt_pk_fp8_f32 v2, v10, v12
	v_med3_f32 v6, v24, s22, v110
	v_med3_f32 v8, v26, s22, v110
	v_cvt_pk_fp8_f32 v3, v6, v8 op_sel:[0,0,1]
	s_waitcnt lgkmcnt(1)
	v_med3_f32 v6, v36, s22, v110
	s_waitcnt lgkmcnt(0)
	v_med3_f32 v8, v38, s22, v110
	v_cvt_pk_fp8_f32 v2, v6, v8 op_sel:[0,0,1]
	v_or_b32_e32 v6, s6, v73
	v_mul_u32_u24_e32 v68, 0x1600, v6
	v_lshl_add_u64 v[40:41], v[14:15], 0, v[68:69]
	global_store_dwordx4 v[40:41], v[2:5], off nt
	v_med3_f32 v8, v23, s22, v110
	v_med3_f32 v10, v35, s22, v110
	v_med3_f32 v2, v7, s22, v110
	v_med3_f32 v4, v11, s22, v110
	v_med3_f32 v7, v13, s22, v110
	v_mov_b32_e32 v5, v69
	v_cvt_pk_fp8_f32 v5, v4, v7
	v_med3_f32 v7, v21, s22, v110
	v_mov_b32_e32 v4, v69
	v_cvt_pk_fp8_f32 v4, v7, v8
	v_med3_f32 v3, v9, s22, v110
	v_cvt_pk_fp8_f32 v5, v2, v3 op_sel:[0,0,1]
	v_med3_f32 v2, v17, s22, v110
	v_med3_f32 v3, v19, s22, v110
	v_cvt_pk_fp8_f32 v4, v2, v3 op_sel:[0,0,1]
	v_med3_f32 v2, v29, s22, v110
	v_med3_f32 v9, v31, s22, v110
	v_mov_b32_e32 v3, v69
	v_cvt_pk_fp8_f32 v3, v2, v9
	v_med3_f32 v9, v33, s22, v110
	v_mov_b32_e32 v2, v69
	v_cvt_pk_fp8_f32 v2, v9, v10
	v_med3_f32 v7, v25, s22, v110
	v_med3_f32 v8, v27, s22, v110
	v_cvt_pk_fp8_f32 v3, v7, v8 op_sel:[0,0,1]
	v_med3_f32 v7, v37, s22, v110
	v_med3_f32 v8, v39, s22, v110
	v_cvt_pk_fp8_f32 v2, v7, v8 op_sel:[0,0,1]
	ds_read2_b32 v[8:9], v109 offset0:222 offset1:230
	ds_read2_b32 v[10:11], v111 offset0:127 offset1:135
	ds_read2_b32 v[12:13], v109 offset0:156 offset1:164
	ds_read2_b32 v[16:17], v109 offset0:189 offset1:197
	v_or_b32_e32 v6, s6, v74
	v_mul_u32_u24_e32 v68, 0x1600, v6
	v_lshl_add_u64 v[6:7], v[14:15], 0, v[68:69]
	global_store_dwordx4 v[6:7], v[2:5], off nt
	s_waitcnt lgkmcnt(0)
	v_med3_f32 v6, v16, s22, v110
	v_med3_f32 v4, v12, s22, v110
	v_mov_b32_e32 v5, v69
	v_cvt_pk_fp8_f32 v5, v4, v6
	ds_read2_b32 v[6:7], v109 offset0:90 offset1:98
	ds_read2_b32 v[18:19], v109 offset0:123 offset1:131
	ds_read2_b32 v[20:21], v109 offset0:24 offset1:32
	ds_read2_b32 v[22:23], v109 offset0:57 offset1:65
	v_med3_f32 v2, v8, s22, v110
	v_med3_f32 v3, v10, s22, v110
	v_cvt_pk_fp8_f32 v5, v2, v3 op_sel:[0,0,1]
	s_waitcnt lgkmcnt(3)
	v_med3_f32 v2, v6, s22, v110
	s_waitcnt lgkmcnt(1)
	v_med3_f32 v6, v20, s22, v110
	s_waitcnt lgkmcnt(0)
	v_med3_f32 v8, v22, s22, v110
	v_mov_b32_e32 v4, v69
	ds_read2_b32 v[24:25], v77 offset0:214 offset1:222
	ds_read2_b32 v[26:27], v77 offset0:247 offset1:255
	ds_read2_b32 v[28:29], v77 offset0:148 offset1:156
	ds_read2_b32 v[30:31], v77 offset0:181 offset1:189
	v_cvt_pk_fp8_f32 v4, v6, v8
	ds_read2_b32 v[32:33], v77 offset0:16 offset1:24
	ds_read2_b32 v[34:35], v77 offset0:49 offset1:57
	v_med3_f32 v3, v18, s22, v110
	ds_read2_b32 v[36:37], v77 offset0:82 offset1:90
	ds_read2_b32 v[38:39], v77 offset0:115 offset1:123
	v_cvt_pk_fp8_f32 v4, v2, v3 op_sel:[0,0,1]
	s_waitcnt lgkmcnt(5)
	v_med3_f32 v2, v28, s22, v110
	s_waitcnt lgkmcnt(4)
	v_med3_f32 v10, v30, s22, v110
	v_mov_b32_e32 v3, v69
	v_cvt_pk_fp8_f32 v3, v2, v10
	s_waitcnt lgkmcnt(3)
	v_med3_f32 v10, v32, s22, v110
	s_waitcnt lgkmcnt(2)
	v_med3_f32 v12, v34, s22, v110
	v_mov_b32_e32 v2, v69
	v_cvt_pk_fp8_f32 v2, v10, v12
	v_med3_f32 v6, v24, s22, v110
	v_med3_f32 v8, v26, s22, v110
	v_cvt_pk_fp8_f32 v3, v6, v8 op_sel:[0,0,1]
	s_waitcnt lgkmcnt(1)
	v_med3_f32 v6, v36, s22, v110
	s_waitcnt lgkmcnt(0)
	v_med3_f32 v8, v38, s22, v110
	v_cvt_pk_fp8_f32 v2, v6, v8 op_sel:[0,0,1]
	v_or_b32_e32 v6, s6, v75
	v_mul_u32_u24_e32 v68, 0x1600, v6
	v_lshl_add_u64 v[40:41], v[14:15], 0, v[68:69]
	global_store_dwordx4 v[40:41], v[2:5], off nt
	v_med3_f32 v6, v17, s22, v110
	v_med3_f32 v8, v23, s22, v110
	v_med3_f32 v4, v13, s22, v110
	v_mov_b32_e32 v5, v69
	v_cvt_pk_fp8_f32 v5, v4, v6
	v_med3_f32 v6, v21, s22, v110
	v_mov_b32_e32 v4, v69
	v_cvt_pk_fp8_f32 v4, v6, v8
	v_med3_f32 v2, v9, s22, v110
	v_med3_f32 v3, v11, s22, v110
	v_cvt_pk_fp8_f32 v5, v2, v3 op_sel:[0,0,1]
	v_med3_f32 v2, v7, s22, v110
	v_med3_f32 v3, v19, s22, v110
	v_cvt_pk_fp8_f32 v4, v2, v3 op_sel:[0,0,1]
	v_med3_f32 v2, v29, s22, v110
	v_med3_f32 v8, v31, s22, v110
	v_mov_b32_e32 v3, v69
	v_cvt_pk_fp8_f32 v3, v2, v8
	v_med3_f32 v8, v33, s22, v110
	v_med3_f32 v9, v35, s22, v110
	v_mov_b32_e32 v2, v69
	v_cvt_pk_fp8_f32 v2, v8, v9
	v_med3_f32 v6, v25, s22, v110
	v_med3_f32 v7, v27, s22, v110
	v_cvt_pk_fp8_f32 v3, v6, v7 op_sel:[0,0,1]
	v_med3_f32 v6, v37, s22, v110
	v_med3_f32 v7, v39, s22, v110
	v_cvt_pk_fp8_f32 v2, v6, v7 op_sel:[0,0,1]
	v_or_b32_e32 v6, s6, v76
	v_mul_u32_u24_e32 v68, 0x1600, v6
	v_lshl_add_u64 v[6:7], v[14:15], 0, v[68:69]
	global_store_dwordx4 v[6:7], v[2:5], off nt
	s_waitcnt lgkmcnt(0)
	s_mov_b64 s[6:7], 0

.LBB0_2083:
	s_or_b64 exec, exec, s[4:5]
	s_mul_i32 s5, s8, 0x1600000
	s_mul_hi_i32 s4, s8, 0x1600000
	s_add_u32 s28, s12, s5
	s_addc_u32 s29, s13, s4
	s_mul_i32 s4, s8, 0x2c00
	s_ashr_i32 s5, s4, 31
	s_lshl_b64 s[4:5], s[4:5], 2
	s_add_u32 s4, s14, s4
	s_waitcnt vmcnt(0)
	ds_write2_b32 v78, v6, v7 offset1:1
	ds_write2_b32 v78, v8, v9 offset0:2 offset1:3
	ds_write2_b32 v79, v2, v3 offset1:1
	ds_write2_b32 v80, v4, v5 offset1:1
	ds_write2_b32 v81, v14, v15 offset1:1
	ds_write2_b32 v82, v16, v17 offset1:1
	ds_write2_b32 v83, v10, v11 offset1:1
	ds_write2_b32 v84, v12, v13 offset1:1
	ds_write2_b32 v85, v22, v23 offset1:1
	ds_write2_b32 v86, v24, v25 offset1:1
	ds_write2_b32 v87, v18, v19 offset1:1
	ds_write2_b32 v88, v20, v21 offset1:1
	ds_write2_b32 v89, v30, v31 offset1:1
	ds_write2_b32 v90, v32, v33 offset1:1
	ds_write2_b32 v91, v26, v27 offset1:1
	ds_write2_b32 v92, v28, v29 offset1:1
	ds_write2_b32 v93, v38, v39 offset1:1
	ds_write2_b32 v94, v40, v41 offset1:1
	ds_write2_b32 v95, v34, v35 offset1:1
	ds_write2_b32 v96, v36, v37 offset1:1
	ds_write2_b32 v97, v46, v47 offset1:1
	ds_write2_b32 v98, v48, v49 offset1:1
	ds_write2_b32 v99, v42, v43 offset1:1
	ds_write2_b32 v100, v44, v45 offset1:1
	ds_write2_b32 v101, v54, v55 offset1:1
	ds_write2_b32 v102, v56, v57 offset1:1
	ds_write2_b32 v103, v50, v51 offset1:1
	ds_write2_b32 v104, v52, v53 offset1:1
	ds_write2_b32 v105, v62, v63 offset1:1
	ds_write2_b32 v106, v64, v65 offset1:1
	ds_write2_b32 v107, v58, v59 offset1:1
	ds_write2_b32 v108, v60, v61 offset1:1
	s_addc_u32 s5, s15, s5
	s_waitcnt lgkmcnt(0)
	s_ashr_i32 s30, s9, 31
	s_add_u32 s8, s28, s9
	s_addc_u32 s9, s29, s30
	v_or_b32_e32 v4, s27, v73
	v_lshl_add_u64 v[2:3], s[8:9], 0, v[66:67]
	v_cmp_gt_i32_e32 vcc, s23, v4
	s_and_saveexec_b64 s[8:9], vcc
	s_cbranch_execz .LBB0_2085
	s_lshl_b32 s28, s26, 6
	s_and_b32 s28, s28, 0xffffff00
	v_and_b32_e32 v4, 0x67, v4
	v_or_b32_e32 v4, s28, v4
	v_or_b32_e32 v5, 0x80, v4
	v_cndmask_b32_e64 v4, v4, v5, s[6:7]
	v_ashrrev_i32_e32 v5, 31, v4
	v_lshl_add_u64 v[6:7], v[4:5], 2, s[4:5]
	global_load_dword v24, v[6:7], off
	v_lshlrev_b64 v[22:23], 11, v[4:5]
	ds_read2_b32 v[6:7], v77 offset1:33
	ds_read2_b32 v[8:9], v77 offset0:66 offset1:99
	ds_read2_b32 v[10:11], v77 offset0:132 offset1:165
	ds_read2_b32 v[12:13], v77 offset0:198 offset1:231
	ds_read2_b32 v[14:15], v109 offset0:8 offset1:41
	ds_read2_b32 v[16:17], v109 offset0:74 offset1:107
	ds_read2_b32 v[18:19], v109 offset0:140 offset1:173
	ds_read2_b32 v[20:21], v109 offset0:206 offset1:239
	s_waitcnt vmcnt(0)
	v_div_scale_f32 v25, s[28:29], v24, v24, 1.0
	v_rcp_f32_e32 v26, v25
	v_div_scale_f32 v4, vcc, 1.0, v24, 1.0
	v_fma_f32 v5, -v25, v26, 1.0
	v_fmac_f32_e32 v26, v5, v26
	v_mul_f32_e32 v5, v4, v26
	v_fma_f32 v27, -v25, v5, v4
	v_fmac_f32_e32 v5, v27, v26
	v_fma_f32 v4, -v25, v5, v4
	v_div_fmas_f32 v4, v4, v26, v5
	v_div_fixup_f32 v4, v4, v24, 1.0
	s_waitcnt lgkmcnt(7)
	v_fmaak_f32 v5, v6, v4, 0x43000000
	v_fmaak_f32 v6, v4, v7, 0x43000000
	s_waitcnt lgkmcnt(6)
	v_fmaak_f32 v7, v4, v8, 0x43000000
	v_fmaak_f32 v8, v4, v9, 0x43000000
	s_waitcnt lgkmcnt(5)
	v_fmaak_f32 v9, v4, v10, 0x43000000
	v_fmaak_f32 v10, v4, v11, 0x43000000
	s_waitcnt lgkmcnt(4)
	v_fmaak_f32 v11, v4, v12, 0x43000000
	v_fmaak_f32 v12, v4, v13, 0x43000000
	s_waitcnt lgkmcnt(3)
	v_fmaak_f32 v13, v4, v14, 0x43000000
	v_fmaak_f32 v14, v4, v15, 0x43000000
	s_waitcnt lgkmcnt(2)
	v_fmaak_f32 v15, v4, v16, 0x43000000
	v_fmaak_f32 v16, v4, v17, 0x43000000
	s_waitcnt lgkmcnt(1)
	v_fmaak_f32 v17, v4, v18, 0x43000000
	v_fmaak_f32 v18, v4, v19, 0x43000000
	v_rndne_f32_e32 v5, v5
	v_rndne_f32_e32 v9, v9
	v_rndne_f32_e32 v13, v13
	v_rndne_f32_e32 v17, v17
	s_waitcnt lgkmcnt(0)
	v_fmaak_f32 v19, v4, v20, 0x43000000
	v_rndne_f32_e32 v6, v6
	v_rndne_f32_e32 v10, v10
	v_rndne_f32_e32 v14, v14
	v_rndne_f32_e32 v18, v18
	v_cvt_pk_u8_f32 v5, v5, 0, 0
	v_cvt_pk_u8_f32 v9, v9, 0, 0
	v_cvt_pk_u8_f32 v13, v13, 0, 0
	v_cvt_pk_u8_f32 v17, v17, 0, 0
	v_fmaak_f32 v4, v4, v21, 0x43000000
	v_rndne_f32_e32 v7, v7
	v_rndne_f32_e32 v11, v11
	v_rndne_f32_e32 v15, v15
	v_rndne_f32_e32 v19, v19
	v_cvt_pk_u8_f32 v5, v6, 1, v5
	v_cvt_pk_u8_f32 v6, v10, 1, v9
	v_cvt_pk_u8_f32 v9, v14, 1, v13
	v_cvt_pk_u8_f32 v10, v18, 1, v17
	v_rndne_f32_e32 v8, v8
	v_rndne_f32_e32 v12, v12
	v_rndne_f32_e32 v16, v16
	v_rndne_f32_e32 v4, v4
	v_cvt_pk_u8_f32 v5, v7, 2, v5
	v_cvt_pk_u8_f32 v6, v11, 2, v6
	v_cvt_pk_u8_f32 v7, v15, 2, v9
	v_cvt_pk_u8_f32 v9, v19, 2, v10
	v_cvt_pk_u8_f32 v5, v8, 3, v5
	v_cvt_pk_u8_f32 v6, v12, 3, v6
	v_cvt_pk_u8_f32 v7, v16, 3, v7
	v_cvt_pk_u8_f32 v8, v4, 3, v9
	v_xor_b32_e32 v4, 0x80808080, v5
	v_xor_b32_e32 v5, 0x80808080, v6
	v_xor_b32_e32 v6, 0x80808080, v7
	v_xor_b32_e32 v7, 0x80808080, v8
	v_lshl_add_u64 v[8:9], v[2:3], 0, v[22:23]
	global_store_dwordx4 v[8:9], v[4:7], off nt
